# speedup vs baseline: 1.0598x; 1.0119x over previous
.LBB3_32:
	s_or_b64 exec, exec, s[8:9]
	v_bfe_u32 v158, v0, 6, 1
	v_lshrrev_b32_e32 v5, 1, v0
	v_and_b32_e32 v8, 31, v0
	v_lshlrev_b32_e32 v157, 6, v158
	v_and_b32_e32 v5, 0xc0, v5
	v_or_b32_e32 v9, v157, v8
	v_lshrrev_b32_e32 v7, 5, v0
	v_bfe_u32 v150, v0, 5, 1
	v_or_b32_e32 v149, v5, v8
	v_bfe_u32 v10, v0, 2, 2
	v_lshlrev_b32_e32 v9, 2, v9
	v_add_u32_e32 v14, 1, v8
	v_add_u32_e32 v8, 2, v8
	v_bitop3_b32 v7, v7, v10, 1 bitop3:0x6c
	v_bitop3_b32 v12, v150, v10, 2 bitop3:0x36
	v_or_b32_e32 v15, v14, v5
	v_or_b32_e32 v16, v8, v5
	v_or_b32_e32 v5, 0x400, v9
	v_or_b32_e32 v151, 2, v150
	v_or_b32_e32 v17, v5, v7
	v_or_b32_e32 v18, v5, v12
	v_or_b32_e32 v5, 0x480, v9
	v_bitop3_b32 v11, v9, v150, v10 bitop3:0xf6
	v_bitop3_b32 v13, v9, v151, v10 bitop3:0xf6
	v_or_b32_e32 v9, v5, v7
	v_or_b32_e32 v12, v5, v12
	v_lshlrev_b32_e32 v5, 2, v149
	v_bitop3_b32 v184, v150, v5, v10 bitop3:0xde
	v_bitop3_b32 v183, v151, v5, v10 bitop3:0xde
	v_mov_b32_e32 v10, 0x1f700
	v_mov_b32_e32 v5, 0x13700
	v_lshl_add_u32 v182, v3, 4, v10
	v_mov_b32_e32 v3, 0
	v_lshl_add_u32 v165, v11, 4, v5
	v_lshl_add_u32 v166, v13, 4, v5
	v_cmp_lt_i32_e64 s[6:7], -1, v2
	v_lshl_add_u64 v[136:137], v[2:3], 2, s[24:25]
	v_bfe_u32 v2, v14, 2, 2
	v_lshlrev_b32_e32 v5, 2, v15
	v_bitop3_b32 v180, v2, v5, v150 bitop3:0xde
	v_bitop3_b32 v179, v2, v5, v151 bitop3:0xde
	v_bfe_u32 v2, v8, 2, 2
	v_lshlrev_b32_e32 v5, 2, v16
	v_bitop3_b32 v178, v2, v5, v150 bitop3:0xde
	v_bitop3_b32 v177, v2, v5, v151 bitop3:0xde
	v_add_u32_e32 v2, 0xb6, v149
	v_bfe_u32 v5, v2, 2, 2
	v_lshlrev_b32_e32 v2, 2, v2
	v_bitop3_b32 v176, v5, v2, v150 bitop3:0xde
	v_bitop3_b32 v175, v5, v2, v151 bitop3:0xde
	v_add_u32_e32 v2, 0xb6, v15
	v_bfe_u32 v5, v2, 2, 2
	v_lshlrev_b32_e32 v2, 2, v2
	v_bitop3_b32 v174, v5, v2, v150 bitop3:0xde
	v_bitop3_b32 v173, v5, v2, v151 bitop3:0xde
	v_add_u32_e32 v2, 0xb6, v16
	v_bfe_u32 v5, v2, 2, 2
	v_lshlrev_b32_e32 v2, 2, v2
	v_bitop3_b32 v172, v5, v2, v150 bitop3:0xde
	v_bitop3_b32 v171, v5, v2, v151 bitop3:0xde
	v_add_u32_e32 v2, 0x16c, v149
	v_bfe_u32 v5, v2, 2, 2
	v_lshlrev_b32_e32 v2, 2, v2
	v_mov_b32_e32 v7, v3
	v_bitop3_b32 v170, v5, v2, v150 bitop3:0xde
	v_bitop3_b32 v169, v5, v2, v151 bitop3:0xde
	v_add_u32_e32 v2, 0x16c, v15
	v_cmp_lt_i32_e64 s[8:9], -1, v6
	v_lshl_add_u64 v[138:139], v[6:7], 2, s[24:25]
	v_bfe_u32 v6, v2, 2, 2
	v_lshlrev_b32_e32 v2, 2, v2
	s_waitcnt lgkmcnt(0)
	v_bitop3_b32 v168, v6, v2, v150 bitop3:0xde
	v_bitop3_b32 v167, v6, v2, v151 bitop3:0xde
	v_add_u32_e32 v2, 0x16c, v16
	s_add_u32 s12, s12, s27
	v_mov_b32_e32 v5, v3
	v_bfe_u32 v6, v2, 2, 2
	v_lshlrev_b32_e32 v2, 2, v2
	s_addc_u32 s13, s13, s26
	v_add_u32_e32 v181, 0x13700, v142
	v_lshrrev_b32_e32 v148, 2, v0
	v_bitop3_b32 v164, v6, v2, v150 bitop3:0xde
	v_bitop3_b32 v163, v6, v2, v151 bitop3:0xde
	v_lshl_add_u32 v161, v17, 4, v10
	v_lshl_add_u32 v162, v18, 4, v10
	v_lshl_add_u32 v159, v9, 4, v10
	v_lshl_add_u32 v160, v12, 4, v10
	v_lshl_add_u64 v[140:141], v[4:5], 2, s[12:13]
	v_mov_b32_e32 v135, v3
	v_mov_b32_e32 v133, v3
	v_mov_b32_e32 v131, v3
	s_mov_b32 s31, 0
	s_mov_b64 s[40:41], s[12:13]
	s_mov_b64 s[12:13], 0
	s_mov_b32 s30, 0x38800000
	s_mov_b64 s[16:17], 0xc000
	s_mov_b64 s[18:19], 0x12000
	s_mov_b64 s[24:25], 0x18000
	s_xor_b64 s[10:11], s[10:11], -1
	v_mov_b32_e32 v2, v3
	v_mov_b32_e32 v4, v3
	v_mov_b32_e32 v6, v3
	v_mov_b32_e32 v8, v3
	v_mov_b32_e32 v9, v3
	v_mov_b32_e32 v10, v3
	v_mov_b32_e32 v11, v3
	v_mov_b32_e32 v12, v3
	v_mov_b32_e32 v13, v3
	v_mov_b32_e32 v14, v3
	v_mov_b32_e32 v15, v3
	v_mov_b32_e32 v16, v3
	v_mov_b32_e32 v17, v3
	v_mov_b32_e32 v34, v3
	v_mov_b32_e32 v35, v3
	v_mov_b32_e32 v36, v3
	v_mov_b32_e32 v37, v3
	v_mov_b32_e32 v38, v3
	v_mov_b32_e32 v39, v3
	v_mov_b32_e32 v40, v3
	v_mov_b32_e32 v41, v3
	v_mov_b32_e32 v42, v3
	v_mov_b32_e32 v43, v3
	v_mov_b32_e32 v44, v3
	v_mov_b32_e32 v45, v3
	v_mov_b32_e32 v46, v3
	v_mov_b32_e32 v47, v3
	v_mov_b32_e32 v48, v3
	v_mov_b32_e32 v49, v3
	v_mov_b32_e32 v66, v3
	v_mov_b32_e32 v67, v3
	v_mov_b32_e32 v68, v3
	v_mov_b32_e32 v69, v3
	v_mov_b32_e32 v70, v3
	v_mov_b32_e32 v71, v3
	v_mov_b32_e32 v72, v3
	v_mov_b32_e32 v73, v3
	v_mov_b32_e32 v74, v3
	v_mov_b32_e32 v75, v3
	v_mov_b32_e32 v76, v3
	v_mov_b32_e32 v77, v3
	v_mov_b32_e32 v78, v3
	v_mov_b32_e32 v79, v3
	v_mov_b32_e32 v80, v3
	v_mov_b32_e32 v81, v3
	v_mov_b32_e32 v98, v3
	v_mov_b32_e32 v99, v3
	v_mov_b32_e32 v100, v3
	v_mov_b32_e32 v101, v3
	v_mov_b32_e32 v102, v3
	v_mov_b32_e32 v103, v3
	v_mov_b32_e32 v104, v3
	v_mov_b32_e32 v105, v3
	v_mov_b32_e32 v106, v3
	v_mov_b32_e32 v107, v3
	v_mov_b32_e32 v108, v3
	v_mov_b32_e32 v109, v3
	v_mov_b32_e32 v110, v3
	v_mov_b32_e32 v111, v3
	v_mov_b32_e32 v112, v3
	v_mov_b32_e32 v113, v3
	v_mov_b32_e32 v18, v3
	v_mov_b32_e32 v19, v3
	v_mov_b32_e32 v20, v3
	v_mov_b32_e32 v21, v3
	v_mov_b32_e32 v22, v3
	v_mov_b32_e32 v23, v3
	v_mov_b32_e32 v24, v3
	v_mov_b32_e32 v25, v3
	v_mov_b32_e32 v26, v3
	v_mov_b32_e32 v27, v3
	v_mov_b32_e32 v28, v3
	v_mov_b32_e32 v29, v3
	v_mov_b32_e32 v30, v3
	v_mov_b32_e32 v31, v3
	v_mov_b32_e32 v32, v3
	v_mov_b32_e32 v33, v3
	v_mov_b32_e32 v50, v3
	v_mov_b32_e32 v51, v3
	v_mov_b32_e32 v52, v3
	v_mov_b32_e32 v53, v3
	v_mov_b32_e32 v54, v3
	v_mov_b32_e32 v55, v3
	v_mov_b32_e32 v56, v3
	v_mov_b32_e32 v57, v3
	v_mov_b32_e32 v58, v3
	v_mov_b32_e32 v59, v3
	v_mov_b32_e32 v60, v3
	v_mov_b32_e32 v61, v3
	v_mov_b32_e32 v62, v3
	v_mov_b32_e32 v63, v3
	v_mov_b32_e32 v64, v3
	v_mov_b32_e32 v65, v3
	v_mov_b32_e32 v82, v3
	v_mov_b32_e32 v83, v3
	v_mov_b32_e32 v84, v3
	v_mov_b32_e32 v85, v3
	v_mov_b32_e32 v86, v3
	v_mov_b32_e32 v87, v3
	v_mov_b32_e32 v88, v3
	v_mov_b32_e32 v89, v3
	v_mov_b32_e32 v90, v3
	v_mov_b32_e32 v91, v3
	v_mov_b32_e32 v92, v3
	v_mov_b32_e32 v93, v3
	v_mov_b32_e32 v94, v3
	v_mov_b32_e32 v95, v3
	v_mov_b32_e32 v96, v3
	v_mov_b32_e32 v97, v3
	v_mov_b32_e32 v114, v3
	v_mov_b32_e32 v115, v3
	v_mov_b32_e32 v116, v3
	v_mov_b32_e32 v117, v3
	v_mov_b32_e32 v118, v3
	v_mov_b32_e32 v119, v3
	v_mov_b32_e32 v120, v3
	v_mov_b32_e32 v121, v3
	v_mov_b32_e32 v122, v3
	v_mov_b32_e32 v123, v3
	v_mov_b32_e32 v124, v3
	v_mov_b32_e32 v125, v3
	v_mov_b32_e32 v126, v3
	v_mov_b32_e32 v127, v3
	v_mov_b32_e32 v128, v3
	v_mov_b32_e32 v129, v3
	v_subrev_u32_e32 v136, s40, v136
	v_subrev_u32_e32 v138, s40, v138
	v_subrev_u32_e32 v140, s40, v140
	v_readfirstlane_b32 s62, v181
	s_add_u32 s44, s40, 0x1fa400
	s_addc_u32 s45, s41, 0
	s_add_u32 s46, s40, 0x219e40
	s_addc_u32 s47, s41, 0
	s_add_u32 s48, s40, 0x239880
	s_addc_u32 s49, s41, 0
	s_add_u32 s50, s40, 0x2592c0
	s_addc_u32 s51, s41, 0
	s_add_u32 s52, s40, 0x278d00
	s_addc_u32 s53, s41, 0
	s_add_u32 s54, s40, 0x298740
	s_addc_u32 s55, s41, 0
	s_add_u32 s56, s40, 0x2b8180
	s_addc_u32 s57, s41, 0
	s_add_u32 s58, s40, 0x2d7bc0
	s_addc_u32 s59, s41, 0
	s_add_u32 s64, s62, 0xc000
	s_add_u32 s65, s62, 0xe000
	s_add_u32 s66, s62, 0x10000
	s_add_u32 s67, s62, 0x0
	s_add_u32 s68, s62, 0x2000
	s_add_u32 s69, s62, 0x4000
	s_add_u32 s70, s62, 0x6000
	s_add_u32 s71, s62, 0x8000
	s_add_u32 s72, s62, 0xa000
	s_barrier
	s_branch .LBB3_34
.LBB3_33:
	s_or_b64 exec, exec, s[26:27]
	v_lshl_add_u32 v142, v168, 4, s34
	v_lshl_add_u32 v200, v167, 4, s34
	ds_read_b128 v[188:191], v142
	ds_read_b128 v[192:195], v200
	ds_read_b128 v[196:199], v142 offset:2048
	ds_read_b128 v[200:203], v200 offset:2048
	ds_read_b128 v[204:207], v165 offset:57344
	ds_read_b128 v[208:211], v166 offset:57344
	v_lshl_add_u32 v142, v164, 4, s34
	v_lshl_add_u32 v232, v163, 4, s34
	s_waitcnt lgkmcnt(0)
	v_mfma_f32_32x32x16_f16 v[98:113], v[204:207], v[188:191], v[98:113]
	s_add_u32 s60, s14, 0x18000
	s_addc_u32 s61, s15, 0
	s_add_u32 s44, s44, 0x1fa400
	s_addc_u32 s45, s45, 0
	s_add_u32 s46, s46, 0x1fa400
	s_addc_u32 s47, s47, 0
	s_add_u32 s48, s48, 0x1fa400
	s_addc_u32 s49, s49, 0
	s_add_u32 s50, s50, 0x1fa400
	s_addc_u32 s51, s51, 0
	s_add_u32 s52, s52, 0x1fa400
	s_addc_u32 s53, s53, 0
	s_add_u32 s54, s54, 0x1fa400
	s_addc_u32 s55, s55, 0
	s_add_u32 s56, s56, 0x1fa400
	s_addc_u32 s57, s57, 0
	s_add_u32 s58, s58, 0x1fa400
	s_addc_u32 s59, s59, 0
	s_cmp_lt_u32 s31, 30
	s_cselect_b64 s[36:37], -1, 0
	s_and_b64 s[36:37], s[36:37], s[10:11]
	s_mov_b32 m0, s70
	s_nop 0
	global_load_lds_dwordx4 v130, s[60:61]
	ds_read_b128 v[212:215], v165 offset:59392
	ds_read_b128 v[216:219], v166 offset:59392
	s_add_u32 s12, s12, 0x1fa400
	s_addc_u32 s13, s13, 0
	s_add_u32 s14, s14, 0x12000
	s_addc_u32 s15, s15, 0
	s_cmp_eq_u32 s12, 0x3d4dc00
	v_mfma_f32_32x32x16_f16 v[114:129], v[204:207], v[192:195], v[114:129]
	s_mov_b32 m0, s71
	s_nop 0
	global_load_lds_dwordx4 v132, s[60:61]
	ds_read_b128 v[220:223], v142
	ds_read_b128 v[224:227], v232
	s_mov_b32 s31, s33
	v_mfma_f32_32x32x16_f16 v[114:129], v[208:211], v[188:191], v[114:129]
	s_mov_b32 m0, s72
	s_nop 0
	global_load_lds_dwordx4 v134, s[60:61]
	ds_read_b128 v[228:231], v142 offset:2048
	ds_read_b128 v[232:235], v232 offset:2048
	v_mfma_f32_32x32x16_f16 v[66:81], v[204:207], v[196:199], v[66:81]
	v_mov_b32_e32 v143, 0
	v_mov_b32_e32 v187, 0
	v_mov_b32_e32 v186, 0
	v_mov_b32_e32 v185, 0
	ds_read_b128 v[236:239], v161
	ds_read_b128 v[240:243], v162
	v_mfma_f32_32x32x16_f16 v[82:97], v[204:207], v[200:203], v[82:97]
	v_mov_b32_e32 v147, 0
	v_mov_b32_e32 v145, 0
	v_mov_b32_e32 v144, 0
	v_mov_b32_e32 v146, 0
	ds_read_b128 v[204:207], v159
	ds_read_b128 v[244:247], v160
	s_waitcnt lgkmcnt(0)
	s_barrier
	v_mfma_f32_32x32x16_f16 v[82:97], v[208:211], v[196:199], v[82:97]
	s_mov_b64 exec, s[36:37]
	global_load_dword v143, v140, s[44:45]
	global_load_dword v187, v140, s[46:47]
	s_mov_b64 exec, -1
	s_nop 0
	s_waitcnt lgkmcnt(0)
	v_mfma_f32_32x32x16_f16 v[34:49], v[212:215], v[188:191], v[34:49]
	s_mov_b64 exec, s[36:37]
	global_load_dword v186, v140, s[48:49]
	global_load_dword v185, v140, s[50:51]
	s_mov_b64 exec, -1
	s_nop 0
	v_mfma_f32_32x32x16_f16 v[50:65], v[212:215], v[192:195], v[50:65]
	s_mov_b64 exec, s[36:37]
	global_load_dword v147, v140, s[52:53]
	global_load_dword v145, v140, s[54:55]
	s_mov_b64 exec, -1
	s_nop 0
	v_mfma_f32_32x32x16_f16 v[50:65], v[216:219], v[188:191], v[50:65]
	s_mov_b64 exec, s[36:37]
	global_load_dword v144, v140, s[56:57]
	global_load_dword v146, v140, s[58:59]
	s_mov_b64 exec, -1
	s_nop 0
	v_mfma_f32_32x32x16_f16 v[2:17], v[212:215], v[196:199], v[2:17]
	v_mfma_f32_32x32x16_f16 v[18:33], v[212:215], v[200:203], v[18:33]
	v_mfma_f32_32x32x16_f16 v[18:33], v[216:219], v[196:199], v[18:33]
	v_mfma_f32_32x32x16_f16 v[98:113], v[236:239], v[220:223], v[98:113]
	v_mfma_f32_32x32x16_f16 v[114:129], v[236:239], v[224:227], v[114:129]
	v_mfma_f32_32x32x16_f16 v[114:129], v[240:243], v[220:223], v[114:129]
	v_mfma_f32_32x32x16_f16 v[66:81], v[236:239], v[228:231], v[66:81]
	v_mfma_f32_32x32x16_f16 v[82:97], v[236:239], v[232:235], v[82:97]
	v_mfma_f32_32x32x16_f16 v[82:97], v[240:243], v[228:231], v[82:97]
	v_mfma_f32_32x32x16_f16 v[34:49], v[204:207], v[220:223], v[34:49]
	v_mfma_f32_32x32x16_f16 v[50:65], v[204:207], v[224:227], v[50:65]
	v_mfma_f32_32x32x16_f16 v[50:65], v[244:247], v[220:223], v[50:65]
	v_mfma_f32_32x32x16_f16 v[2:17], v[204:207], v[228:231], v[2:17]
	v_mfma_f32_32x32x16_f16 v[18:33], v[204:207], v[232:235], v[18:33]
	v_mfma_f32_32x32x16_f16 v[18:33], v[244:247], v[228:231], v[18:33]
	s_cbranch_scc1 .LBB3_46
.LBB3_34:
	s_and_b32 s34, s31, 1
	s_mul_i32 s34, s34, 0x9b80
	v_lshl_add_u32 v142, v184, 4, s34
	v_lshl_add_u32 v200, v183, 4, s34
	ds_read_b128 v[188:191], v142
	ds_read_b128 v[192:195], v200
	ds_read_b128 v[196:199], v142 offset:2048
	ds_read_b128 v[200:203], v200 offset:2048
	s_waitcnt vmcnt(0)
	ds_read_b128 v[204:207], v165
	ds_read_b128 v[208:211], v166
	s_add_i32 s33, s31, 1
	s_and_b32 s35, s33, 1
	s_waitcnt lgkmcnt(0)
	v_mfma_f32_32x32x16_f16 v[98:113], v[204:207], v[188:191], v[98:113]
	ds_read_b128 v[212:215], v165 offset:2048
	ds_read_b128 v[216:219], v166 offset:2048
	s_waitcnt vmcnt(0)
	s_mul_i32 s35, s35, 0x9b80
	v_mfma_f32_32x32x16_f16 v[114:129], v[204:207], v[192:195], v[114:129]
	v_cvt_f16_f32_e32 v250, v143
	v_cvt_f16_f32_e32 v251, v187
	v_cvt_f32_f16_e32 v254, v250
	v_cvt_f32_f16_e32 v255, v251
	v_cmp_lt_f32_e64 s[36:37], |v254|, s30
	v_cmp_lt_f32_e64 s[38:39], |v255|, s30
	s_nop 0
	v_mfma_f32_32x32x16_f16 v[114:129], v[208:211], v[188:191], v[114:129]
	v_cndmask_b32_e64 v254, v254, 0, s[36:37]
	v_cndmask_b32_e64 v250, v250, 0, s[36:37]
	v_cndmask_b32_e64 v255, v255, 0, s[38:39]
	v_cndmask_b32_e64 v251, v251, 0, s[38:39]
	v_sub_f32_e32 v143, v143, v254
	v_sub_f32_e32 v187, v187, v255
	v_mul_f32_e32 v143, 0x45000000, v143
	v_mfma_f32_32x32x16_f16 v[66:81], v[204:207], v[196:199], v[66:81]
	v_mul_f32_e32 v187, 0x45000000, v187
	v_pack_b32_f16 v248, v250, v251
	v_cvt_pk_f16_f32 v252, v143, v187
	v_cvt_f16_f32_e32 v250, v186
	v_cvt_f16_f32_e32 v251, v185
	v_cvt_f32_f16_e32 v254, v250
	v_cvt_f32_f16_e32 v255, v251
	v_mfma_f32_32x32x16_f16 v[82:97], v[204:207], v[200:203], v[82:97]
	v_cmp_lt_f32_e64 s[36:37], |v254|, s30
	v_cmp_lt_f32_e64 s[38:39], |v255|, s30
	s_nop 0
	v_cndmask_b32_e64 v254, v254, 0, s[36:37]
	v_cndmask_b32_e64 v250, v250, 0, s[36:37]
	v_cndmask_b32_e64 v255, v255, 0, s[38:39]
	v_cndmask_b32_e64 v251, v251, 0, s[38:39]
	v_mfma_f32_32x32x16_f16 v[82:97], v[208:211], v[196:199], v[82:97]
	v_sub_f32_e32 v186, v186, v254
	v_sub_f32_e32 v185, v185, v255
	v_mul_f32_e32 v186, 0x45000000, v186
	v_mul_f32_e32 v185, 0x45000000, v185
	v_pack_b32_f16 v249, v250, v251
	v_cvt_pk_f16_f32 v253, v186, v185
	v_cvt_f16_f32_e32 v143, v147
	s_waitcnt lgkmcnt(1)
	v_mfma_f32_32x32x16_f16 v[34:49], v[212:215], v[188:191], v[34:49]
	v_cvt_f16_f32_e32 v187, v145
	v_cvt_f32_f16_e32 v186, v143
	v_cvt_f32_f16_e32 v185, v187
	v_cmp_lt_f32_e64 s[36:37], |v186|, s30
	v_cmp_lt_f32_e64 s[38:39], |v185|, s30
	s_nop 0
	v_cndmask_b32_e64 v186, v186, 0, s[36:37]
	v_mfma_f32_32x32x16_f16 v[50:65], v[212:215], v[192:195], v[50:65]
	v_cndmask_b32_e64 v143, v143, 0, s[36:37]
	v_cndmask_b32_e64 v185, v185, 0, s[38:39]
	v_cndmask_b32_e64 v187, v187, 0, s[38:39]
	v_sub_f32_e32 v147, v147, v186
	v_sub_f32_e32 v145, v145, v185
	v_mul_f32_e32 v147, 0x45000000, v147
	v_mul_f32_e32 v145, 0x45000000, v145
	s_waitcnt lgkmcnt(0)
	v_mfma_f32_32x32x16_f16 v[50:65], v[216:219], v[188:191], v[50:65]
	v_pack_b32_f16 v250, v143, v187
	v_cvt_pk_f16_f32 v254, v147, v145
	v_cvt_f16_f32_e32 v143, v144
	v_cvt_f16_f32_e32 v187, v146
	v_cvt_f32_f16_e32 v186, v143
	v_cvt_f32_f16_e32 v185, v187
	v_cmp_lt_f32_e64 s[36:37], |v186|, s30
	v_mfma_f32_32x32x16_f16 v[2:17], v[212:215], v[196:199], v[2:17]
	v_cmp_lt_f32_e64 s[38:39], |v185|, s30
	s_nop 0
	v_cndmask_b32_e64 v186, v186, 0, s[36:37]
	v_cndmask_b32_e64 v143, v143, 0, s[36:37]
	v_cndmask_b32_e64 v185, v185, 0, s[38:39]
	v_cndmask_b32_e64 v187, v187, 0, s[38:39]
	v_sub_f32_e32 v144, v144, v186
	v_mfma_f32_32x32x16_f16 v[18:33], v[212:215], v[200:203], v[18:33]
	v_sub_f32_e32 v146, v146, v185
	v_mul_f32_e32 v144, 0x45000000, v144
	v_mul_f32_e32 v146, 0x45000000, v146
	v_pack_b32_f16 v251, v143, v187
	v_cvt_pk_f16_f32 v255, v144, v146
	v_mfma_f32_32x32x16_f16 v[18:33], v[216:219], v[196:199], v[18:33]
	v_lshl_add_u32 v147, v152, 4, s35
	v_lshl_add_u32 v145, v1, 4, s35
	s_and_saveexec_b64 s[26:27], s[0:1]
	ds_write_b128 v147, v[248:251]
	ds_write_b128 v145, v[252:255]
	s_mov_b64 exec, s[26:27]
	v_lshl_add_u32 v193, v180, 4, s34
	v_lshl_add_u32 v206, v179, 4, s34
	ds_read_b128 v[194:197], v193
	ds_read_b128 v[198:201], v206
	ds_read_b128 v[202:205], v193 offset:2048
	ds_read_b128 v[206:209], v206 offset:2048
	ds_read_b128 v[210:213], v165 offset:8192
	ds_read_b128 v[214:217], v166 offset:8192
	v_lshl_add_u32 v193, v178, 4, s34
	s_waitcnt lgkmcnt(0)
	v_mfma_f32_32x32x16_f16 v[98:113], v[210:213], v[194:197], v[98:113]
	s_add_u32 s60, s14, 0xc000
	s_addc_u32 s61, s15, 0
	s_mov_b32 m0, s64
	s_nop 0
	global_load_lds_dwordx4 v130, s[60:61]
	ds_read_b128 v[218:221], v165 offset:10240
	ds_read_b128 v[222:225], v166 offset:10240
	v_mfma_f32_32x32x16_f16 v[114:129], v[210:213], v[198:201], v[114:129]
	s_mov_b32 m0, s65
	s_nop 0
	global_load_lds_dwordx4 v132, s[60:61]
	v_mfma_f32_32x32x16_f16 v[114:129], v[214:217], v[194:197], v[114:129]
	s_mov_b32 m0, s66
	s_nop 0
	global_load_lds_dwordx4 v134, s[60:61]
	v_mfma_f32_32x32x16_f16 v[66:81], v[210:213], v[202:205], v[66:81]
	v_mov_b32_e32 v143, 0
	v_mov_b32_e32 v187, 0
	v_mov_b32_e32 v186, 0
	v_mov_b32_e32 v185, 0
	v_mfma_f32_32x32x16_f16 v[82:97], v[210:213], v[206:209], v[82:97]
	v_mov_b32_e32 v147, 0
	v_mov_b32_e32 v145, 0
	v_mov_b32_e32 v144, 0
	v_mov_b32_e32 v146, 0
	ds_read_b128 v[210:213], v165 offset:16384
	v_mfma_f32_32x32x16_f16 v[82:97], v[214:217], v[202:205], v[82:97]
	s_mov_b64 exec, s[6:7]
	global_load_dword v143, v136, s[44:45]
	global_load_dword v187, v136, s[46:47]
	s_mov_b64 exec, -1
	s_nop 0
	ds_read_b128 v[214:217], v166 offset:16384
	s_waitcnt lgkmcnt(0)
	v_mfma_f32_32x32x16_f16 v[34:49], v[218:221], v[194:197], v[34:49]
	s_mov_b64 exec, s[6:7]
	global_load_dword v186, v136, s[48:49]
	global_load_dword v185, v136, s[50:51]
	s_mov_b64 exec, -1
	s_nop 0
	v_mfma_f32_32x32x16_f16 v[50:65], v[218:221], v[198:201], v[50:65]
	s_mov_b64 exec, s[6:7]
	global_load_dword v147, v136, s[52:53]
	global_load_dword v145, v136, s[54:55]
	s_mov_b64 exec, -1
	s_nop 0
	v_mfma_f32_32x32x16_f16 v[50:65], v[222:225], v[194:197], v[50:65]
	s_mov_b64 exec, s[6:7]
	global_load_dword v144, v136, s[56:57]
	global_load_dword v146, v136, s[58:59]
	s_mov_b64 exec, -1
	s_nop 0
	ds_read_b128 v[194:197], v193
	v_mfma_f32_32x32x16_f16 v[2:17], v[218:221], v[202:205], v[2:17]
	v_mfma_f32_32x32x16_f16 v[18:33], v[218:221], v[206:209], v[18:33]
	v_lshl_add_u32 v206, v177, 4, s34
	ds_read_b128 v[198:201], v206
	ds_read_b128 v[206:209], v206 offset:2048
	v_mfma_f32_32x32x16_f16 v[18:33], v[222:225], v[202:205], v[18:33]
	ds_read_b128 v[202:205], v193 offset:2048
	ds_read_b128 v[218:221], v165 offset:18432
	v_lshl_add_u32 v193, v176, 4, s34
	s_waitcnt lgkmcnt(0)
	v_mfma_f32_32x32x16_f16 v[98:113], v[210:213], v[194:197], v[98:113]
	ds_read_b128 v[222:225], v166 offset:18432
	s_waitcnt lgkmcnt(0)
	s_barrier
	v_mfma_f32_32x32x16_f16 v[114:129], v[210:213], v[198:201], v[114:129]
	v_mfma_f32_32x32x16_f16 v[114:129], v[214:217], v[194:197], v[114:129]
	v_mfma_f32_32x32x16_f16 v[66:81], v[210:213], v[202:205], v[66:81]
	v_mfma_f32_32x32x16_f16 v[82:97], v[210:213], v[206:209], v[82:97]
	ds_read_b128 v[210:213], v165 offset:24576
	v_mfma_f32_32x32x16_f16 v[82:97], v[214:217], v[202:205], v[82:97]
	ds_read_b128 v[214:217], v166 offset:24576
	v_mfma_f32_32x32x16_f16 v[34:49], v[218:221], v[194:197], v[34:49]
	v_mfma_f32_32x32x16_f16 v[50:65], v[218:221], v[198:201], v[50:65]
	s_waitcnt lgkmcnt(0)
	v_mfma_f32_32x32x16_f16 v[50:65], v[222:225], v[194:197], v[50:65]
	ds_read_b128 v[194:197], v193
	v_mfma_f32_32x32x16_f16 v[2:17], v[218:221], v[202:205], v[2:17]
	v_mfma_f32_32x32x16_f16 v[18:33], v[218:221], v[206:209], v[18:33]
	v_lshl_add_u32 v206, v175, 4, s34
	ds_read_b128 v[198:201], v206
	ds_read_b128 v[206:209], v206 offset:2048
	v_mfma_f32_32x32x16_f16 v[18:33], v[222:225], v[202:205], v[18:33]
	ds_read_b128 v[202:205], v193 offset:2048
	ds_read_b128 v[218:221], v165 offset:26624
	s_waitcnt lgkmcnt(0)
	v_mfma_f32_32x32x16_f16 v[98:113], v[210:213], v[194:197], v[98:113]
	ds_read_b128 v[222:225], v166 offset:26624
	s_waitcnt vmcnt(0)
	v_mfma_f32_32x32x16_f16 v[114:129], v[210:213], v[198:201], v[114:129]
	v_cvt_f16_f32_e32 v250, v143
	v_cvt_f16_f32_e32 v251, v187
	v_cvt_f32_f16_e32 v254, v250
	v_cvt_f32_f16_e32 v255, v251
	v_cmp_lt_f32_e64 s[36:37], |v254|, s30
	v_cmp_lt_f32_e64 s[38:39], |v255|, s30
	s_nop 0
	v_mfma_f32_32x32x16_f16 v[114:129], v[214:217], v[194:197], v[114:129]
	v_cndmask_b32_e64 v254, v254, 0, s[36:37]
	v_cndmask_b32_e64 v250, v250, 0, s[36:37]
	v_cndmask_b32_e64 v255, v255, 0, s[38:39]
	v_cndmask_b32_e64 v251, v251, 0, s[38:39]
	v_sub_f32_e32 v143, v143, v254
	v_sub_f32_e32 v187, v187, v255
	v_mul_f32_e32 v143, 0x45000000, v143
	v_mfma_f32_32x32x16_f16 v[66:81], v[210:213], v[202:205], v[66:81]
	v_mul_f32_e32 v187, 0x45000000, v187
	v_pack_b32_f16 v248, v250, v251
	v_cvt_pk_f16_f32 v252, v143, v187
	v_cvt_f16_f32_e32 v250, v186
	v_cvt_f16_f32_e32 v251, v185
	v_cvt_f32_f16_e32 v254, v250
	v_cvt_f32_f16_e32 v255, v251
	v_mfma_f32_32x32x16_f16 v[82:97], v[210:213], v[206:209], v[82:97]
	v_cmp_lt_f32_e64 s[36:37], |v254|, s30
	v_cmp_lt_f32_e64 s[38:39], |v255|, s30
	s_nop 0
	v_cndmask_b32_e64 v254, v254, 0, s[36:37]
	v_cndmask_b32_e64 v250, v250, 0, s[36:37]
	v_cndmask_b32_e64 v255, v255, 0, s[38:39]
	v_cndmask_b32_e64 v251, v251, 0, s[38:39]
	v_mfma_f32_32x32x16_f16 v[82:97], v[214:217], v[202:205], v[82:97]
	v_sub_f32_e32 v186, v186, v254
	v_sub_f32_e32 v185, v185, v255
	v_mul_f32_e32 v186, 0x45000000, v186
	v_mul_f32_e32 v185, 0x45000000, v185
	v_pack_b32_f16 v249, v250, v251
	v_cvt_pk_f16_f32 v253, v186, v185
	v_cvt_f16_f32_e32 v143, v147
	v_mfma_f32_32x32x16_f16 v[34:49], v[218:221], v[194:197], v[34:49]
	v_cvt_f16_f32_e32 v187, v145
	v_cvt_f32_f16_e32 v186, v143
	v_cvt_f32_f16_e32 v185, v187
	v_cmp_lt_f32_e64 s[36:37], |v186|, s30
	v_cmp_lt_f32_e64 s[38:39], |v185|, s30
	s_nop 0
	v_cndmask_b32_e64 v186, v186, 0, s[36:37]
	v_mfma_f32_32x32x16_f16 v[50:65], v[218:221], v[198:201], v[50:65]
	v_cndmask_b32_e64 v143, v143, 0, s[36:37]
	v_cndmask_b32_e64 v185, v185, 0, s[38:39]
	v_cndmask_b32_e64 v187, v187, 0, s[38:39]
	v_sub_f32_e32 v147, v147, v186
	v_sub_f32_e32 v145, v145, v185
	v_mul_f32_e32 v147, 0x45000000, v147
	v_mul_f32_e32 v145, 0x45000000, v145
	s_waitcnt lgkmcnt(0)
	v_mfma_f32_32x32x16_f16 v[50:65], v[222:225], v[194:197], v[50:65]
	v_pack_b32_f16 v250, v143, v187
	v_cvt_pk_f16_f32 v254, v147, v145
	v_cvt_f16_f32_e32 v143, v144
	v_cvt_f16_f32_e32 v187, v146
	v_cvt_f32_f16_e32 v186, v143
	v_cvt_f32_f16_e32 v185, v187
	v_cmp_lt_f32_e64 s[36:37], |v186|, s30
	v_mfma_f32_32x32x16_f16 v[2:17], v[218:221], v[202:205], v[2:17]
	v_cmp_lt_f32_e64 s[38:39], |v185|, s30
	s_nop 0
	v_cndmask_b32_e64 v186, v186, 0, s[36:37]
	v_cndmask_b32_e64 v143, v143, 0, s[36:37]
	v_cndmask_b32_e64 v185, v185, 0, s[38:39]
	v_cndmask_b32_e64 v187, v187, 0, s[38:39]
	v_sub_f32_e32 v144, v144, v186
	v_mfma_f32_32x32x16_f16 v[18:33], v[218:221], v[206:209], v[18:33]
	v_sub_f32_e32 v146, v146, v185
	v_mul_f32_e32 v144, 0x45000000, v144
	v_mul_f32_e32 v146, 0x45000000, v146
	v_pack_b32_f16 v251, v143, v187
	v_cvt_pk_f16_f32 v255, v144, v146
	v_mfma_f32_32x32x16_f16 v[18:33], v[222:225], v[202:205], v[18:33]
	v_lshl_add_u32 v147, v154, 4, s35
	v_lshl_add_u32 v145, v153, 4, s35
	s_and_saveexec_b64 s[26:27], s[2:3]
	ds_write_b128 v147, v[248:251]
	ds_write_b128 v145, v[252:255]
	s_mov_b64 exec, s[26:27]
	v_lshl_add_u32 v193, v174, 4, s34
	v_lshl_add_u32 v206, v173, 4, s34
	ds_read_b128 v[194:197], v193
	ds_read_b128 v[198:201], v206
	ds_read_b128 v[202:205], v193 offset:2048
	ds_read_b128 v[206:209], v206 offset:2048
	ds_read_b128 v[210:213], v165 offset:32768
	ds_read_b128 v[214:217], v166 offset:32768
	v_lshl_add_u32 v193, v172, 4, s34
	s_waitcnt lgkmcnt(0)
	v_mfma_f32_32x32x16_f16 v[98:113], v[210:213], v[194:197], v[98:113]
	s_add_u32 s60, s14, 0x12000
	s_addc_u32 s61, s15, 0
	s_mov_b32 m0, s67
	s_nop 0
	global_load_lds_dwordx4 v130, s[60:61]
	ds_read_b128 v[218:221], v165 offset:34816
	ds_read_b128 v[222:225], v166 offset:34816
	v_mfma_f32_32x32x16_f16 v[114:129], v[210:213], v[198:201], v[114:129]
	s_mov_b32 m0, s68
	s_nop 0
	global_load_lds_dwordx4 v132, s[60:61]
	v_mfma_f32_32x32x16_f16 v[114:129], v[214:217], v[194:197], v[114:129]
	s_mov_b32 m0, s69
	s_nop 0
	global_load_lds_dwordx4 v134, s[60:61]
	v_mfma_f32_32x32x16_f16 v[66:81], v[210:213], v[202:205], v[66:81]
	v_mov_b32_e32 v143, 0
	v_mov_b32_e32 v187, 0
	v_mov_b32_e32 v186, 0
	v_mov_b32_e32 v185, 0
	v_mfma_f32_32x32x16_f16 v[82:97], v[210:213], v[206:209], v[82:97]
	v_mov_b32_e32 v147, 0
	v_mov_b32_e32 v145, 0
	v_mov_b32_e32 v144, 0
	v_mov_b32_e32 v146, 0
	ds_read_b128 v[210:213], v165 offset:40960
	v_mfma_f32_32x32x16_f16 v[82:97], v[214:217], v[202:205], v[82:97]
	s_mov_b64 exec, s[8:9]
	global_load_dword v143, v138, s[44:45]
	global_load_dword v187, v138, s[46:47]
	s_mov_b64 exec, -1
	s_nop 0
	ds_read_b128 v[214:217], v166 offset:40960
	s_waitcnt lgkmcnt(0)
	v_mfma_f32_32x32x16_f16 v[34:49], v[218:221], v[194:197], v[34:49]
	s_mov_b64 exec, s[8:9]
	global_load_dword v186, v138, s[48:49]
	global_load_dword v185, v138, s[50:51]
	s_mov_b64 exec, -1
	s_nop 0
	v_mfma_f32_32x32x16_f16 v[50:65], v[218:221], v[198:201], v[50:65]
	s_mov_b64 exec, s[8:9]
	global_load_dword v147, v138, s[52:53]
	global_load_dword v145, v138, s[54:55]
	s_mov_b64 exec, -1
	s_nop 0
	v_mfma_f32_32x32x16_f16 v[50:65], v[222:225], v[194:197], v[50:65]
	s_mov_b64 exec, s[8:9]
	global_load_dword v144, v138, s[56:57]
	global_load_dword v146, v138, s[58:59]
	s_mov_b64 exec, -1
	s_nop 0
	ds_read_b128 v[194:197], v193
	v_mfma_f32_32x32x16_f16 v[2:17], v[218:221], v[202:205], v[2:17]
	v_mfma_f32_32x32x16_f16 v[18:33], v[218:221], v[206:209], v[18:33]
	v_lshl_add_u32 v206, v171, 4, s34
	ds_read_b128 v[198:201], v206
	ds_read_b128 v[206:209], v206 offset:2048
	v_mfma_f32_32x32x16_f16 v[18:33], v[222:225], v[202:205], v[18:33]
	ds_read_b128 v[202:205], v193 offset:2048
	ds_read_b128 v[218:221], v165 offset:43008
	v_lshl_add_u32 v193, v170, 4, s34
	s_waitcnt lgkmcnt(0)
	v_mfma_f32_32x32x16_f16 v[98:113], v[210:213], v[194:197], v[98:113]
	ds_read_b128 v[222:225], v166 offset:43008
	s_waitcnt lgkmcnt(0)
	s_barrier
	v_mfma_f32_32x32x16_f16 v[114:129], v[210:213], v[198:201], v[114:129]
	v_mfma_f32_32x32x16_f16 v[114:129], v[214:217], v[194:197], v[114:129]
	v_mfma_f32_32x32x16_f16 v[66:81], v[210:213], v[202:205], v[66:81]
	v_mfma_f32_32x32x16_f16 v[82:97], v[210:213], v[206:209], v[82:97]
	s_waitcnt vmcnt(0)
	ds_read_b128 v[210:213], v165 offset:49152
	v_mfma_f32_32x32x16_f16 v[82:97], v[214:217], v[202:205], v[82:97]
	ds_read_b128 v[214:217], v166 offset:49152
	v_mfma_f32_32x32x16_f16 v[34:49], v[218:221], v[194:197], v[34:49]
	v_mfma_f32_32x32x16_f16 v[50:65], v[218:221], v[198:201], v[50:65]
	s_waitcnt lgkmcnt(2)
	v_mfma_f32_32x32x16_f16 v[50:65], v[222:225], v[194:197], v[50:65]
	ds_read_b128 v[194:197], v193
	v_mfma_f32_32x32x16_f16 v[2:17], v[218:221], v[202:205], v[2:17]
	v_mfma_f32_32x32x16_f16 v[18:33], v[218:221], v[206:209], v[18:33]
	v_lshl_add_u32 v206, v169, 4, s34
	ds_read_b128 v[198:201], v206
	ds_read_b128 v[206:209], v206 offset:2048
	v_mfma_f32_32x32x16_f16 v[18:33], v[222:225], v[202:205], v[18:33]
	ds_read_b128 v[202:205], v193 offset:2048
	ds_read_b128 v[218:221], v165 offset:51200
	s_waitcnt lgkmcnt(4)
	v_mfma_f32_32x32x16_f16 v[98:113], v[210:213], v[194:197], v[98:113]
	ds_read_b128 v[222:225], v166 offset:51200
	s_waitcnt vmcnt(0)
	s_waitcnt lgkmcnt(4)
	v_mfma_f32_32x32x16_f16 v[114:129], v[210:213], v[198:201], v[114:129]
	v_cvt_f16_f32_e32 v250, v143
	v_cvt_f16_f32_e32 v251, v187
	v_cvt_f32_f16_e32 v254, v250
	v_cvt_f32_f16_e32 v255, v251
	v_cmp_lt_f32_e64 s[36:37], |v254|, s30
	v_cmp_lt_f32_e64 s[38:39], |v255|, s30
	s_nop 0
	v_mfma_f32_32x32x16_f16 v[114:129], v[214:217], v[194:197], v[114:129]
	v_cndmask_b32_e64 v254, v254, 0, s[36:37]
	v_cndmask_b32_e64 v250, v250, 0, s[36:37]
	v_cndmask_b32_e64 v255, v255, 0, s[38:39]
	v_cndmask_b32_e64 v251, v251, 0, s[38:39]
	v_sub_f32_e32 v143, v143, v254
	v_sub_f32_e32 v187, v187, v255
	v_mul_f32_e32 v143, 0x45000000, v143
	s_waitcnt lgkmcnt(2)
	v_mfma_f32_32x32x16_f16 v[66:81], v[210:213], v[202:205], v[66:81]
	v_mul_f32_e32 v187, 0x45000000, v187
	v_pack_b32_f16 v248, v250, v251
	v_cvt_pk_f16_f32 v252, v143, v187
	v_cvt_f16_f32_e32 v250, v186
	v_cvt_f16_f32_e32 v251, v185
	v_cvt_f32_f16_e32 v254, v250
	v_cvt_f32_f16_e32 v255, v251
	v_mfma_f32_32x32x16_f16 v[82:97], v[210:213], v[206:209], v[82:97]
	v_cmp_lt_f32_e64 s[36:37], |v254|, s30
	v_cmp_lt_f32_e64 s[38:39], |v255|, s30
	s_nop 0
	v_cndmask_b32_e64 v254, v254, 0, s[36:37]
	v_cndmask_b32_e64 v250, v250, 0, s[36:37]
	v_cndmask_b32_e64 v255, v255, 0, s[38:39]
	v_cndmask_b32_e64 v251, v251, 0, s[38:39]
	v_mfma_f32_32x32x16_f16 v[82:97], v[214:217], v[202:205], v[82:97]
	v_sub_f32_e32 v186, v186, v254
	v_sub_f32_e32 v185, v185, v255
	v_mul_f32_e32 v186, 0x45000000, v186
	v_mul_f32_e32 v185, 0x45000000, v185
	v_pack_b32_f16 v249, v250, v251
	v_cvt_pk_f16_f32 v253, v186, v185
	v_cvt_f16_f32_e32 v143, v147
	s_waitcnt lgkmcnt(1)
	v_mfma_f32_32x32x16_f16 v[34:49], v[218:221], v[194:197], v[34:49]
	v_cvt_f16_f32_e32 v187, v145
	v_cvt_f32_f16_e32 v186, v143
	v_cvt_f32_f16_e32 v185, v187
	v_cmp_lt_f32_e64 s[36:37], |v186|, s30
	v_cmp_lt_f32_e64 s[38:39], |v185|, s30
	s_nop 0
	v_cndmask_b32_e64 v186, v186, 0, s[36:37]
	v_mfma_f32_32x32x16_f16 v[50:65], v[218:221], v[198:201], v[50:65]
	v_cndmask_b32_e64 v143, v143, 0, s[36:37]
	v_cndmask_b32_e64 v185, v185, 0, s[38:39]
	v_cndmask_b32_e64 v187, v187, 0, s[38:39]
	v_sub_f32_e32 v147, v147, v186
	v_sub_f32_e32 v145, v145, v185
	v_mul_f32_e32 v147, 0x45000000, v147
	v_mul_f32_e32 v145, 0x45000000, v145
	s_waitcnt lgkmcnt(0)
	v_mfma_f32_32x32x16_f16 v[50:65], v[222:225], v[194:197], v[50:65]
	v_pack_b32_f16 v250, v143, v187
	v_cvt_pk_f16_f32 v254, v147, v145
	v_cvt_f16_f32_e32 v143, v144
	v_cvt_f16_f32_e32 v187, v146
	v_cvt_f32_f16_e32 v186, v143
	v_cvt_f32_f16_e32 v185, v187
	v_cmp_lt_f32_e64 s[36:37], |v186|, s30
	v_mfma_f32_32x32x16_f16 v[2:17], v[218:221], v[202:205], v[2:17]
	v_cmp_lt_f32_e64 s[38:39], |v185|, s30
	s_nop 0
	v_cndmask_b32_e64 v186, v186, 0, s[36:37]
	v_cndmask_b32_e64 v143, v143, 0, s[36:37]
	v_cndmask_b32_e64 v185, v185, 0, s[38:39]
	v_cndmask_b32_e64 v187, v187, 0, s[38:39]
	v_sub_f32_e32 v144, v144, v186
	v_mfma_f32_32x32x16_f16 v[18:33], v[218:221], v[206:209], v[18:33]
	v_sub_f32_e32 v146, v146, v185
	v_mul_f32_e32 v144, 0x45000000, v144
	v_mul_f32_e32 v146, 0x45000000, v146
	v_pack_b32_f16 v251, v143, v187
	v_cvt_pk_f16_f32 v255, v144, v146
	v_mfma_f32_32x32x16_f16 v[18:33], v[222:225], v[202:205], v[18:33]
	v_lshl_add_u32 v147, v156, 4, s35
	v_lshl_add_u32 v145, v155, 4, s35
	s_and_saveexec_b64 s[26:27], s[4:5]
	ds_write_b128 v147, v[248:251]
	ds_write_b128 v145, v[252:255]
	s_mov_b64 exec, s[26:27]
	s_branch .LBB3_33

.LBB11_2:
	s_andn2_b64 vcc, exec, s[4:5]
	s_cbranch_vccnz .LBB11_16
	s_lshl_b32 s2, s2, 8
	v_lshrrev_b32_e32 v2, 1, v0
	s_addk_i32 s2, 0xce00
	v_and_b32_e32 v2, 0xe0, v2
	v_and_b32_e32 v145, 31, v0
	v_or_b32_e32 v9, s2, v2
	v_or_b32_e32 v144, v9, v145
	s_movk_i32 s2, 0x7e90
	v_mov_b32_e32 v2, 0x7e8f
	v_cmp_gt_i32_e64 s[8:9], s2, v144
	s_mov_b32 s2, 0xb60b60b7
	s_load_dwordx2 s[4:5], s[0:1], 0x1a8
	v_cndmask_b32_e64 v2, v2, v144, s[8:9]
	v_mul_hi_i32 v3, v2, s2
	v_add_u32_e32 v3, v3, v2
	v_lshrrev_b32_e32 v4, 31, v3
	v_ashrrev_i32_e32 v3, 7, v3
	v_add_u32_e32 v8, v3, v4
	s_movk_i32 s2, 0xff4c
	v_mad_u64_u32 v[2:3], s[6:7], v8, s2, v[2:3]
	s_movk_i32 s2, 0xb6
	v_mul_lo_u32 v3, v8, s2
	s_movk_i32 s2, 0xbf
	v_add3_u32 v6, v3, v2, s2
	v_ashrrev_i32_e32 v7, 31, v6
	s_lshl_b32 s36, s3, 3
	v_mov_b64_e32 v[198:199], v[6:7]
	v_bfe_u32 v164, v0, 5, 1
	s_waitcnt lgkmcnt(0)
	s_mov_b64 s[38:39], s[4:5]
	s_or_b32 s34, s36, 1
	s_or_b32 s30, s36, 2
	s_or_b32 s28, s36, 3
	s_or_b32 s26, s36, 4
	s_or_b32 s24, s36, 5
	s_or_b32 s10, s36, 6
	s_or_b32 s2, s36, 7
	s_nop 0
	s_load_dwordx8 s[12:19], s[0:1], 0x1b0
	s_load_dwordx4 s[20:23], s[0:1], 0x1d0
	s_movk_i32 s3, 0x80
	v_cmp_gt_u32_e64 s[4:5], s3, v0
	v_lshlrev_b32_e32 v3, 2, v0
	v_mov_b32_e32 v4, 0
	v_mov_b32_e32 v10, 0
	v_mov_b32_e32 v11, 0
	v_mov_b32_e32 v12, 0
	v_mov_b32_e32 v6, 0
	v_mov_b32_e32 v7, 0
	s_and_saveexec_b64 s[6:7], s[4:5]
	s_cbranch_execz .LBB11_5
	v_lshlrev_b32_e32 v13, 3, v0
	s_waitcnt lgkmcnt(0)
	global_load_dwordx2 v[6:7], v13, s[12:13]
	global_load_dword v12, v3, s[14:15]
	global_load_dword v11, v3, s[16:17]
	global_load_dword v10, v3, s[18:19]
	global_load_dword v4, v3, s[20:21]

.LBB11_9:
	s_or_b64 exec, exec, s[12:13]
	s_and_saveexec_b64 s[4:5], s[6:7]
	v_mov_b32_e32 v1, 0x21200
	v_lshl_add_u32 v0, v0, 2, v1
	ds_write_b32 v0, v5
	s_or_b64 exec, exec, s[4:5]
	s_movk_i32 s3, 0x7e90
	v_cmp_gt_i32_e32 vcc, s3, v9
	s_waitcnt lgkmcnt(0)
	s_barrier
	s_and_saveexec_b64 s[4:5], vcc
	s_cbranch_execz .LBB11_16
	v_lshlrev_b32_e32 v94, 5, v164
	v_or_b32_e32 v0, 0x1f800, v94
	v_or_b32_e32 v4, 0x1fa00, v94
	v_cvt_f32_i32_e32 v9, v8
	v_cvt_f32_i32_e32 v8, v2
	ds_read_b128 v[0:3], v0
	ds_read_b128 v[4:7], v4
	v_lshlrev_b32_e32 v165, 4, v164
	s_movk_i32 s3, 0x110
	v_pk_add_f32 v[92:93], v[8:9], 0.5 op_sel_hi:[1,0]
	s_waitcnt lgkmcnt(1)
	v_mov_b32_e32 v8, v0
	s_waitcnt lgkmcnt(0)
	v_mov_b32_e32 v9, v4
	v_or_b32_e32 v0, 0x1fc00, v94
	v_pk_mul_f32 v[20:21], v[92:93], v[8:9]
	v_or_b32_e32 v4, 0x1fe00, v94
	ds_read_b128 v[8:11], v0
	ds_read_b128 v[12:15], v4
	v_or_b32_e32 v0, 0x20000, v94
	ds_read_b128 v[16:19], v0
	v_add_f32_e32 v0, v20, v21
	s_waitcnt lgkmcnt(2)
	v_add_f32_e32 v0, v8, v0
	v_or_b32_e32 v4, 0x1f810, v94
	ds_read_b128 v[20:23], v4
	s_waitcnt lgkmcnt(1)
	v_fma_f32 v0, v12, v0, v16
	v_mov_b32_e32 v4, v1
	v_max_f32_e32 v24, 0, v0
	v_pk_mul_f32 v[0:1], v[92:93], v[4:5]
	v_or_b32_e32 v4, 0x1fc10, v94
	v_add_f32_e32 v0, v0, v1
	v_add_f32_e32 v0, v9, v0
	v_fma_f32 v0, v13, v0, v17
	v_max_f32_e32 v25, 0, v0
	v_mov_b32_e32 v0, v2
	v_mov_b32_e32 v1, v6
	v_pk_mul_f32 v[0:1], v[92:93], v[0:1]
	v_mov_b32_e32 v6, v3
	v_add_f32_e32 v0, v0, v1
	v_add_f32_e32 v0, v10, v0
	v_fma_f32 v0, v14, v0, v18
	v_max_f32_e32 v18, 0, v0
	v_pk_mul_f32 v[0:1], v[92:93], v[6:7]
	v_or_b32_e32 v8, 0x1fe10, v94
	v_add_f32_e32 v0, v0, v1
	v_add_f32_e32 v0, v11, v0
	v_fmac_f32_e32 v19, v15, v0
	v_or_b32_e32 v0, 0x1fa10, v94
	ds_read_b128 v[0:3], v0
	ds_read_b128 v[4:7], v4
	v_or_b32_e32 v12, 0x20010, v94
	ds_read_b128 v[8:11], v8
	ds_read_b128 v[12:15], v12
	s_waitcnt lgkmcnt(4)
	v_mov_b32_e32 v16, v20
	s_waitcnt lgkmcnt(3)
	v_mov_b32_e32 v17, v0
	v_pk_mul_f32 v[16:17], v[92:93], v[16:17]
	v_mad_u32_u24 v166, v145, s3, v165
	v_add_f32_e32 v0, v16, v17
	s_waitcnt lgkmcnt(2)
	v_add_f32_e32 v0, v4, v0
	s_waitcnt lgkmcnt(0)
	v_fma_f32 v0, v8, v0, v12
	v_max_f32_e32 v4, 0, v0
	v_mov_b32_e32 v0, v21
	v_pk_mul_f32 v[0:1], v[92:93], v[0:1]
	v_max_f32_e32 v19, 0, v19
	v_add_f32_e32 v0, v0, v1
	v_add_f32_e32 v0, v5, v0
	v_fma_f32 v0, v9, v0, v13
	v_max_f32_e32 v5, 0, v0
	v_mov_b32_e32 v0, v22
	v_mov_b32_e32 v1, v2
	v_pk_mul_f32 v[0:1], v[92:93], v[0:1]
	v_mov_b32_e32 v2, v23
	v_add_f32_e32 v0, v0, v1
	v_add_f32_e32 v0, v6, v0
	v_fma_f32 v0, v10, v0, v14
	v_max_f32_e32 v6, 0, v0
	v_pk_mul_f32 v[0:1], v[92:93], v[2:3]
	ds_read_b128 v[96:99], v166 offset:32
	v_add_f32_e32 v8, v0, v1
	ds_read_b128 v[0:3], v166
	v_add_f32_e32 v7, v7, v8
	v_fmac_f32_e32 v15, v11, v7
	v_max_f32_e32 v7, 0, v15
	v_cvt_pk_f16_f32 v7, v6, v7
	v_cvt_pk_f16_f32 v6, v4, v5
	v_cvt_pk_f16_f32 v5, v18, v19
	v_cvt_pk_f16_f32 v4, v24, v25
	v_or_b32_e32 v8, 0x1f840, v94
	v_or_b32_e32 v9, 0x1fa40, v94
	s_waitcnt lgkmcnt(0)
	v_mfma_f32_32x32x16_f16 v[48:63], v[0:3], v[4:7], 0
	v_mov_b32_e32 v190, 0x8180
	v_mad_i64_i32 v[192:193], s[40:41], s36, v190, v[198:199]
	v_lshlrev_b64 v[192:193], 6, v[192:193]
	v_lshl_add_u64 v[196:197], s[38:39], 0, v[192:193]
	v_mov_b32_e32 v193, 0
	v_lshlrev_b32_e32 v192, 3, v164
	v_lshl_add_u64 v[196:197], v[196:197], 0, v[192:193]
	global_load_dwordx2 v[90:91], v[196:197], off
	global_load_dwordx2 v[88:89], v[196:197], off offset:32
	global_load_dwordx2 v[84:85], v[196:197], off offset:48
	global_load_dwordx2 v[86:87], v[196:197], off offset:16
	ds_read_b128 v[0:3], v166 offset:8704
	ds_read_b128 v[100:103], v166 offset:8736
	v_or_b32_e32 v95, 0x1fc40, v94
	s_mov_b32 s4, 0x3a000000
	s_ashr_i32 s37, s36, 31
	s_waitcnt lgkmcnt(1)
	v_mfma_f32_32x32x16_f16 v[32:47], v[0:3], v[4:7], 0
	v_mad_i64_i32 v[196:197], s[40:41], s34, v190, v[198:199]
	v_lshlrev_b64 v[196:197], 6, v[196:197]
	v_lshl_add_u64 v[196:197], s[38:39], 0, v[196:197]
	v_lshl_add_u64 v[196:197], v[196:197], 0, v[192:193]
	global_load_dwordx2 v[82:83], v[196:197], off
	global_load_dwordx2 v[80:81], v[196:197], off offset:32
	global_load_dwordx2 v[76:77], v[196:197], off offset:48
	global_load_dwordx2 v[78:79], v[196:197], off offset:16
	ds_read_b128 v[0:3], v166 offset:17408
	ds_read_b128 v[104:107], v166 offset:17440
	s_ashr_i32 s35, s34, 31
	s_ashr_i32 s31, s30, 31
	s_ashr_i32 s29, s28, 31
	s_ashr_i32 s27, s26, 31
	s_ashr_i32 s25, s24, 31
	s_ashr_i32 s11, s10, 31
	s_waitcnt lgkmcnt(1)
	v_mfma_f32_32x32x16_f16 v[16:31], v[0:3], v[4:7], 0
	v_mad_i64_i32 v[196:197], s[40:41], s30, v190, v[198:199]
	v_lshlrev_b64 v[196:197], 6, v[196:197]
	v_lshl_add_u64 v[196:197], s[38:39], 0, v[196:197]
	v_lshl_add_u64 v[196:197], v[196:197], 0, v[192:193]
	global_load_dwordx2 v[74:75], v[196:197], off
	global_load_dwordx2 v[72:73], v[196:197], off offset:32
	global_load_dwordx2 v[68:69], v[196:197], off offset:48
	global_load_dwordx2 v[70:71], v[196:197], off offset:16
	ds_read_b128 v[0:3], v166 offset:26112
	ds_read_b128 v[108:111], v8
	ds_read_b128 v[112:115], v9
	ds_read_b128 v[116:119], v166 offset:26144
	s_ashr_i32 s3, s2, 31
	s_waitcnt lgkmcnt(2)
	v_mov_b32_e32 v120, v108
	s_waitcnt lgkmcnt(1)
	v_mov_b32_e32 v121, v112
	v_pk_mul_f32 v[124:125], v[92:93], v[120:121]
	v_or_b32_e32 v108, 0x1fe40, v94
	ds_read_b128 v[120:123], v95
	ds_read_b128 v[168:171], v108
	v_or_b32_e32 v95, 0x20040, v94
	ds_read_b128 v[172:175], v95
	v_or_b32_e32 v108, 0x1f850, v94
	v_mov_b32_e32 v112, v109
	ds_read_b128 v[176:179], v108
	v_pk_mul_f32 v[108:109], v[92:93], v[112:113]
	v_add_f32_e32 v95, v124, v125
	v_add_f32_e32 v108, v108, v109
	s_waitcnt lgkmcnt(3)
	v_add_f32_e32 v108, v121, v108
	s_waitcnt lgkmcnt(1)
	v_fma_f32 v108, v169, v108, v173
	v_max_f32_e32 v167, 0, v108
	v_mov_b32_e32 v108, v110
	v_mov_b32_e32 v109, v114
	v_pk_mul_f32 v[108:109], v[92:93], v[108:109]
	v_add_f32_e32 v95, v120, v95
	v_add_f32_e32 v108, v108, v109
	v_add_f32_e32 v108, v122, v108
	v_fma_f32 v108, v170, v108, v174
	v_mov_b32_e32 v114, v111
	v_fma_f32 v95, v168, v95, v172
	v_max_f32_e32 v172, 0, v108
	v_pk_mul_f32 v[108:109], v[92:93], v[114:115]
	v_or_b32_e32 v112, 0x1fc50, v94
	v_add_f32_e32 v108, v108, v109
	v_add_f32_e32 v108, v123, v108
	v_fmac_f32_e32 v175, v171, v108
	v_or_b32_e32 v108, 0x1fa50, v94
	ds_read_b128 v[108:111], v108
	ds_read_b128 v[112:115], v112
	v_or_b32_e32 v120, 0x1fe50, v94
	v_or_b32_e32 v125, 0x20050, v94
	ds_read_b128 v[120:123], v120
	ds_read_b128 v[168:171], v125
	s_waitcnt lgkmcnt(4)
	v_mov_b32_e32 v124, v176
	s_waitcnt lgkmcnt(3)
	v_mov_b32_e32 v125, v108
	v_pk_mul_f32 v[124:125], v[92:93], v[124:125]
	v_max_f32_e32 v95, 0, v95
	v_add_f32_e32 v108, v124, v125
	s_waitcnt lgkmcnt(2)
	v_add_f32_e32 v108, v112, v108
	s_waitcnt lgkmcnt(0)
	v_fma_f32 v108, v120, v108, v168
	v_max_f32_e32 v112, 0, v108
	v_mov_b32_e32 v108, v177
	v_pk_mul_f32 v[108:109], v[92:93], v[108:109]
	v_max_f32_e32 v173, 0, v175
	v_add_f32_e32 v108, v108, v109
	v_add_f32_e32 v108, v113, v108
	v_fma_f32 v108, v121, v108, v169
	v_max_f32_e32 v113, 0, v108
	v_mov_b32_e32 v108, v178
	v_mov_b32_e32 v109, v110
	v_pk_mul_f32 v[108:109], v[92:93], v[108:109]
	v_mov_b32_e32 v110, v179
	v_add_f32_e32 v108, v108, v109
	v_add_f32_e32 v108, v114, v108
	v_fma_f32 v108, v122, v108, v170
	v_max_f32_e32 v114, 0, v108
	v_pk_mul_f32 v[108:109], v[92:93], v[110:111]
	v_mfma_f32_32x32x16_f16 v[0:15], v[0:3], v[4:7], 0
	v_mad_i64_i32 v[196:197], s[40:41], s28, v190, v[198:199]
	v_lshlrev_b64 v[196:197], 6, v[196:197]
	v_lshl_add_u64 v[196:197], s[38:39], 0, v[196:197]
	v_lshl_add_u64 v[196:197], v[196:197], 0, v[192:193]
	global_load_dwordx2 v[66:67], v[196:197], off
	global_load_dwordx2 v[64:65], v[196:197], off offset:32
	global_load_dwordx2 v[126:127], v[196:197], off offset:48
	global_load_dwordx2 v[162:163], v[196:197], off offset:16
	v_add_f32_e32 v108, v108, v109
	v_add_f32_e32 v108, v115, v108
	v_fmac_f32_e32 v171, v123, v108
	v_max_f32_e32 v108, 0, v171
	v_cvt_pk_f16_f32 v111, v114, v108
	v_cvt_pk_f16_f32 v110, v112, v113
	v_cvt_pk_f16_f32 v109, v172, v173
	v_cvt_pk_f16_f32 v108, v95, v167
	v_or_b32_e32 v95, 0x1f880, v94
	s_nop 0
	v_mfma_f32_32x32x16_f16 v[32:47], v[100:103], v[108:111], v[32:47]
	v_mad_i64_i32 v[196:197], s[40:41], s26, v190, v[198:199]
	v_lshlrev_b64 v[196:197], 6, v[196:197]
	v_lshl_add_u64 v[196:197], s[38:39], 0, v[196:197]
	v_lshl_add_u64 v[196:197], v[196:197], 0, v[192:193]
	global_load_dwordx2 v[160:161], v[196:197], off
	global_load_dwordx2 v[128:129], v[196:197], off offset:32
	global_load_dwordx2 v[130:131], v[196:197], off offset:48
	global_load_dwordx2 v[158:159], v[196:197], off offset:16
	v_or_b32_e32 v100, 0x1fa80, v94
	v_mfma_f32_32x32x16_f16 v[48:63], v[96:99], v[108:111], v[48:63]
	v_mad_i64_i32 v[196:197], s[40:41], s24, v190, v[198:199]
	v_lshlrev_b64 v[196:197], 6, v[196:197]
	v_lshl_add_u64 v[196:197], s[38:39], 0, v[196:197]
	v_lshl_add_u64 v[196:197], v[196:197], 0, v[192:193]
	global_load_dwordx2 v[156:157], v[196:197], off
	global_load_dwordx2 v[132:133], v[196:197], off offset:32
	global_load_dwordx2 v[134:135], v[196:197], off offset:48
	global_load_dwordx2 v[154:155], v[196:197], off offset:16
	ds_read_b128 v[96:99], v95
	ds_read_b128 v[100:103], v100
	v_or_b32_e32 v95, 0x1fc80, v94
	v_mfma_f32_32x32x16_f16 v[16:31], v[104:107], v[108:111], v[16:31]
	v_mad_i64_i32 v[196:197], s[40:41], s10, v190, v[198:199]
	v_mad_i64_i32 v[198:199], s[40:41], s2, v190, v[198:199]
	v_lshlrev_b64 v[196:197], 6, v[196:197]
	v_lshlrev_b64 v[198:199], 6, v[198:199]
	v_lshl_add_u64 v[196:197], s[38:39], 0, v[196:197]
	v_lshl_add_u64 v[198:199], s[38:39], 0, v[198:199]
	v_lshl_add_u64 v[196:197], v[196:197], 0, v[192:193]
	v_lshl_add_u64 v[198:199], v[198:199], 0, v[192:193]
	global_load_dwordx2 v[152:153], v[196:197], off
	global_load_dwordx2 v[136:137], v[196:197], off offset:32
	global_load_dwordx2 v[138:139], v[196:197], off offset:48
	global_load_dwordx2 v[150:151], v[196:197], off offset:16
	global_load_dwordx2 v[148:149], v[198:199], off
	global_load_dwordx2 v[140:141], v[198:199], off offset:32
	global_load_dwordx2 v[142:143], v[198:199], off offset:48
	global_load_dwordx2 v[146:147], v[198:199], off offset:16
	s_waitcnt lgkmcnt(1)
	v_mov_b32_e32 v104, v96
	s_waitcnt lgkmcnt(0)
	v_mov_b32_e32 v105, v100
	v_or_b32_e32 v96, 0x1fe80, v94
	v_mov_b32_e32 v100, v97
	v_mfma_f32_32x32x16_f16 v[0:15], v[116:119], v[108:111], v[0:15]
	v_mul_f32_e64 v116, v92, v104
	v_mul_f32_e64 v117, v93, v105
	ds_read_b128 v[104:107], v95
	ds_read_b128 v[108:111], v96
	v_or_b32_e32 v95, 0x20080, v94
	ds_read_b128 v[112:115], v95
	v_or_b32_e32 v96, 0x1f890, v94
	v_add_f32_e32 v95, v116, v117
	ds_read_b128 v[116:119], v96
	v_pk_mul_f32 v[96:97], v[92:93], v[100:101]
	v_or_b32_e32 v100, 0x1fc90, v94
	v_add_f32_e32 v96, v96, v97
	s_waitcnt lgkmcnt(3)
	v_add_f32_e32 v96, v105, v96
	s_waitcnt lgkmcnt(1)
	v_fma_f32 v96, v109, v96, v113
	v_max_f32_e32 v120, 0, v96
	v_mov_b32_e32 v96, v98
	v_mov_b32_e32 v97, v102
	v_pk_mul_f32 v[96:97], v[92:93], v[96:97]
	v_mov_b32_e32 v102, v99
	v_add_f32_e32 v96, v96, v97
	v_add_f32_e32 v96, v106, v96
	v_fma_f32 v96, v110, v96, v114
	v_max_f32_e32 v114, 0, v96
	v_pk_mul_f32 v[96:97], v[92:93], v[102:103]
	v_add_f32_e32 v95, v104, v95
	v_add_f32_e32 v96, v96, v97
	v_add_f32_e32 v96, v107, v96
	v_fmac_f32_e32 v115, v111, v96
	v_or_b32_e32 v96, 0x1fa90, v94
	ds_read_b128 v[96:99], v96
	ds_read_b128 v[100:103], v100
	v_fma_f32 v95, v108, v95, v112
	v_or_b32_e32 v104, 0x1fe90, v94
	v_or_b32_e32 v108, 0x20090, v94
	ds_read_b128 v[104:107], v104
	ds_read_b128 v[108:111], v108
	s_waitcnt lgkmcnt(4)
	v_mov_b32_e32 v112, v116
	s_waitcnt lgkmcnt(3)
	v_mov_b32_e32 v113, v96
	v_pk_mul_f32 v[112:113], v[92:93], v[112:113]
	v_max_f32_e32 v95, 0, v95
	v_add_f32_e32 v96, v112, v113
	s_waitcnt lgkmcnt(2)
	v_add_f32_e32 v96, v100, v96
	s_waitcnt lgkmcnt(0)
	v_fma_f32 v96, v104, v96, v108
	v_max_f32_e32 v100, 0, v96
	v_mov_b32_e32 v96, v117
	v_pk_mul_f32 v[96:97], v[92:93], v[96:97]
	v_max_f32_e32 v115, 0, v115
	v_add_f32_e32 v96, v96, v97
	v_add_f32_e32 v96, v101, v96
	v_fma_f32 v96, v105, v96, v109
	v_max_f32_e32 v101, 0, v96
	v_mov_b32_e32 v96, v118
	v_mov_b32_e32 v97, v98
	v_pk_mul_f32 v[96:97], v[92:93], v[96:97]
	v_mov_b32_e32 v98, v119
	v_add_f32_e32 v96, v96, v97
	v_add_f32_e32 v96, v102, v96
	v_fma_f32 v96, v106, v96, v110
	v_max_f32_e32 v102, 0, v96
	v_pk_mul_f32 v[96:97], v[92:93], v[98:99]
	s_nop 0
	v_add_f32_e32 v104, v96, v97
	ds_read_b128 v[96:99], v166 offset:64
	v_add_f32_e32 v103, v103, v104
	v_fmac_f32_e32 v111, v107, v103
	v_max_f32_e32 v103, 0, v111
	v_cvt_pk_f16_f32 v103, v102, v103
	v_cvt_pk_f16_f32 v102, v100, v101
	v_cvt_pk_f16_f32 v101, v114, v115
	v_cvt_pk_f16_f32 v100, v95, v120
	ds_read_b128 v[104:107], v166 offset:96
	v_or_b32_e32 v95, 0x1f8c0, v94
	s_waitcnt lgkmcnt(1)
	v_mfma_f32_32x32x16_f16 v[48:63], v[96:99], v[100:103], v[48:63]
	ds_read_b128 v[96:99], v166 offset:8768
	ds_read_b128 v[108:111], v166 offset:8800
	v_or_b32_e32 v120, 0x1fac0, v94
	s_waitcnt lgkmcnt(1)
	v_mfma_f32_32x32x16_f16 v[32:47], v[96:99], v[100:103], v[32:47]
	ds_read_b128 v[96:99], v166 offset:17472
	ds_read_b128 v[112:115], v166 offset:17504
	s_waitcnt lgkmcnt(1)
	v_mfma_f32_32x32x16_f16 v[16:31], v[96:99], v[100:103], v[16:31]
	ds_read_b128 v[96:99], v166 offset:26176
	ds_read_b128 v[116:119], v95
	ds_read_b128 v[120:123], v120
	ds_read_b128 v[168:171], v166 offset:26208
	v_or_b32_e32 v95, 0x1fcc0, v94
	s_waitcnt lgkmcnt(3)
	v_mfma_f32_32x32x16_f16 v[0:15], v[96:99], v[100:103], v[0:15]
	s_waitcnt lgkmcnt(2)
	v_mov_b32_e32 v96, v116
	s_waitcnt lgkmcnt(1)
	v_mov_b32_e32 v97, v120
	v_or_b32_e32 v100, 0x1fec0, v94
	v_pk_mul_f32 v[124:125], v[92:93], v[96:97]
	ds_read_b128 v[96:99], v95
	ds_read_b128 v[100:103], v100
	v_or_b32_e32 v95, 0x200c0, v94
	ds_read_b128 v[172:175], v95
	v_add_f32_e32 v95, v124, v125
	v_mov_b32_e32 v120, v117
	s_waitcnt lgkmcnt(2)
	v_add_f32_e32 v95, v96, v95
	v_or_b32_e32 v96, 0x1f8d0, v94
	v_pk_mul_f32 v[116:117], v[92:93], v[120:121]
	ds_read_b128 v[176:179], v96
	v_add_f32_e32 v96, v116, v117
	v_add_f32_e32 v96, v97, v96
	s_waitcnt lgkmcnt(1)
	v_fma_f32 v96, v101, v96, v173
	v_max_f32_e32 v167, 0, v96
	v_mov_b32_e32 v96, v118
	v_mov_b32_e32 v97, v122
	v_pk_mul_f32 v[96:97], v[92:93], v[96:97]
	v_mov_b32_e32 v122, v119
	v_add_f32_e32 v96, v96, v97
	v_add_f32_e32 v96, v98, v96
	v_fma_f32 v96, v102, v96, v174
	v_fma_f32 v95, v100, v95, v172
	v_max_f32_e32 v172, 0, v96
	v_pk_mul_f32 v[96:97], v[92:93], v[122:123]
	v_or_b32_e32 v100, 0x1fcd0, v94
	v_add_f32_e32 v96, v96, v97
	v_add_f32_e32 v96, v99, v96
	v_fmac_f32_e32 v175, v103, v96
	v_or_b32_e32 v96, 0x1fad0, v94
	ds_read_b128 v[96:99], v96
	ds_read_b128 v[100:103], v100
	v_or_b32_e32 v116, 0x1fed0, v94
	v_or_b32_e32 v120, 0x200d0, v94
	ds_read_b128 v[116:119], v116
	ds_read_b128 v[120:123], v120
	s_waitcnt lgkmcnt(4)
	v_mov_b32_e32 v124, v176
	s_waitcnt lgkmcnt(3)
	v_mov_b32_e32 v125, v96
	v_pk_mul_f32 v[124:125], v[92:93], v[124:125]
	v_max_f32_e32 v95, 0, v95
	v_add_f32_e32 v96, v124, v125
	s_waitcnt lgkmcnt(2)
	v_add_f32_e32 v96, v100, v96
	s_waitcnt lgkmcnt(0)
	v_fma_f32 v96, v116, v96, v120
	v_max_f32_e32 v100, 0, v96
	v_mov_b32_e32 v96, v177
	v_pk_mul_f32 v[96:97], v[92:93], v[96:97]
	v_max_f32_e32 v173, 0, v175
	v_add_f32_e32 v96, v96, v97
	v_add_f32_e32 v96, v101, v96
	v_fma_f32 v96, v117, v96, v121
	v_max_f32_e32 v101, 0, v96
	v_mov_b32_e32 v96, v178
	v_mov_b32_e32 v97, v98
	v_pk_mul_f32 v[96:97], v[92:93], v[96:97]
	v_mov_b32_e32 v98, v179
	v_add_f32_e32 v96, v96, v97
	v_add_f32_e32 v96, v102, v96
	v_fma_f32 v96, v118, v96, v122
	v_max_f32_e32 v102, 0, v96
	v_pk_mul_f32 v[96:97], v[92:93], v[98:99]
	v_cvt_pk_f16_f32 v98, v100, v101
	v_add_f32_e32 v96, v96, v97
	v_add_f32_e32 v96, v103, v96
	v_fmac_f32_e32 v123, v119, v96
	v_max_f32_e32 v96, 0, v123
	v_cvt_pk_f16_f32 v99, v102, v96
	v_cvt_pk_f16_f32 v97, v172, v173
	v_cvt_pk_f16_f32 v96, v95, v167
	v_or_b32_e32 v95, 0x1f900, v94
	s_nop 0
	v_mfma_f32_32x32x16_f16 v[48:63], v[104:107], v[96:99], v[48:63]
	v_or_b32_e32 v104, 0x1fb00, v94
	ds_read_b128 v[100:103], v95
	ds_read_b128 v[104:107], v104
	v_or_b32_e32 v95, 0x1fd00, v94
	v_mfma_f32_32x32x16_f16 v[32:47], v[108:111], v[96:99], v[32:47]
	v_mfma_f32_32x32x16_f16 v[16:31], v[112:115], v[96:99], v[16:31]
	v_mfma_f32_32x32x16_f16 v[0:15], v[168:171], v[96:99], v[0:15]
	s_waitcnt lgkmcnt(1)
	v_mov_b32_e32 v96, v100
	s_waitcnt lgkmcnt(0)
	v_mov_b32_e32 v97, v104
	v_mul_f32_e64 v116, v92, v96
	v_mul_f32_e64 v117, v93, v97
	v_or_b32_e32 v100, 0x1ff00, v94
	ds_read_b128 v[96:99], v95
	ds_read_b128 v[108:111], v100
	v_or_b32_e32 v95, 0x20100, v94
	ds_read_b128 v[112:115], v95
	v_add_f32_e32 v95, v116, v117
	v_mov_b32_e32 v104, v101
	s_waitcnt lgkmcnt(2)
	v_add_f32_e32 v95, v96, v95
	v_or_b32_e32 v96, 0x1f910, v94
	v_pk_mul_f32 v[100:101], v[92:93], v[104:105]
	ds_read_b128 v[116:119], v96
	v_add_f32_e32 v96, v100, v101
	v_add_f32_e32 v96, v97, v96
	s_waitcnt lgkmcnt(1)
	v_fma_f32 v96, v109, v96, v113
	v_max_f32_e32 v120, 0, v96
	v_mov_b32_e32 v96, v102
	v_mov_b32_e32 v97, v106
	v_pk_mul_f32 v[96:97], v[92:93], v[96:97]
	v_mov_b32_e32 v106, v103
	v_add_f32_e32 v96, v96, v97
	v_add_f32_e32 v96, v98, v96
	v_fma_f32 v96, v110, v96, v114
	v_max_f32_e32 v114, 0, v96
	v_pk_mul_f32 v[96:97], v[92:93], v[106:107]
	v_or_b32_e32 v100, 0x1fd10, v94
	v_add_f32_e32 v96, v96, v97
	v_add_f32_e32 v96, v99, v96
	v_fmac_f32_e32 v115, v111, v96
	v_or_b32_e32 v96, 0x1fb10, v94
	ds_read_b128 v[96:99], v96
	ds_read_b128 v[100:103], v100
	v_fma_f32 v95, v108, v95, v112
	v_or_b32_e32 v104, 0x1ff10, v94
	v_or_b32_e32 v108, 0x20110, v94
	ds_read_b128 v[104:107], v104
	ds_read_b128 v[108:111], v108
	s_waitcnt lgkmcnt(4)
	v_mov_b32_e32 v112, v116
	s_waitcnt lgkmcnt(3)
	v_mov_b32_e32 v113, v96
	v_pk_mul_f32 v[112:113], v[92:93], v[112:113]
	v_max_f32_e32 v95, 0, v95
	v_add_f32_e32 v96, v112, v113
	s_waitcnt lgkmcnt(2)
	v_add_f32_e32 v96, v100, v96
	s_waitcnt lgkmcnt(0)
	v_fma_f32 v96, v104, v96, v108
	v_max_f32_e32 v100, 0, v96
	v_mov_b32_e32 v96, v117
	v_pk_mul_f32 v[96:97], v[92:93], v[96:97]
	v_max_f32_e32 v115, 0, v115
	v_add_f32_e32 v96, v96, v97
	v_add_f32_e32 v96, v101, v96
	v_fma_f32 v96, v105, v96, v109
	v_max_f32_e32 v101, 0, v96
	v_mov_b32_e32 v96, v118
	v_mov_b32_e32 v97, v98
	v_pk_mul_f32 v[96:97], v[92:93], v[96:97]
	v_mov_b32_e32 v98, v119
	v_add_f32_e32 v96, v96, v97
	v_add_f32_e32 v96, v102, v96
	v_fma_f32 v96, v106, v96, v110
	v_max_f32_e32 v102, 0, v96
	v_pk_mul_f32 v[96:97], v[92:93], v[98:99]
	s_nop 0
	v_add_f32_e32 v104, v96, v97
	ds_read_b128 v[96:99], v166 offset:128
	v_add_f32_e32 v103, v103, v104
	v_fmac_f32_e32 v111, v107, v103
	v_max_f32_e32 v103, 0, v111
	v_cvt_pk_f16_f32 v103, v102, v103
	v_cvt_pk_f16_f32 v102, v100, v101
	v_cvt_pk_f16_f32 v101, v114, v115
	v_cvt_pk_f16_f32 v100, v95, v120
	ds_read_b128 v[104:107], v166 offset:160
	v_or_b32_e32 v95, 0x1f940, v94
	s_waitcnt lgkmcnt(1)
	v_mfma_f32_32x32x16_f16 v[48:63], v[96:99], v[100:103], v[48:63]
	ds_read_b128 v[96:99], v166 offset:8832
	ds_read_b128 v[108:111], v166 offset:8864
	v_or_b32_e32 v120, 0x1fb40, v94
	s_waitcnt lgkmcnt(1)
	v_mfma_f32_32x32x16_f16 v[32:47], v[96:99], v[100:103], v[32:47]
	ds_read_b128 v[96:99], v166 offset:17536
	ds_read_b128 v[112:115], v166 offset:17568
	s_waitcnt lgkmcnt(1)
	v_mfma_f32_32x32x16_f16 v[16:31], v[96:99], v[100:103], v[16:31]
	ds_read_b128 v[96:99], v166 offset:26240
	ds_read_b128 v[116:119], v95
	ds_read_b128 v[120:123], v120
	ds_read_b128 v[168:171], v166 offset:26272
	v_or_b32_e32 v95, 0x1fd40, v94
	s_waitcnt lgkmcnt(3)
	v_mfma_f32_32x32x16_f16 v[0:15], v[96:99], v[100:103], v[0:15]
	s_waitcnt lgkmcnt(2)
	v_mov_b32_e32 v96, v116
	s_waitcnt lgkmcnt(1)
	v_mov_b32_e32 v97, v120
	v_or_b32_e32 v100, 0x1ff40, v94
	v_pk_mul_f32 v[124:125], v[92:93], v[96:97]
	ds_read_b128 v[96:99], v95
	ds_read_b128 v[100:103], v100
	v_or_b32_e32 v95, 0x20140, v94
	ds_read_b128 v[172:175], v95
	v_add_f32_e32 v95, v124, v125
	v_mov_b32_e32 v120, v117
	s_waitcnt lgkmcnt(2)
	v_add_f32_e32 v95, v96, v95
	v_or_b32_e32 v96, 0x1f950, v94
	v_pk_mul_f32 v[116:117], v[92:93], v[120:121]
	ds_read_b128 v[176:179], v96
	v_add_f32_e32 v96, v116, v117
	v_add_f32_e32 v96, v97, v96
	s_waitcnt lgkmcnt(1)
	v_fma_f32 v96, v101, v96, v173
	v_max_f32_e32 v167, 0, v96
	v_mov_b32_e32 v96, v118
	v_mov_b32_e32 v97, v122
	v_pk_mul_f32 v[96:97], v[92:93], v[96:97]
	v_mov_b32_e32 v122, v119
	v_add_f32_e32 v96, v96, v97
	v_add_f32_e32 v96, v98, v96
	v_fma_f32 v96, v102, v96, v174
	v_fma_f32 v95, v100, v95, v172
	v_max_f32_e32 v172, 0, v96
	v_pk_mul_f32 v[96:97], v[92:93], v[122:123]
	v_or_b32_e32 v100, 0x1fd50, v94
	v_add_f32_e32 v96, v96, v97
	v_add_f32_e32 v96, v99, v96
	v_fmac_f32_e32 v175, v103, v96
	v_or_b32_e32 v96, 0x1fb50, v94
	ds_read_b128 v[96:99], v96
	ds_read_b128 v[100:103], v100
	v_or_b32_e32 v116, 0x1ff50, v94
	v_or_b32_e32 v120, 0x20150, v94
	ds_read_b128 v[116:119], v116
	ds_read_b128 v[120:123], v120
	s_waitcnt lgkmcnt(4)
	v_mov_b32_e32 v124, v176
	s_waitcnt lgkmcnt(3)
	v_mov_b32_e32 v125, v96
	v_pk_mul_f32 v[124:125], v[92:93], v[124:125]
	v_max_f32_e32 v95, 0, v95
	v_add_f32_e32 v96, v124, v125
	s_waitcnt lgkmcnt(2)
	v_add_f32_e32 v96, v100, v96
	s_waitcnt lgkmcnt(0)
	v_fma_f32 v96, v116, v96, v120
	v_max_f32_e32 v100, 0, v96
	v_mov_b32_e32 v96, v177
	v_pk_mul_f32 v[96:97], v[92:93], v[96:97]
	v_max_f32_e32 v173, 0, v175
	v_add_f32_e32 v96, v96, v97
	v_add_f32_e32 v96, v101, v96
	v_fma_f32 v96, v117, v96, v121
	v_max_f32_e32 v101, 0, v96
	v_mov_b32_e32 v96, v178
	v_mov_b32_e32 v97, v98
	v_pk_mul_f32 v[96:97], v[92:93], v[96:97]
	v_mov_b32_e32 v98, v179
	v_add_f32_e32 v96, v96, v97
	v_add_f32_e32 v96, v102, v96
	v_fma_f32 v96, v118, v96, v122
	v_max_f32_e32 v102, 0, v96
	v_pk_mul_f32 v[96:97], v[92:93], v[98:99]
	v_cvt_pk_f16_f32 v98, v100, v101
	v_add_f32_e32 v96, v96, v97
	v_add_f32_e32 v96, v103, v96
	v_fmac_f32_e32 v123, v119, v96
	v_max_f32_e32 v96, 0, v123
	v_cvt_pk_f16_f32 v99, v102, v96
	v_cvt_pk_f16_f32 v97, v172, v173
	v_cvt_pk_f16_f32 v96, v95, v167
	v_or_b32_e32 v95, 0x1f980, v94
	s_nop 0
	v_mfma_f32_32x32x16_f16 v[48:63], v[104:107], v[96:99], v[48:63]
	v_or_b32_e32 v104, 0x1fb80, v94
	ds_read_b128 v[100:103], v95
	ds_read_b128 v[104:107], v104
	v_or_b32_e32 v95, 0x1fd80, v94
	v_mfma_f32_32x32x16_f16 v[32:47], v[108:111], v[96:99], v[32:47]
	v_mfma_f32_32x32x16_f16 v[16:31], v[112:115], v[96:99], v[16:31]
	v_mfma_f32_32x32x16_f16 v[0:15], v[168:171], v[96:99], v[0:15]
	s_waitcnt lgkmcnt(1)
	v_mov_b32_e32 v96, v100
	s_waitcnt lgkmcnt(0)
	v_mov_b32_e32 v97, v104
	v_mul_f32_e64 v116, v92, v96
	v_mul_f32_e64 v117, v93, v97
	v_or_b32_e32 v100, 0x1ff80, v94
	ds_read_b128 v[96:99], v95
	ds_read_b128 v[108:111], v100
	v_or_b32_e32 v95, 0x20180, v94
	ds_read_b128 v[112:115], v95
	v_add_f32_e32 v95, v116, v117
	v_mov_b32_e32 v104, v101
	s_waitcnt lgkmcnt(2)
	v_add_f32_e32 v95, v96, v95
	v_or_b32_e32 v96, 0x1f990, v94
	v_pk_mul_f32 v[100:101], v[92:93], v[104:105]
	ds_read_b128 v[116:119], v96
	v_add_f32_e32 v96, v100, v101
	v_add_f32_e32 v96, v97, v96
	s_waitcnt lgkmcnt(1)
	v_fma_f32 v96, v109, v96, v113
	v_max_f32_e32 v120, 0, v96
	v_mov_b32_e32 v96, v102
	v_mov_b32_e32 v97, v106
	v_pk_mul_f32 v[96:97], v[92:93], v[96:97]
	v_mov_b32_e32 v106, v103
	v_add_f32_e32 v96, v96, v97
	v_add_f32_e32 v96, v98, v96
	v_fma_f32 v96, v110, v96, v114
	v_max_f32_e32 v114, 0, v96
	v_pk_mul_f32 v[96:97], v[92:93], v[106:107]
	v_or_b32_e32 v100, 0x1fd90, v94
	v_add_f32_e32 v96, v96, v97
	v_add_f32_e32 v96, v99, v96
	v_fmac_f32_e32 v115, v111, v96
	v_or_b32_e32 v96, 0x1fb90, v94
	ds_read_b128 v[96:99], v96
	ds_read_b128 v[100:103], v100
	v_fma_f32 v95, v108, v95, v112
	v_or_b32_e32 v104, 0x1ff90, v94
	v_or_b32_e32 v108, 0x20190, v94
	ds_read_b128 v[104:107], v104
	ds_read_b128 v[108:111], v108
	s_waitcnt lgkmcnt(4)
	v_mov_b32_e32 v112, v116
	s_waitcnt lgkmcnt(3)
	v_mov_b32_e32 v113, v96
	v_pk_mul_f32 v[112:113], v[92:93], v[112:113]
	v_max_f32_e32 v95, 0, v95
	v_add_f32_e32 v96, v112, v113
	s_waitcnt lgkmcnt(2)
	v_add_f32_e32 v96, v100, v96
	s_waitcnt lgkmcnt(0)
	v_fma_f32 v96, v104, v96, v108
	v_max_f32_e32 v100, 0, v96
	v_mov_b32_e32 v96, v117
	v_pk_mul_f32 v[96:97], v[92:93], v[96:97]
	v_max_f32_e32 v115, 0, v115
	v_add_f32_e32 v96, v96, v97
	v_add_f32_e32 v96, v101, v96
	v_fma_f32 v96, v105, v96, v109
	v_max_f32_e32 v101, 0, v96
	v_mov_b32_e32 v96, v118
	v_mov_b32_e32 v97, v98
	v_pk_mul_f32 v[96:97], v[92:93], v[96:97]
	v_mov_b32_e32 v98, v119
	v_add_f32_e32 v96, v96, v97
	v_add_f32_e32 v96, v102, v96
	v_fma_f32 v96, v106, v96, v110
	v_max_f32_e32 v102, 0, v96
	v_pk_mul_f32 v[96:97], v[92:93], v[98:99]
	s_nop 0
	v_add_f32_e32 v104, v96, v97
	ds_read_b128 v[96:99], v166 offset:192
	v_add_f32_e32 v103, v103, v104
	v_fmac_f32_e32 v111, v107, v103
	v_max_f32_e32 v103, 0, v111
	v_cvt_pk_f16_f32 v103, v102, v103
	v_cvt_pk_f16_f32 v102, v100, v101
	v_cvt_pk_f16_f32 v101, v114, v115
	v_cvt_pk_f16_f32 v100, v95, v120
	ds_read_b128 v[104:107], v166 offset:224
	v_or_b32_e32 v95, 0x1f9c0, v94
	s_waitcnt lgkmcnt(1)
	v_mfma_f32_32x32x16_f16 v[48:63], v[96:99], v[100:103], v[48:63]
	ds_read_b128 v[96:99], v166 offset:8896
	ds_read_b128 v[108:111], v166 offset:8928
	v_or_b32_e32 v120, 0x1fbc0, v94
	s_waitcnt lgkmcnt(1)
	v_mfma_f32_32x32x16_f16 v[32:47], v[96:99], v[100:103], v[32:47]
	ds_read_b128 v[96:99], v166 offset:17600
	ds_read_b128 v[112:115], v166 offset:17632
	s_waitcnt lgkmcnt(1)
	v_mfma_f32_32x32x16_f16 v[16:31], v[96:99], v[100:103], v[16:31]
	ds_read_b128 v[96:99], v166 offset:26304
	ds_read_b128 v[116:119], v95
	ds_read_b128 v[120:123], v120
	ds_read_b128 v[168:171], v166 offset:26336
	v_or_b32_e32 v95, 0x1fdc0, v94
	s_waitcnt lgkmcnt(3)
	v_mfma_f32_32x32x16_f16 v[0:15], v[96:99], v[100:103], v[0:15]
	s_waitcnt lgkmcnt(2)
	v_mov_b32_e32 v96, v116
	s_waitcnt lgkmcnt(1)
	v_mov_b32_e32 v97, v120
	v_or_b32_e32 v100, 0x1ffc0, v94
	v_pk_mul_f32 v[124:125], v[92:93], v[96:97]
	ds_read_b128 v[96:99], v95
	ds_read_b128 v[100:103], v100
	v_or_b32_e32 v95, 0x201c0, v94
	ds_read_b128 v[172:175], v95
	v_add_f32_e32 v95, v124, v125
	s_waitcnt lgkmcnt(2)
	v_add_f32_e32 v95, v96, v95
	v_mov_b32_e32 v120, v117
	v_pk_mul_f32 v[116:117], v[92:93], v[120:121]
	s_waitcnt lgkmcnt(0)
	v_fma_f32 v95, v100, v95, v172
	v_or_b32_e32 v96, 0x1f9d0, v94
	v_max_f32_e32 v167, 0, v95
	v_add_f32_e32 v95, v116, v117
	ds_read_b128 v[176:179], v96
	v_add_f32_e32 v95, v97, v95
	v_mov_b32_e32 v96, v118
	v_mov_b32_e32 v97, v122
	v_fma_f32 v95, v101, v95, v173
	v_pk_mul_f32 v[96:97], v[92:93], v[96:97]
	v_max_f32_e32 v172, 0, v95
	v_add_f32_e32 v95, v96, v97
	v_add_f32_e32 v95, v98, v95
	v_mov_b32_e32 v122, v119
	v_fma_f32 v95, v102, v95, v174
	v_pk_mul_f32 v[96:97], v[92:93], v[122:123]
	v_max_f32_e32 v173, 0, v95
	v_add_f32_e32 v95, v96, v97
	v_add_f32_e32 v95, v99, v95
	v_fmac_f32_e32 v175, v103, v95
	v_or_b32_e32 v95, 0x1fbd0, v94
	v_or_b32_e32 v100, 0x1fdd0, v94
	ds_read_b128 v[96:99], v95
	ds_read_b128 v[100:103], v100
	v_or_b32_e32 v95, 0x1ffd0, v94
	v_or_b32_e32 v94, 0x201d0, v94
	ds_read_b128 v[116:119], v95
	ds_read_b128 v[120:123], v94
	s_waitcnt lgkmcnt(4)
	v_mov_b32_e32 v124, v176
	s_waitcnt lgkmcnt(3)
	v_mov_b32_e32 v125, v96
	v_pk_mul_f32 v[94:95], v[92:93], v[124:125]
	v_mov_b32_e32 v96, v177
	v_add_f32_e32 v94, v94, v95
	s_waitcnt lgkmcnt(2)
	v_add_f32_e32 v94, v100, v94
	s_waitcnt lgkmcnt(0)
	v_fma_f32 v94, v116, v94, v120
	v_max_f32_e32 v100, 0, v94
	v_pk_mul_f32 v[94:95], v[92:93], v[96:97]
	v_max_f32_e32 v174, 0, v175
	v_add_f32_e32 v94, v94, v95
	v_add_f32_e32 v94, v101, v94
	v_fma_f32 v94, v117, v94, v121
	v_max_f32_e32 v96, 0, v94
	v_mov_b32_e32 v94, v178
	v_mov_b32_e32 v95, v98
	v_mov_b32_e32 v98, v179
	v_pk_mul_f32 v[94:95], v[92:93], v[94:95]
	v_pk_mul_f32 v[92:93], v[92:93], v[98:99]
	v_add_f32_e32 v94, v94, v95
	v_add_f32_e32 v92, v92, v93
	v_add_f32_e32 v94, v102, v94
	v_add_f32_e32 v92, v103, v92
	v_fma_f32 v94, v118, v94, v122
	v_fmac_f32_e32 v123, v119, v92
	v_max_f32_e32 v94, 0, v94
	v_max_f32_e32 v92, 0, v123
	v_cvt_pk_f16_f32 v95, v94, v92
	v_cvt_pk_f16_f32 v94, v100, v96
	v_cvt_pk_f16_f32 v93, v173, v174
	v_cvt_pk_f16_f32 v92, v167, v172
	s_waitcnt vmcnt(0)
	v_cvt_f32_f16_sdwa v183, v163 dst_sel:DWORD dst_unused:UNUSED_PAD src0_sel:WORD_1
	v_cvt_f32_f16_e32 v182, v163
	v_cvt_f32_f16_sdwa v163, v127 dst_sel:DWORD dst_unused:UNUSED_PAD src0_sel:WORD_1
	v_cvt_f32_f16_sdwa v97, v90 dst_sel:DWORD dst_unused:UNUSED_PAD src0_sel:WORD_1
	v_cvt_f32_f16_e32 v96, v90
	v_mfma_f32_32x32x16_f16 v[48:63], v[104:107], v[92:95], v[48:63]
	v_cvt_f32_f16_sdwa v99, v88 dst_sel:DWORD dst_unused:UNUSED_PAD src0_sel:WORD_1
	v_cvt_f32_f16_e32 v98, v88
	v_or_b32_e32 v88, 0x21600, v165
	v_cvt_f32_f16_sdwa v101, v89 dst_sel:DWORD dst_unused:UNUSED_PAD src0_sel:WORD_1
	v_cvt_f32_f16_e32 v100, v89
	v_pk_fma_f32 v[96:97], v[98:99], s[4:5], v[96:97] op_sel_hi:[1,0,1]
	v_cvt_f32_f16_sdwa v99, v91 dst_sel:DWORD dst_unused:UNUSED_PAD src0_sel:WORD_1
	v_mfma_f32_32x32x16_f16 v[32:47], v[108:111], v[92:95], v[32:47]
	v_cvt_f32_f16_e32 v98, v91
	v_mfma_f32_32x32x16_f16 v[16:31], v[112:115], v[92:95], v[16:31]
	v_mfma_f32_32x32x16_f16 v[0:15], v[168:171], v[92:95], v[0:15]
	ds_read_b128 v[92:95], v88
	v_or_b32_e32 v88, 0x21620, v165
	ds_read_b128 v[88:91], v88
	s_waitcnt lgkmcnt(1)
	v_add_f32_e64 v48, v48, v92
	v_add_f32_e64 v49, v49, v93
	v_pk_add_f32 v[48:49], v[96:97], v[48:49]
	v_cvt_f32_f16_sdwa v93, v86 dst_sel:DWORD dst_unused:UNUSED_PAD src0_sel:WORD_1
	v_cvt_f32_f16_e32 v92, v86
	v_cvt_f32_f16_sdwa v97, v84 dst_sel:DWORD dst_unused:UNUSED_PAD src0_sel:WORD_1
	v_cvt_f32_f16_e32 v96, v84
	v_cvt_pk_f16_f32 v112, v48, v49
	v_pk_fma_f32 v[48:49], v[100:101], s[4:5], v[98:99] op_sel_hi:[1,0,1]
	v_pk_add_f32 v[50:51], v[50:51], v[94:95]
	v_cvt_f32_f16_e32 v86, v85
	v_pk_add_f32 v[48:49], v[48:49], v[50:51]
	v_cvt_f32_f16_sdwa v51, v87 dst_sel:DWORD dst_unused:UNUSED_PAD src0_sel:WORD_1
	v_cvt_f32_f16_e32 v50, v87
	v_cvt_f32_f16_sdwa v87, v85 dst_sel:DWORD dst_unused:UNUSED_PAD src0_sel:WORD_1
	v_cvt_pk_f16_f32 v113, v48, v49
	v_pk_fma_f32 v[48:49], v[96:97], s[4:5], v[92:93] op_sel_hi:[1,0,1]
	s_waitcnt lgkmcnt(0)
	v_pk_add_f32 v[52:53], v[52:53], v[88:89]
	s_nop 0
	v_pk_add_f32 v[48:49], v[48:49], v[52:53]
	v_cvt_f32_f16_sdwa v53, v82 dst_sel:DWORD dst_unused:UNUSED_PAD src0_sel:WORD_1
	v_cvt_pk_f16_f32 v114, v48, v49
	v_pk_fma_f32 v[48:49], v[86:87], s[4:5], v[50:51] op_sel_hi:[1,0,1]
	v_pk_add_f32 v[50:51], v[54:55], v[90:91]
	v_cvt_f32_f16_e32 v52, v82
	v_pk_add_f32 v[48:49], v[48:49], v[50:51]
	v_cvt_f32_f16_sdwa v55, v80 dst_sel:DWORD dst_unused:UNUSED_PAD src0_sel:WORD_1
	v_cvt_pk_f16_f32 v115, v48, v49
	v_or_b32_e32 v48, 0x21640, v165
	v_cvt_f32_f16_e32 v54, v80
	ds_read_b128 v[48:51], v48
	v_cvt_f32_f16_sdwa v87, v83 dst_sel:DWORD dst_unused:UNUSED_PAD src0_sel:WORD_1
	v_cvt_f32_f16_e32 v86, v83
	v_cvt_f32_f16_sdwa v83, v81 dst_sel:DWORD dst_unused:UNUSED_PAD src0_sel:WORD_1
	v_cvt_f32_f16_e32 v82, v81
	v_pk_fma_f32 v[84:85], v[54:55], s[4:5], v[52:53] op_sel_hi:[1,0,1]
	v_or_b32_e32 v52, 0x21660, v165
	ds_read_b128 v[52:55], v52
	s_waitcnt lgkmcnt(1)
	v_pk_add_f32 v[48:49], v[56:57], v[48:49]
	v_cvt_f32_f16_sdwa v57, v78 dst_sel:DWORD dst_unused:UNUSED_PAD src0_sel:WORD_1
	v_cvt_f32_f16_e32 v56, v78
	v_cvt_f32_f16_sdwa v81, v76 dst_sel:DWORD dst_unused:UNUSED_PAD src0_sel:WORD_1
	v_cvt_f32_f16_e32 v80, v76
	v_pk_add_f32 v[48:49], v[84:85], v[48:49]
	v_pk_add_f32 v[50:51], v[58:59], v[50:51]
	v_cvt_pk_f16_f32 v116, v48, v49
	v_pk_fma_f32 v[48:49], v[82:83], s[4:5], v[86:87] op_sel_hi:[1,0,1]
	s_waitcnt lgkmcnt(0)
	v_pk_add_f32 v[52:53], v[60:61], v[52:53]
	v_pk_add_f32 v[48:49], v[48:49], v[50:51]
	v_cvt_f32_f16_sdwa v51, v79 dst_sel:DWORD dst_unused:UNUSED_PAD src0_sel:WORD_1
	v_cvt_pk_f16_f32 v117, v48, v49
	v_pk_fma_f32 v[48:49], v[80:81], s[4:5], v[56:57] op_sel_hi:[1,0,1]
	v_cvt_f32_f16_e32 v50, v79
	v_cvt_f32_f16_sdwa v57, v77 dst_sel:DWORD dst_unused:UNUSED_PAD src0_sel:WORD_1
	v_cvt_f32_f16_e32 v56, v77
	v_pk_add_f32 v[48:49], v[48:49], v[52:53]
	v_cvt_f32_f16_sdwa v53, v74 dst_sel:DWORD dst_unused:UNUSED_PAD src0_sel:WORD_1
	v_cvt_pk_f16_f32 v118, v48, v49
	v_pk_fma_f32 v[48:49], v[56:57], s[4:5], v[50:51] op_sel_hi:[1,0,1]
	v_pk_add_f32 v[50:51], v[62:63], v[54:55]
	v_cvt_f32_f16_e32 v52, v74
	v_pk_add_f32 v[48:49], v[48:49], v[50:51]
	v_cvt_f32_f16_sdwa v55, v72 dst_sel:DWORD dst_unused:UNUSED_PAD src0_sel:WORD_1
	v_cvt_pk_f16_f32 v119, v48, v49
	v_or_b32_e32 v48, 0x21680, v165
	v_cvt_f32_f16_e32 v54, v72
	ds_read_b128 v[48:51], v48
	v_cvt_f32_f16_sdwa v59, v75 dst_sel:DWORD dst_unused:UNUSED_PAD src0_sel:WORD_1
	v_cvt_f32_f16_e32 v58, v75
	v_pk_fma_f32 v[56:57], v[54:55], s[4:5], v[52:53] op_sel_hi:[1,0,1]
	v_cvt_f32_f16_sdwa v61, v73 dst_sel:DWORD dst_unused:UNUSED_PAD src0_sel:WORD_1
	v_cvt_f32_f16_e32 v60, v73
	v_or_b32_e32 v52, 0x216a0, v165
	ds_read_b128 v[52:55], v52
	s_waitcnt lgkmcnt(1)
	v_pk_add_f32 v[32:33], v[32:33], v[48:49]
	v_cvt_f32_f16_sdwa v49, v70 dst_sel:DWORD dst_unused:UNUSED_PAD src0_sel:WORD_1
	v_pk_add_f32 v[32:33], v[56:57], v[32:33]
	v_cvt_f32_f16_e32 v48, v70
	v_cvt_f32_f16_sdwa v57, v68 dst_sel:DWORD dst_unused:UNUSED_PAD src0_sel:WORD_1
	v_cvt_f32_f16_e32 v56, v68
	v_cvt_pk_f16_f32 v120, v32, v33
	v_pk_fma_f32 v[32:33], v[60:61], s[4:5], v[58:59] op_sel_hi:[1,0,1]
	v_pk_add_f32 v[34:35], v[34:35], v[50:51]
	s_waitcnt lgkmcnt(0)
	v_pk_add_f32 v[36:37], v[36:37], v[52:53]
	v_pk_add_f32 v[32:33], v[32:33], v[34:35]
	v_cvt_f32_f16_sdwa v35, v71 dst_sel:DWORD dst_unused:UNUSED_PAD src0_sel:WORD_1
	v_cvt_pk_f16_f32 v121, v32, v33
	v_pk_fma_f32 v[32:33], v[56:57], s[4:5], v[48:49] op_sel_hi:[1,0,1]
	v_cvt_f32_f16_e32 v34, v71
	v_cvt_f32_f16_sdwa v49, v69 dst_sel:DWORD dst_unused:UNUSED_PAD src0_sel:WORD_1
	v_cvt_f32_f16_e32 v48, v69
	v_pk_add_f32 v[32:33], v[32:33], v[36:37]
	v_cvt_f32_f16_sdwa v37, v66 dst_sel:DWORD dst_unused:UNUSED_PAD src0_sel:WORD_1
	v_cvt_pk_f16_f32 v122, v32, v33
	v_pk_fma_f32 v[32:33], v[48:49], s[4:5], v[34:35] op_sel_hi:[1,0,1]
	v_pk_add_f32 v[34:35], v[38:39], v[54:55]
	v_cvt_f32_f16_e32 v36, v66
	v_cvt_f32_f16_sdwa v39, v64 dst_sel:DWORD dst_unused:UNUSED_PAD src0_sel:WORD_1
	v_cvt_f32_f16_e32 v38, v64
	v_pk_add_f32 v[32:33], v[32:33], v[34:35]
	v_or_b32_e32 v48, 0x216c0, v165
	v_cvt_pk_f16_f32 v123, v32, v33
	v_pk_fma_f32 v[32:33], v[38:39], s[4:5], v[36:37] op_sel_hi:[1,0,1]
	ds_read_b128 v[36:39], v166 offset:34816
	v_cvt_f32_f16_sdwa v35, v67 dst_sel:DWORD dst_unused:UNUSED_PAD src0_sel:WORD_1
	v_cvt_f32_f16_e32 v34, v67
	v_cvt_f32_f16_sdwa v57, v65 dst_sel:DWORD dst_unused:UNUSED_PAD src0_sel:WORD_1
	v_cvt_f32_f16_e32 v56, v65
	v_or_b32_e32 v52, 0x216e0, v165
	ds_read_b128 v[48:51], v48
	ds_read_b128 v[168:171], v52
	ds_read_b128 v[52:55], v166 offset:43520
	ds_read_b128 v[172:175], v166 offset:34848
	s_waitcnt lgkmcnt(4)
	v_mfma_f32_32x32x16_f16 v[96:111], v[36:39], v[112:115], 0
	s_waitcnt lgkmcnt(3)
	v_add_f32_e64 v36, v40, v48
	v_add_f32_e64 v37, v41, v49
	v_fma_f32 v40, v56, s4, v34
	v_fma_f32 v41, v57, s4, v35
	v_pk_add_f32 v[32:33], v[32:33], v[36:37]
	v_pk_add_f32 v[42:43], v[42:43], v[50:51]
	v_cvt_pk_f16_f32 v124, v32, v33
	ds_read_b128 v[32:35], v166 offset:52224
	ds_read_b128 v[36:39], v166 offset:43552
	v_pk_add_f32 v[48:49], v[40:41], v[42:43]
	s_waitcnt lgkmcnt(3)
	v_mfma_f32_32x32x16_f16 v[80:95], v[52:55], v[112:115], 0
	v_cvt_f32_f16_sdwa v51, v162 dst_sel:DWORD dst_unused:UNUSED_PAD src0_sel:WORD_1
	v_cvt_f32_f16_e32 v50, v162
	v_cvt_f32_f16_sdwa v53, v126 dst_sel:DWORD dst_unused:UNUSED_PAD src0_sel:WORD_1
	v_cvt_f32_f16_e32 v52, v126
	ds_read_b128 v[40:43], v166 offset:60928
	ds_read_b128 v[176:179], v166 offset:52256
	v_cvt_f32_f16_e32 v162, v127
	v_cvt_pk_f16_f32 v125, v48, v49
	v_pk_fma_f32 v[180:181], v[52:53], s[4:5], v[50:51] op_sel_hi:[1,0,1]
	s_waitcnt lgkmcnt(1)
	v_mfma_f32_32x32x16_f16 v[48:63], v[40:43], v[112:115], 0
	v_add_f32_e64 v40, v44, v168
	v_add_f32_e64 v41, v45, v169
	v_add_f32_e64 v42, v46, v170
	v_add_f32_e64 v43, v47, v171
	v_add_f32_e64 v40, v180, v40
	v_add_f32_e64 v41, v181, v41
	v_cvt_f32_f16_sdwa v45, v160 dst_sel:DWORD dst_unused:UNUSED_PAD src0_sel:WORD_1
	v_cvt_pk_f16_f32 v126, v40, v41
	v_pk_fma_f32 v[40:41], v[162:163], s[4:5], v[182:183] op_sel_hi:[1,0,1]
	v_cvt_f32_f16_e32 v44, v160
	v_pk_add_f32 v[40:41], v[40:41], v[42:43]
	v_cvt_f32_f16_sdwa v47, v128 dst_sel:DWORD dst_unused:UNUSED_PAD src0_sel:WORD_1
	v_cvt_pk_f16_f32 v127, v40, v41
	v_or_b32_e32 v40, 0x21700, v165
	ds_read_b128 v[40:43], v40
	v_cvt_f32_f16_e32 v46, v128
	v_mfma_f32_32x32x16_f16 v[64:79], v[32:35], v[112:115], 0
	ds_read_b128 v[32:35], v166 offset:60960
	v_cvt_f32_f16_e32 v160, v130
	v_fma_f32 v44, v46, s4, v44
	v_fma_f32 v45, v47, s4, v45
	v_cvt_f32_f16_sdwa v47, v129 dst_sel:DWORD dst_unused:UNUSED_PAD src0_sel:WORD_1
	v_cvt_f32_f16_e32 v46, v129
	v_mfma_f32_32x32x16_f16 v[80:95], v[36:39], v[116:119], v[80:95]
	v_or_b32_e32 v36, 0x21720, v165
	ds_read_b128 v[36:39], v36
	s_waitcnt lgkmcnt(2)
	v_add_f32_e64 v16, v16, v40
	v_add_f32_e64 v17, v17, v41
	v_cvt_f32_f16_sdwa v41, v161 dst_sel:DWORD dst_unused:UNUSED_PAD src0_sel:WORD_1
	v_cvt_f32_f16_e32 v40, v161
	v_pk_add_f32 v[16:17], v[44:45], v[16:17]
	v_pk_add_f32 v[18:19], v[18:19], v[42:43]
	v_cvt_pk_f16_f32 v128, v16, v17
	v_pk_fma_f32 v[16:17], v[46:47], s[4:5], v[40:41] op_sel_hi:[1,0,1]
	ds_read_b128 v[44:47], v166 offset:34880
	v_mfma_f32_32x32x16_f16 v[96:111], v[172:175], v[116:119], v[96:111]
	v_cvt_f32_f16_sdwa v41, v158 dst_sel:DWORD dst_unused:UNUSED_PAD src0_sel:WORD_1
	v_cvt_f32_f16_e32 v40, v158
	v_cvt_f32_f16_sdwa v161, v130 dst_sel:DWORD dst_unused:UNUSED_PAD src0_sel:WORD_1
	v_add_f32_e64 v16, v16, v18
	v_add_f32_e64 v17, v17, v19
	s_waitcnt lgkmcnt(1)
	v_pk_add_f32 v[20:21], v[20:21], v[36:37]
	v_cvt_pk_f16_f32 v129, v16, v17
	v_cvt_f32_f16_sdwa v37, v159 dst_sel:DWORD dst_unused:UNUSED_PAD src0_sel:WORD_1
	v_mfma_f32_32x32x16_f16 v[48:63], v[32:35], v[116:119], v[48:63]
	ds_read_b128 v[16:19], v166 offset:43584
	ds_read_b128 v[32:35], v166 offset:34912
	v_cvt_f32_f16_e32 v36, v159
	v_cvt_f32_f16_sdwa v159, v131 dst_sel:DWORD dst_unused:UNUSED_PAD src0_sel:WORD_1
	v_cvt_f32_f16_e32 v158, v131
	v_pk_fma_f32 v[160:161], v[160:161], s[4:5], v[40:41] op_sel_hi:[1,0,1]
	v_mfma_f32_32x32x16_f16 v[64:79], v[176:179], v[116:119], v[64:79]
	s_waitcnt lgkmcnt(1)
	v_mfma_f32_32x32x16_f16 v[80:95], v[16:19], v[120:123], v[80:95]
	v_add_f32_e64 v16, v160, v20
	v_add_f32_e64 v17, v161, v21
	v_add_f32_e64 v18, v22, v38
	v_add_f32_e64 v19, v23, v39
	v_cvt_pk_f16_f32 v130, v16, v17
	v_pk_fma_f32 v[16:17], v[158:159], s[4:5], v[36:37] op_sel_hi:[1,0,1]
	s_nop 0
	v_pk_add_f32 v[36:37], v[16:17], v[18:19]
	v_mfma_f32_32x32x16_f16 v[96:111], v[44:47], v[120:123], v[96:111]
	ds_read_b128 v[40:43], v166 offset:52288
	ds_read_b128 v[44:47], v166 offset:43616
	ds_read_b128 v[16:19], v166 offset:60992
	ds_read_b128 v[20:23], v166 offset:52320
	v_cvt_pk_f16_f32 v131, v36, v37
	ds_read_b128 v[36:39], v166 offset:61024
	s_waitcnt lgkmcnt(4)
	v_mfma_f32_32x32x16_f16 v[64:79], v[40:43], v[120:123], v[64:79]
	v_cvt_f32_f16_sdwa v43, v132 dst_sel:DWORD dst_unused:UNUSED_PAD src0_sel:WORD_1
	v_cvt_f32_f16_e32 v42, v132
	v_or_b32_e32 v132, 0x21740, v165
	v_cvt_f32_f16_sdwa v41, v156 dst_sel:DWORD dst_unused:UNUSED_PAD src0_sel:WORD_1
	v_cvt_f32_f16_e32 v40, v156
	v_cvt_f32_f16_e32 v156, v133
	v_pk_fma_f32 v[40:41], v[42:43], s[4:5], v[40:41] op_sel_hi:[1,0,1]
	s_waitcnt lgkmcnt(2)
	v_mfma_f32_32x32x16_f16 v[48:63], v[16:19], v[120:123], v[48:63]
	ds_read_b128 v[16:19], v132
	v_cvt_f32_f16_sdwa v43, v157 dst_sel:DWORD dst_unused:UNUSED_PAD src0_sel:WORD_1
	v_cvt_f32_f16_e32 v42, v157
	v_cvt_f32_f16_sdwa v157, v133 dst_sel:DWORD dst_unused:UNUSED_PAD src0_sel:WORD_1
	v_or_b32_e32 v132, 0x21760, v165
	s_waitcnt lgkmcnt(0)
	v_pk_add_f32 v[16:17], v[24:25], v[16:17]
	v_cvt_f32_f16_sdwa v25, v154 dst_sel:DWORD dst_unused:UNUSED_PAD src0_sel:WORD_1
	v_mfma_f32_32x32x16_f16 v[96:111], v[32:35], v[124:127], v[96:111]
	ds_read_b128 v[32:35], v132
	v_add_f32_e64 v16, v40, v16
	v_add_f32_e64 v17, v41, v17
	v_cvt_f32_f16_e32 v24, v154
	v_cvt_f32_f16_sdwa v41, v134 dst_sel:DWORD dst_unused:UNUSED_PAD src0_sel:WORD_1
	v_cvt_f32_f16_e32 v40, v134
	v_cvt_pk_f16_f32 v132, v16, v17
	v_pk_fma_f32 v[16:17], v[156:157], s[4:5], v[42:43] op_sel_hi:[1,0,1]
	v_pk_add_f32 v[18:19], v[26:27], v[18:19]
	v_mfma_f32_32x32x16_f16 v[80:95], v[44:47], v[124:127], v[80:95]
	v_add_f32_e64 v16, v16, v18
	v_add_f32_e64 v17, v17, v19
	s_waitcnt lgkmcnt(0)
	v_add_f32_e64 v18, v28, v32
	v_add_f32_e64 v19, v29, v33
	v_cvt_pk_f16_f32 v133, v16, v17
	v_pk_fma_f32 v[16:17], v[40:41], s[4:5], v[24:25] op_sel_hi:[1,0,1]
	v_pk_add_f32 v[30:31], v[30:31], v[34:35]
	v_pk_add_f32 v[16:17], v[16:17], v[18:19]
	v_cvt_f32_f16_sdwa v33, v152 dst_sel:DWORD dst_unused:UNUSED_PAD src0_sel:WORD_1
	v_cvt_pk_f16_f32 v134, v16, v17
	ds_read_b128 v[16:19], v166 offset:34944
	v_mfma_f32_32x32x16_f16 v[64:79], v[20:23], v[124:127], v[64:79]
	v_cvt_f32_f16_sdwa v21, v155 dst_sel:DWORD dst_unused:UNUSED_PAD src0_sel:WORD_1
	v_cvt_f32_f16_e32 v20, v155
	v_cvt_f32_f16_sdwa v23, v135 dst_sel:DWORD dst_unused:UNUSED_PAD src0_sel:WORD_1
	v_cvt_f32_f16_e32 v22, v135
	v_cvt_f32_f16_e32 v32, v152
	v_cvt_f32_f16_sdwa v35, v136 dst_sel:DWORD dst_unused:UNUSED_PAD src0_sel:WORD_1
	v_cvt_f32_f16_e32 v34, v136
	v_pk_fma_f32 v[28:29], v[22:23], s[4:5], v[20:21] op_sel_hi:[1,0,1]
	ds_read_b128 v[20:23], v166 offset:43648
	ds_read_b128 v[24:27], v166 offset:34976
	s_waitcnt lgkmcnt(2)
	v_mfma_f32_32x32x16_f16 v[96:111], v[16:19], v[128:131], v[96:111]
	v_add_f32_e64 v16, v28, v30
	v_add_f32_e64 v17, v29, v31
	v_fma_f32 v40, v34, s4, v32
	v_fma_f32 v41, v35, s4, v33
	v_cvt_pk_f16_f32 v135, v16, v17
	ds_read_b128 v[16:19], v166 offset:52352
	ds_read_b128 v[28:31], v166 offset:43680
	v_cvt_f32_f16_sdwa v43, v153 dst_sel:DWORD dst_unused:UNUSED_PAD src0_sel:WORD_1
	v_cvt_f32_f16_e32 v42, v153
	v_cvt_f32_f16_sdwa v45, v137 dst_sel:DWORD dst_unused:UNUSED_PAD src0_sel:WORD_1
	v_mfma_f32_32x32x16_f16 v[48:63], v[36:39], v[124:127], v[48:63]
	v_or_b32_e32 v36, 0x21780, v165
	v_cvt_f32_f16_e32 v44, v137
	s_waitcnt lgkmcnt(3)
	v_mfma_f32_32x32x16_f16 v[80:95], v[20:23], v[128:131], v[80:95]
	ds_read_b128 v[20:23], v36
	ds_read_b128 v[32:35], v166 offset:61056
	ds_read_b128 v[36:39], v166 offset:52384
	s_waitcnt lgkmcnt(2)
	v_add_f32_e64 v0, v0, v20
	v_add_f32_e64 v1, v1, v21
	v_pk_add_f32 v[0:1], v[40:41], v[0:1]
	v_mfma_f32_32x32x16_f16 v[64:79], v[16:19], v[128:131], v[64:79]
	v_or_b32_e32 v16, 0x217a0, v165
	ds_read_b128 v[16:19], v16
	v_add_f32_e64 v2, v2, v22
	v_add_f32_e64 v3, v3, v23
	v_cvt_f32_f16_sdwa v21, v150 dst_sel:DWORD dst_unused:UNUSED_PAD src0_sel:WORD_1
	v_cvt_f32_f16_e32 v20, v150
	v_cvt_f32_f16_sdwa v23, v138 dst_sel:DWORD dst_unused:UNUSED_PAD src0_sel:WORD_1
	v_cvt_f32_f16_e32 v22, v138
	v_cvt_pk_f16_f32 v136, v0, v1
	v_pk_fma_f32 v[0:1], v[44:45], s[4:5], v[42:43] op_sel_hi:[1,0,1]
	ds_read_b128 v[40:43], v166 offset:61088
	v_pk_add_f32 v[0:1], v[0:1], v[2:3]
	s_waitcnt lgkmcnt(1)
	v_pk_add_f32 v[2:3], v[4:5], v[16:17]
	v_cvt_f32_f16_sdwa v5, v151 dst_sel:DWORD dst_unused:UNUSED_PAD src0_sel:WORD_1
	v_cvt_f32_f16_e32 v4, v151
	v_cvt_f32_f16_sdwa v17, v139 dst_sel:DWORD dst_unused:UNUSED_PAD src0_sel:WORD_1
	v_cvt_f32_f16_e32 v16, v139
	v_cvt_pk_f16_f32 v137, v0, v1
	v_pk_fma_f32 v[0:1], v[22:23], s[4:5], v[20:21] op_sel_hi:[1,0,1]
	v_mfma_f32_32x32x16_f16 v[48:63], v[32:35], v[128:131], v[48:63]
	v_add_f32_e64 v0, v0, v2
	v_add_f32_e64 v1, v1, v3
	v_add_f32_e64 v2, v6, v18
	v_add_f32_e64 v3, v7, v19
	v_cvt_pk_f16_f32 v138, v0, v1
	v_pk_fma_f32 v[0:1], v[16:17], s[4:5], v[4:5] op_sel_hi:[1,0,1]
	v_cvt_f32_f16_sdwa v5, v148 dst_sel:DWORD dst_unused:UNUSED_PAD src0_sel:WORD_1
	v_pk_add_f32 v[0:1], v[0:1], v[2:3]
	v_cvt_f32_f16_e32 v4, v148
	v_cvt_pk_f16_f32 v139, v0, v1
	ds_read_b128 v[0:3], v166 offset:35008
	v_mfma_f32_32x32x16_f16 v[96:111], v[24:27], v[132:135], v[96:111]
	v_cvt_f32_f16_sdwa v7, v140 dst_sel:DWORD dst_unused:UNUSED_PAD src0_sel:WORD_1
	v_cvt_f32_f16_e32 v6, v140
	v_or_b32_e32 v16, 0x217c0, v165
	v_or_b32_e32 v17, 0x217e0, v165
	v_cvt_f32_f16_sdwa v33, v141 dst_sel:DWORD dst_unused:UNUSED_PAD src0_sel:WORD_1
	v_cvt_f32_f16_e32 v32, v141
	v_mfma_f32_32x32x16_f16 v[80:95], v[28:31], v[132:135], v[80:95]
	v_fma_f32 v28, v6, s4, v4
	v_fma_f32 v29, v7, s4, v5
	v_cvt_f32_f16_sdwa v31, v149 dst_sel:DWORD dst_unused:UNUSED_PAD src0_sel:WORD_1
	v_cvt_f32_f16_e32 v30, v149
	ds_read_b128 v[4:7], v16
	ds_read_b128 v[16:19], v17
	ds_read_b128 v[20:23], v166 offset:43712
	ds_read_b128 v[24:27], v166 offset:35040
	s_waitcnt lgkmcnt(3)
	v_pk_add_f32 v[10:11], v[10:11], v[6:7]
	v_mfma_f32_32x32x16_f16 v[64:79], v[36:39], v[132:135], v[64:79]
	v_mfma_f32_32x32x16_f16 v[48:63], v[40:43], v[132:135], v[48:63]
	v_mfma_f32_32x32x16_f16 v[96:111], v[0:3], v[136:139], v[96:111]
	v_add_f32_e64 v0, v8, v4
	v_add_f32_e64 v1, v9, v5
	v_fma_f32 v8, v32, s4, v30
	v_fma_f32 v9, v33, s4, v31
	v_add_f32_e64 v0, v28, v0
	v_add_f32_e64 v1, v29, v1
	v_pk_add_f32 v[28:29], v[8:9], v[10:11]
	v_cvt_pk_f16_f32 v140, v0, v1
	ds_read_b128 v[0:3], v166 offset:52416
	ds_read_b128 v[4:7], v166 offset:43744
	v_cvt_f32_f16_sdwa v31, v146 dst_sel:DWORD dst_unused:UNUSED_PAD src0_sel:WORD_1
	s_waitcnt lgkmcnt(3)
	v_mfma_f32_32x32x16_f16 v[80:95], v[20:23], v[136:139], v[80:95]
	ds_read_b128 v[8:11], v166 offset:61120
	ds_read_b128 v[20:23], v166 offset:52448
	v_cvt_f32_f16_e32 v30, v146
	v_cvt_f32_f16_sdwa v33, v142 dst_sel:DWORD dst_unused:UNUSED_PAD src0_sel:WORD_1
	v_cvt_f32_f16_e32 v32, v142
	v_cvt_pk_f16_f32 v141, v28, v29
	v_lshlrev_b32_e32 v146, 2, v164
	v_pk_fma_f32 v[28:29], v[32:33], s[4:5], v[30:31] op_sel_hi:[1,0,1]
	s_waitcnt lgkmcnt(3)
	v_mfma_f32_32x32x16_f16 v[64:79], v[0:3], v[136:139], v[64:79]
	ds_read_b128 v[0:3], v166 offset:61152
	v_cvt_f32_f16_sdwa v31, v147 dst_sel:DWORD dst_unused:UNUSED_PAD src0_sel:WORD_1
	v_cvt_f32_f16_e32 v30, v147
	v_cvt_f32_f16_sdwa v33, v143 dst_sel:DWORD dst_unused:UNUSED_PAD src0_sel:WORD_1
	v_cvt_f32_f16_e32 v32, v143
	v_lshlrev_b32_e32 v147, 2, v146
	s_waitcnt lgkmcnt(2)
	v_mfma_f32_32x32x16_f16 v[48:63], v[8:11], v[136:139], v[48:63]
	v_add_f32_e64 v8, v12, v16
	v_add_f32_e64 v9, v13, v17
	v_add_f32_e64 v10, v14, v18
	v_add_f32_e64 v11, v15, v19
	v_add_f32_e64 v8, v28, v8
	v_add_f32_e64 v9, v29, v9
	v_cvt_pk_f16_f32 v142, v8, v9
	v_pk_fma_f32 v[8:9], v[32:33], s[4:5], v[30:31] op_sel_hi:[1,0,1]
	s_load_dwordx4 s[4:7], s[0:1], 0x1f0
	v_pk_add_f32 v[8:9], v[8:9], v[10:11]
	s_nop 0
	v_cvt_pk_f16_f32 v143, v8, v9
	s_nop 1
	v_mfma_f32_32x32x16_f16 v[96:111], v[24:27], v[140:143], v[96:111]
	v_mfma_f32_32x32x16_f16 v[80:95], v[4:7], v[140:143], v[80:95]
	v_mul_u32_u24_e32 v4, 0x110, v145
	v_ashrrev_i32_e32 v145, 31, v144
	s_waitcnt lgkmcnt(0)
	v_mfma_f32_32x32x16_f16 v[64:79], v[20:23], v[140:143], v[64:79]
	v_mfma_f32_32x32x16_f16 v[48:63], v[0:3], v[140:143], v[48:63]
	s_and_saveexec_b64 s[0:1], s[8:9]
	s_cbranch_execz .LBB11_14
	v_or_b32_e32 v0, 0x21200, v147
	ds_read_b128 v[6:9], v0
	v_or_b32_e32 v2, 0x21220, v147
	ds_read_b128 v[10:13], v2
	v_lshlrev_b64 v[0:1], 5, v[144:145]
	v_lshl_add_u64 v[0:1], s[4:5], 0, v[0:1]
	s_waitcnt lgkmcnt(1)
	v_pk_add_f32 v[2:3], v[96:97], v[6:7]
	s_lshl_b64 s[4:5], s[36:37], 20
	v_cvt_pk_f16_f32 v6, v2, v3
	v_pk_add_f32 v[2:3], v[98:99], v[8:9]
	v_lshl_add_u64 v[8:9], v[0:1], 0, s[4:5]
	v_cvt_pk_f16_f32 v7, v2, v3
	v_lshlrev_b32_e32 v2, 1, v146
	v_mov_b32_e32 v3, 0
	v_lshl_add_u64 v[14:15], v[8:9], 0, v[2:3]
	global_store_dwordx2 v[14:15], v[6:7], off
	s_waitcnt lgkmcnt(0)
	v_pk_add_f32 v[6:7], v[100:101], v[10:11]
	v_or_b32_e32 v5, 0x21240, v147
	v_cvt_pk_f16_f32 v10, v6, v7
	ds_read_b128 v[6:9], v5
	v_pk_add_f32 v[12:13], v[102:103], v[12:13]
	v_or_b32_e32 v5, 0x21260, v147
	v_cvt_pk_f16_f32 v11, v12, v13
	global_store_dwordx2 v[14:15], v[10:11], off offset:16
	ds_read_b128 v[10:13], v5
	s_waitcnt lgkmcnt(1)
	v_pk_add_f32 v[6:7], v[104:105], v[6:7]
	v_pk_add_f32 v[8:9], v[106:107], v[8:9]
	s_lshl_b64 s[4:5], s[34:35], 20
	v_cvt_pk_f16_f32 v6, v6, v7
	v_cvt_pk_f16_f32 v7, v8, v9
	v_lshl_add_u64 v[8:9], v[0:1], 0, s[4:5]
	v_lshl_add_u64 v[14:15], v[8:9], 0, v[2:3]
	global_store_dwordx2 v[14:15], v[6:7], off
	s_waitcnt lgkmcnt(0)
	v_pk_add_f32 v[6:7], v[108:109], v[10:11]
	v_or_b32_e32 v5, 0x21280, v147
	v_cvt_pk_f16_f32 v10, v6, v7
	ds_read_b128 v[6:9], v5
	v_pk_add_f32 v[12:13], v[110:111], v[12:13]
	v_or_b32_e32 v5, 0x212a0, v147
	v_cvt_pk_f16_f32 v11, v12, v13
	global_store_dwordx2 v[14:15], v[10:11], off offset:16
	ds_read_b128 v[10:13], v5
	s_waitcnt lgkmcnt(1)
	v_pk_add_f32 v[6:7], v[80:81], v[6:7]
	v_pk_add_f32 v[8:9], v[82:83], v[8:9]
	s_lshl_b64 s[4:5], s[30:31], 20
	v_cvt_pk_f16_f32 v6, v6, v7
	v_cvt_pk_f16_f32 v7, v8, v9
	v_lshl_add_u64 v[8:9], v[0:1], 0, s[4:5]
	v_lshl_add_u64 v[14:15], v[8:9], 0, v[2:3]
	global_store_dwordx2 v[14:15], v[6:7], off
	s_waitcnt lgkmcnt(0)
	v_pk_add_f32 v[6:7], v[84:85], v[10:11]
	v_or_b32_e32 v5, 0x212c0, v147
	v_cvt_pk_f16_f32 v10, v6, v7
	ds_read_b128 v[6:9], v5
	v_pk_add_f32 v[12:13], v[86:87], v[12:13]
	v_or_b32_e32 v5, 0x212e0, v147
	v_cvt_pk_f16_f32 v11, v12, v13
	global_store_dwordx2 v[14:15], v[10:11], off offset:16
	ds_read_b128 v[10:13], v5
	s_waitcnt lgkmcnt(1)
	v_pk_add_f32 v[6:7], v[88:89], v[6:7]
	v_pk_add_f32 v[8:9], v[90:91], v[8:9]
	s_lshl_b64 s[4:5], s[28:29], 20
	v_cvt_pk_f16_f32 v6, v6, v7
	v_cvt_pk_f16_f32 v7, v8, v9
	v_lshl_add_u64 v[8:9], v[0:1], 0, s[4:5]
	v_lshl_add_u64 v[14:15], v[8:9], 0, v[2:3]
	global_store_dwordx2 v[14:15], v[6:7], off
	s_waitcnt lgkmcnt(0)
	v_pk_add_f32 v[6:7], v[92:93], v[10:11]
	v_or_b32_e32 v5, 0x21300, v147
	v_cvt_pk_f16_f32 v10, v6, v7
	ds_read_b128 v[6:9], v5
	v_pk_add_f32 v[12:13], v[94:95], v[12:13]
	v_or_b32_e32 v5, 0x21320, v147
	v_cvt_pk_f16_f32 v11, v12, v13
	global_store_dwordx2 v[14:15], v[10:11], off offset:16
	ds_read_b128 v[10:13], v5
	s_waitcnt lgkmcnt(1)
	v_pk_add_f32 v[6:7], v[64:65], v[6:7]
	v_pk_add_f32 v[8:9], v[66:67], v[8:9]
	s_lshl_b64 s[4:5], s[26:27], 20
	v_cvt_pk_f16_f32 v6, v6, v7
	v_cvt_pk_f16_f32 v7, v8, v9
	v_lshl_add_u64 v[8:9], v[0:1], 0, s[4:5]
	v_lshl_add_u64 v[14:15], v[8:9], 0, v[2:3]
	global_store_dwordx2 v[14:15], v[6:7], off
	s_waitcnt lgkmcnt(0)
	v_pk_add_f32 v[6:7], v[68:69], v[10:11]
	v_or_b32_e32 v5, 0x21340, v147
	v_cvt_pk_f16_f32 v10, v6, v7
	ds_read_b128 v[6:9], v5
	v_pk_add_f32 v[12:13], v[70:71], v[12:13]
	v_or_b32_e32 v5, 0x21360, v147
	v_cvt_pk_f16_f32 v11, v12, v13
	global_store_dwordx2 v[14:15], v[10:11], off offset:16
	ds_read_b128 v[10:13], v5
	s_waitcnt lgkmcnt(1)
	v_pk_add_f32 v[6:7], v[72:73], v[6:7]
	v_pk_add_f32 v[8:9], v[74:75], v[8:9]
	s_lshl_b64 s[4:5], s[24:25], 20
	v_cvt_pk_f16_f32 v6, v6, v7
	v_cvt_pk_f16_f32 v7, v8, v9
	v_lshl_add_u64 v[8:9], v[0:1], 0, s[4:5]
	v_lshl_add_u64 v[14:15], v[8:9], 0, v[2:3]
	global_store_dwordx2 v[14:15], v[6:7], off
	s_waitcnt lgkmcnt(0)
	v_pk_add_f32 v[6:7], v[76:77], v[10:11]
	v_or_b32_e32 v5, 0x21380, v147
	v_cvt_pk_f16_f32 v10, v6, v7
	ds_read_b128 v[6:9], v5
	v_pk_add_f32 v[12:13], v[78:79], v[12:13]
	v_or_b32_e32 v5, 0x213a0, v147
	v_cvt_pk_f16_f32 v11, v12, v13
	global_store_dwordx2 v[14:15], v[10:11], off offset:16
	ds_read_b128 v[10:13], v5
	s_waitcnt lgkmcnt(1)
	v_pk_add_f32 v[6:7], v[48:49], v[6:7]
	v_pk_add_f32 v[8:9], v[50:51], v[8:9]
	s_lshl_b64 s[4:5], s[10:11], 20
	v_cvt_pk_f16_f32 v6, v6, v7
	v_cvt_pk_f16_f32 v7, v8, v9
	v_lshl_add_u64 v[8:9], v[0:1], 0, s[4:5]
	v_lshl_add_u64 v[14:15], v[8:9], 0, v[2:3]
	global_store_dwordx2 v[14:15], v[6:7], off
	s_waitcnt lgkmcnt(0)
	v_pk_add_f32 v[6:7], v[52:53], v[10:11]
	v_or_b32_e32 v5, 0x213c0, v147
	v_cvt_pk_f16_f32 v10, v6, v7
	v_pk_add_f32 v[12:13], v[54:55], v[12:13]
	ds_read_b128 v[6:9], v5
	v_cvt_pk_f16_f32 v11, v12, v13
	v_or_b32_e32 v5, 0x213e0, v147
	global_store_dwordx2 v[14:15], v[10:11], off offset:16
	ds_read_b128 v[10:13], v5
	s_lshl_b64 s[4:5], s[2:3], 20
	s_waitcnt lgkmcnt(1)
	v_pk_add_f32 v[6:7], v[56:57], v[6:7]
	v_pk_add_f32 v[8:9], v[58:59], v[8:9]
	v_lshl_add_u64 v[0:1], v[0:1], 0, s[4:5]
	v_cvt_pk_f16_f32 v6, v6, v7
	v_cvt_pk_f16_f32 v7, v8, v9
	v_lshl_add_u64 v[0:1], v[0:1], 0, v[2:3]
	global_store_dwordx2 v[0:1], v[6:7], off
	s_waitcnt lgkmcnt(0)
	v_pk_add_f32 v[2:3], v[60:61], v[10:11]
	v_pk_add_f32 v[6:7], v[62:63], v[12:13]
	v_cvt_pk_f16_f32 v2, v2, v3
	v_cvt_pk_f16_f32 v3, v6, v7
	global_store_dwordx2 v[0:1], v[2:3], off offset:16

	.amdhsa_kernel _Z12tailA_kernel5TailP3KvP
		.amdhsa_group_segment_fixed_size 137216
		.amdhsa_private_segment_fixed_size 0
		.amdhsa_kernarg_size 512
		.amdhsa_user_sgpr_count 2
		.amdhsa_user_sgpr_dispatch_ptr 0
		.amdhsa_user_sgpr_queue_ptr 0
		.amdhsa_user_sgpr_kernarg_segment_ptr 1
		.amdhsa_user_sgpr_dispatch_id 0
		.amdhsa_user_sgpr_kernarg_preload_length 0
		.amdhsa_user_sgpr_kernarg_preload_offset 0
		.amdhsa_user_sgpr_private_segment_size 0
		.amdhsa_uses_dynamic_stack 0
		.amdhsa_enable_private_segment 0
		.amdhsa_system_sgpr_workgroup_id_x 1
		.amdhsa_system_sgpr_workgroup_id_y 1
		.amdhsa_system_sgpr_workgroup_id_z 0
		.amdhsa_system_sgpr_workgroup_info 0
		.amdhsa_system_vgpr_workitem_id 0
		.amdhsa_next_free_vgpr 200
		.amdhsa_next_free_sgpr 96
		.amdhsa_accum_offset 200
		.amdhsa_reserve_vcc 1
		.amdhsa_float_round_mode_32 0
		.amdhsa_float_round_mode_16_64 0
		.amdhsa_float_denorm_mode_32 3
		.amdhsa_float_denorm_mode_16_64 3
		.amdhsa_dx10_clamp 1
		.amdhsa_ieee_mode 1
		.amdhsa_fp16_overflow 0
		.amdhsa_tg_split 0
		.amdhsa_exception_fp_ieee_invalid_op 0
		.amdhsa_exception_fp_denorm_src 0
		.amdhsa_exception_fp_ieee_div_zero 0
		.amdhsa_exception_fp_ieee_overflow 0
		.amdhsa_exception_fp_ieee_underflow 0
		.amdhsa_exception_fp_ieee_inexact 0
		.amdhsa_exception_int_div_zero 0
	.end_amdhsa_kernel

.LBB12_16:
	s_and_b64 vcc, exec, s[4:5]
	s_cbranch_vccz .LBB12_30
	s_lshl_b32 s2, s2, 8
	v_lshrrev_b32_e32 v1, 1, v0
	s_addk_i32 s2, 0xe00
	v_and_b32_e32 v1, 0xe0, v1
	v_and_b32_e32 v145, 31, v0
	v_or_b32_e32 v8, s2, v1
	v_or_b32_e32 v144, v8, v145
	s_movk_i32 s2, 0x7e90
	v_mov_b32_e32 v1, 0x7e8f
	v_cmp_gt_i32_e64 s[8:9], s2, v144
	s_mov_b32 s2, 0xb60b60b7
	s_load_dwordx2 s[4:5], s[0:1], 0x1a8
	v_cndmask_b32_e64 v2, v1, v144, s[8:9]
	v_mul_hi_i32 v1, v2, s2
	v_add_u32_e32 v1, v1, v2
	v_lshrrev_b32_e32 v3, 31, v1
	v_ashrrev_i32_e32 v1, 7, v1
	v_add_u32_e32 v1, v1, v3
	s_movk_i32 s2, 0xff4c
	v_mad_u64_u32 v[2:3], s[6:7], v1, s2, v[2:3]
	s_movk_i32 s2, 0xb6
	v_mul_lo_u32 v3, v1, s2
	s_movk_i32 s2, 0xbf
	v_add3_u32 v6, v3, v2, s2
	v_ashrrev_i32_e32 v7, 31, v6
	s_lshl_b32 s36, s3, 3
	v_mov_b64_e32 v[198:199], v[6:7]
	v_bfe_u32 v164, v0, 5, 1
	s_waitcnt lgkmcnt(0)
	s_mov_b64 s[38:39], s[4:5]
	s_or_b32 s34, s36, 1
	s_or_b32 s30, s36, 2
	s_or_b32 s28, s36, 3
	s_or_b32 s26, s36, 4
	s_or_b32 s24, s36, 5
	s_or_b32 s10, s36, 6
	s_or_b32 s2, s36, 7
	s_nop 0
	s_load_dwordx8 s[12:19], s[0:1], 0x1b0
	s_load_dwordx4 s[20:23], s[0:1], 0x1d0
	s_movk_i32 s3, 0x80
	v_cmp_gt_u32_e64 s[4:5], s3, v0
	v_lshlrev_b32_e32 v3, 2, v0
	v_mov_b32_e32 v4, 0
	v_mov_b32_e32 v9, 0
	v_mov_b32_e32 v10, 0
	v_mov_b32_e32 v11, 0
	v_mov_b32_e32 v6, 0
	v_mov_b32_e32 v7, 0
	s_and_saveexec_b64 s[6:7], s[4:5]
	s_cbranch_execz .LBB12_19
	v_lshlrev_b32_e32 v12, 3, v0
	s_waitcnt lgkmcnt(0)
	global_load_dwordx2 v[6:7], v12, s[12:13]
	global_load_dword v11, v3, s[14:15]
	global_load_dword v10, v3, s[16:17]
	global_load_dword v9, v3, s[18:19]
	global_load_dword v4, v3, s[20:21]

.LBB12_23:
	s_or_b64 exec, exec, s[12:13]
	s_and_saveexec_b64 s[4:5], s[6:7]
	v_mov_b32_e32 v3, 0x23600
	v_lshl_add_u32 v0, v0, 2, v3
	ds_write_b32 v0, v5
	s_or_b64 exec, exec, s[4:5]
	s_movk_i32 s3, 0x7e90
	v_cmp_gt_i32_e32 vcc, s3, v8
	s_waitcnt lgkmcnt(0)
	s_barrier
	s_and_saveexec_b64 s[4:5], vcc
	s_cbranch_execz .LBB12_30
	v_lshlrev_b32_e32 v94, 5, v164
	v_or_b32_e32 v0, 0x21c00, v94
	v_or_b32_e32 v4, 0x21e00, v94
	v_cvt_f32_i32_e32 v9, v1
	v_cvt_f32_i32_e32 v8, v2
	ds_read_b128 v[0:3], v0
	ds_read_b128 v[4:7], v4
	v_lshlrev_b32_e32 v165, 4, v164
	s_movk_i32 s3, 0x110
	v_pk_add_f32 v[92:93], v[8:9], 0.5 op_sel_hi:[1,0]
	s_waitcnt lgkmcnt(1)
	v_mov_b32_e32 v8, v0
	s_waitcnt lgkmcnt(0)
	v_mov_b32_e32 v9, v4
	v_or_b32_e32 v0, 0x22000, v94
	v_pk_mul_f32 v[20:21], v[92:93], v[8:9]
	v_or_b32_e32 v4, 0x22200, v94
	ds_read_b128 v[8:11], v0
	ds_read_b128 v[12:15], v4
	v_or_b32_e32 v0, 0x22400, v94
	ds_read_b128 v[16:19], v0
	v_add_f32_e32 v0, v20, v21
	s_waitcnt lgkmcnt(2)
	v_add_f32_e32 v0, v8, v0
	v_or_b32_e32 v4, 0x21c10, v94
	ds_read_b128 v[20:23], v4
	s_waitcnt lgkmcnt(1)
	v_fma_f32 v0, v12, v0, v16
	v_mov_b32_e32 v4, v1
	v_max_f32_e32 v24, 0, v0
	v_pk_mul_f32 v[0:1], v[92:93], v[4:5]
	v_or_b32_e32 v4, 0x22010, v94
	v_add_f32_e32 v0, v0, v1
	v_add_f32_e32 v0, v9, v0
	v_fma_f32 v0, v13, v0, v17
	v_max_f32_e32 v25, 0, v0
	v_mov_b32_e32 v0, v2
	v_mov_b32_e32 v1, v6
	v_pk_mul_f32 v[0:1], v[92:93], v[0:1]
	v_mov_b32_e32 v6, v3
	v_add_f32_e32 v0, v0, v1
	v_add_f32_e32 v0, v10, v0
	v_fma_f32 v0, v14, v0, v18
	v_max_f32_e32 v18, 0, v0
	v_pk_mul_f32 v[0:1], v[92:93], v[6:7]
	v_or_b32_e32 v8, 0x22210, v94
	v_add_f32_e32 v0, v0, v1
	v_add_f32_e32 v0, v11, v0
	v_fmac_f32_e32 v19, v15, v0
	v_or_b32_e32 v0, 0x21e10, v94
	ds_read_b128 v[0:3], v0
	ds_read_b128 v[4:7], v4
	v_or_b32_e32 v12, 0x22410, v94
	ds_read_b128 v[8:11], v8
	ds_read_b128 v[12:15], v12
	s_waitcnt lgkmcnt(4)
	v_mov_b32_e32 v16, v20
	s_waitcnt lgkmcnt(3)
	v_mov_b32_e32 v17, v0
	v_pk_mul_f32 v[16:17], v[92:93], v[16:17]
	v_mad_u32_u24 v166, v145, s3, v165
	v_add_f32_e32 v0, v16, v17
	s_waitcnt lgkmcnt(2)
	v_add_f32_e32 v0, v4, v0
	s_waitcnt lgkmcnt(0)
	v_fma_f32 v0, v8, v0, v12
	v_max_f32_e32 v4, 0, v0
	v_mov_b32_e32 v0, v21
	v_pk_mul_f32 v[0:1], v[92:93], v[0:1]
	v_max_f32_e32 v19, 0, v19
	v_add_f32_e32 v0, v0, v1
	v_add_f32_e32 v0, v5, v0
	v_fma_f32 v0, v9, v0, v13
	v_max_f32_e32 v5, 0, v0
	v_mov_b32_e32 v0, v22
	v_mov_b32_e32 v1, v2
	v_pk_mul_f32 v[0:1], v[92:93], v[0:1]
	v_mov_b32_e32 v2, v23
	v_add_f32_e32 v0, v0, v1
	v_add_f32_e32 v0, v6, v0
	v_fma_f32 v0, v10, v0, v14
	v_max_f32_e32 v6, 0, v0
	v_pk_mul_f32 v[0:1], v[92:93], v[2:3]
	ds_read_b128 v[96:99], v166 offset:32
	v_add_f32_e32 v8, v0, v1
	ds_read_b128 v[0:3], v166
	v_add_f32_e32 v7, v7, v8
	v_fmac_f32_e32 v15, v11, v7
	v_max_f32_e32 v7, 0, v15
	v_cvt_pk_f16_f32 v7, v6, v7
	v_cvt_pk_f16_f32 v6, v4, v5
	v_cvt_pk_f16_f32 v5, v18, v19
	v_cvt_pk_f16_f32 v4, v24, v25
	v_or_b32_e32 v8, 0x21c40, v94
	v_or_b32_e32 v9, 0x21e40, v94
	s_waitcnt lgkmcnt(0)
	v_mfma_f32_32x32x16_f16 v[48:63], v[0:3], v[4:7], 0
	v_mov_b32_e32 v190, 0x8180
	v_mad_i64_i32 v[192:193], s[40:41], s36, v190, v[198:199]
	v_lshlrev_b64 v[192:193], 6, v[192:193]
	v_lshl_add_u64 v[196:197], s[38:39], 0, v[192:193]
	v_mov_b32_e32 v193, 0
	v_lshlrev_b32_e32 v192, 3, v164
	v_lshl_add_u64 v[196:197], v[196:197], 0, v[192:193]
	global_load_dwordx2 v[90:91], v[196:197], off
	global_load_dwordx2 v[88:89], v[196:197], off offset:32
	global_load_dwordx2 v[84:85], v[196:197], off offset:48
	global_load_dwordx2 v[86:87], v[196:197], off offset:16
	ds_read_b128 v[0:3], v166 offset:8704
	ds_read_b128 v[100:103], v166 offset:8736
	v_or_b32_e32 v95, 0x22040, v94
	s_mov_b32 s4, 0x3a000000
	s_ashr_i32 s37, s36, 31
	s_waitcnt lgkmcnt(1)
	v_mfma_f32_32x32x16_f16 v[32:47], v[0:3], v[4:7], 0
	v_mad_i64_i32 v[196:197], s[40:41], s34, v190, v[198:199]
	v_lshlrev_b64 v[196:197], 6, v[196:197]
	v_lshl_add_u64 v[196:197], s[38:39], 0, v[196:197]
	v_lshl_add_u64 v[196:197], v[196:197], 0, v[192:193]
	global_load_dwordx2 v[82:83], v[196:197], off
	global_load_dwordx2 v[80:81], v[196:197], off offset:32
	global_load_dwordx2 v[76:77], v[196:197], off offset:48
	global_load_dwordx2 v[78:79], v[196:197], off offset:16
	ds_read_b128 v[0:3], v166 offset:17408
	ds_read_b128 v[104:107], v166 offset:17440
	s_ashr_i32 s35, s34, 31
	s_ashr_i32 s31, s30, 31
	s_ashr_i32 s29, s28, 31
	s_ashr_i32 s27, s26, 31
	s_ashr_i32 s25, s24, 31
	s_ashr_i32 s11, s10, 31
	s_waitcnt lgkmcnt(1)
	v_mfma_f32_32x32x16_f16 v[16:31], v[0:3], v[4:7], 0
	v_mad_i64_i32 v[196:197], s[40:41], s30, v190, v[198:199]
	v_lshlrev_b64 v[196:197], 6, v[196:197]
	v_lshl_add_u64 v[196:197], s[38:39], 0, v[196:197]
	v_lshl_add_u64 v[196:197], v[196:197], 0, v[192:193]
	global_load_dwordx2 v[74:75], v[196:197], off
	global_load_dwordx2 v[72:73], v[196:197], off offset:32
	global_load_dwordx2 v[68:69], v[196:197], off offset:48
	global_load_dwordx2 v[70:71], v[196:197], off offset:16
	ds_read_b128 v[0:3], v166 offset:26112
	ds_read_b128 v[108:111], v8
	ds_read_b128 v[112:115], v9
	ds_read_b128 v[116:119], v166 offset:26144
	s_ashr_i32 s3, s2, 31
	s_waitcnt lgkmcnt(2)
	v_mov_b32_e32 v120, v108
	s_waitcnt lgkmcnt(1)
	v_mov_b32_e32 v121, v112
	v_pk_mul_f32 v[124:125], v[92:93], v[120:121]
	v_or_b32_e32 v108, 0x22240, v94
	ds_read_b128 v[120:123], v95
	ds_read_b128 v[168:171], v108
	v_or_b32_e32 v95, 0x22440, v94
	ds_read_b128 v[172:175], v95
	v_or_b32_e32 v108, 0x21c50, v94
	v_mov_b32_e32 v112, v109
	ds_read_b128 v[176:179], v108
	v_pk_mul_f32 v[108:109], v[92:93], v[112:113]
	v_add_f32_e32 v95, v124, v125
	v_add_f32_e32 v108, v108, v109
	s_waitcnt lgkmcnt(3)
	v_add_f32_e32 v108, v121, v108
	s_waitcnt lgkmcnt(1)
	v_fma_f32 v108, v169, v108, v173
	v_max_f32_e32 v167, 0, v108
	v_mov_b32_e32 v108, v110
	v_mov_b32_e32 v109, v114
	v_pk_mul_f32 v[108:109], v[92:93], v[108:109]
	v_add_f32_e32 v95, v120, v95
	v_add_f32_e32 v108, v108, v109
	v_add_f32_e32 v108, v122, v108
	v_fma_f32 v108, v170, v108, v174
	v_mov_b32_e32 v114, v111
	v_fma_f32 v95, v168, v95, v172
	v_max_f32_e32 v172, 0, v108
	v_pk_mul_f32 v[108:109], v[92:93], v[114:115]
	v_or_b32_e32 v112, 0x22050, v94
	v_add_f32_e32 v108, v108, v109
	v_add_f32_e32 v108, v123, v108
	v_fmac_f32_e32 v175, v171, v108
	v_or_b32_e32 v108, 0x21e50, v94
	ds_read_b128 v[108:111], v108
	ds_read_b128 v[112:115], v112
	v_or_b32_e32 v120, 0x22250, v94
	v_or_b32_e32 v125, 0x22450, v94
	ds_read_b128 v[120:123], v120
	ds_read_b128 v[168:171], v125
	s_waitcnt lgkmcnt(4)
	v_mov_b32_e32 v124, v176
	s_waitcnt lgkmcnt(3)
	v_mov_b32_e32 v125, v108
	v_pk_mul_f32 v[124:125], v[92:93], v[124:125]
	v_max_f32_e32 v95, 0, v95
	v_add_f32_e32 v108, v124, v125
	s_waitcnt lgkmcnt(2)
	v_add_f32_e32 v108, v112, v108
	s_waitcnt lgkmcnt(0)
	v_fma_f32 v108, v120, v108, v168
	v_max_f32_e32 v112, 0, v108
	v_mov_b32_e32 v108, v177
	v_pk_mul_f32 v[108:109], v[92:93], v[108:109]
	v_max_f32_e32 v173, 0, v175
	v_add_f32_e32 v108, v108, v109
	v_add_f32_e32 v108, v113, v108
	v_fma_f32 v108, v121, v108, v169
	v_max_f32_e32 v113, 0, v108
	v_mov_b32_e32 v108, v178
	v_mov_b32_e32 v109, v110
	v_pk_mul_f32 v[108:109], v[92:93], v[108:109]
	v_mov_b32_e32 v110, v179
	v_add_f32_e32 v108, v108, v109
	v_add_f32_e32 v108, v114, v108
	v_fma_f32 v108, v122, v108, v170
	v_max_f32_e32 v114, 0, v108
	v_pk_mul_f32 v[108:109], v[92:93], v[110:111]
	v_mfma_f32_32x32x16_f16 v[0:15], v[0:3], v[4:7], 0
	v_mad_i64_i32 v[196:197], s[40:41], s28, v190, v[198:199]
	v_lshlrev_b64 v[196:197], 6, v[196:197]
	v_lshl_add_u64 v[196:197], s[38:39], 0, v[196:197]
	v_lshl_add_u64 v[196:197], v[196:197], 0, v[192:193]
	global_load_dwordx2 v[66:67], v[196:197], off
	global_load_dwordx2 v[64:65], v[196:197], off offset:32
	global_load_dwordx2 v[126:127], v[196:197], off offset:48
	global_load_dwordx2 v[162:163], v[196:197], off offset:16
	v_add_f32_e32 v108, v108, v109
	v_add_f32_e32 v108, v115, v108
	v_fmac_f32_e32 v171, v123, v108
	v_max_f32_e32 v108, 0, v171
	v_cvt_pk_f16_f32 v111, v114, v108
	v_cvt_pk_f16_f32 v110, v112, v113
	v_cvt_pk_f16_f32 v109, v172, v173
	v_cvt_pk_f16_f32 v108, v95, v167
	v_or_b32_e32 v95, 0x21c80, v94
	s_nop 0
	v_mfma_f32_32x32x16_f16 v[32:47], v[100:103], v[108:111], v[32:47]
	v_mad_i64_i32 v[196:197], s[40:41], s26, v190, v[198:199]
	v_lshlrev_b64 v[196:197], 6, v[196:197]
	v_lshl_add_u64 v[196:197], s[38:39], 0, v[196:197]
	v_lshl_add_u64 v[196:197], v[196:197], 0, v[192:193]
	global_load_dwordx2 v[160:161], v[196:197], off
	global_load_dwordx2 v[128:129], v[196:197], off offset:32
	global_load_dwordx2 v[130:131], v[196:197], off offset:48
	global_load_dwordx2 v[158:159], v[196:197], off offset:16
	v_or_b32_e32 v100, 0x21e80, v94
	v_mfma_f32_32x32x16_f16 v[48:63], v[96:99], v[108:111], v[48:63]
	v_mad_i64_i32 v[196:197], s[40:41], s24, v190, v[198:199]
	v_lshlrev_b64 v[196:197], 6, v[196:197]
	v_lshl_add_u64 v[196:197], s[38:39], 0, v[196:197]
	v_lshl_add_u64 v[196:197], v[196:197], 0, v[192:193]
	global_load_dwordx2 v[156:157], v[196:197], off
	global_load_dwordx2 v[132:133], v[196:197], off offset:32
	global_load_dwordx2 v[134:135], v[196:197], off offset:48
	global_load_dwordx2 v[154:155], v[196:197], off offset:16
	ds_read_b128 v[96:99], v95
	ds_read_b128 v[100:103], v100
	v_or_b32_e32 v95, 0x22080, v94
	v_mfma_f32_32x32x16_f16 v[16:31], v[104:107], v[108:111], v[16:31]
	v_mad_i64_i32 v[196:197], s[40:41], s10, v190, v[198:199]
	v_mad_i64_i32 v[198:199], s[40:41], s2, v190, v[198:199]
	v_lshlrev_b64 v[196:197], 6, v[196:197]
	v_lshlrev_b64 v[198:199], 6, v[198:199]
	v_lshl_add_u64 v[196:197], s[38:39], 0, v[196:197]
	v_lshl_add_u64 v[198:199], s[38:39], 0, v[198:199]
	v_lshl_add_u64 v[196:197], v[196:197], 0, v[192:193]
	v_lshl_add_u64 v[198:199], v[198:199], 0, v[192:193]
	global_load_dwordx2 v[152:153], v[196:197], off
	global_load_dwordx2 v[136:137], v[196:197], off offset:32
	global_load_dwordx2 v[138:139], v[196:197], off offset:48
	global_load_dwordx2 v[150:151], v[196:197], off offset:16
	global_load_dwordx2 v[148:149], v[198:199], off
	global_load_dwordx2 v[140:141], v[198:199], off offset:32
	global_load_dwordx2 v[142:143], v[198:199], off offset:48
	global_load_dwordx2 v[146:147], v[198:199], off offset:16
	s_waitcnt lgkmcnt(1)
	v_mov_b32_e32 v104, v96
	s_waitcnt lgkmcnt(0)
	v_mov_b32_e32 v105, v100
	v_or_b32_e32 v96, 0x22280, v94
	v_mov_b32_e32 v100, v97
	v_mfma_f32_32x32x16_f16 v[0:15], v[116:119], v[108:111], v[0:15]
	v_mul_f32_e64 v116, v92, v104
	v_mul_f32_e64 v117, v93, v105
	ds_read_b128 v[104:107], v95
	ds_read_b128 v[108:111], v96
	v_or_b32_e32 v95, 0x22480, v94
	ds_read_b128 v[112:115], v95
	v_or_b32_e32 v96, 0x21c90, v94
	v_add_f32_e32 v95, v116, v117
	ds_read_b128 v[116:119], v96
	v_pk_mul_f32 v[96:97], v[92:93], v[100:101]
	v_or_b32_e32 v100, 0x22090, v94
	v_add_f32_e32 v96, v96, v97
	s_waitcnt lgkmcnt(3)
	v_add_f32_e32 v96, v105, v96
	s_waitcnt lgkmcnt(1)
	v_fma_f32 v96, v109, v96, v113
	v_max_f32_e32 v120, 0, v96
	v_mov_b32_e32 v96, v98
	v_mov_b32_e32 v97, v102
	v_pk_mul_f32 v[96:97], v[92:93], v[96:97]
	v_mov_b32_e32 v102, v99
	v_add_f32_e32 v96, v96, v97
	v_add_f32_e32 v96, v106, v96
	v_fma_f32 v96, v110, v96, v114
	v_max_f32_e32 v114, 0, v96
	v_pk_mul_f32 v[96:97], v[92:93], v[102:103]
	v_add_f32_e32 v95, v104, v95
	v_add_f32_e32 v96, v96, v97
	v_add_f32_e32 v96, v107, v96
	v_fmac_f32_e32 v115, v111, v96
	v_or_b32_e32 v96, 0x21e90, v94
	ds_read_b128 v[96:99], v96
	ds_read_b128 v[100:103], v100
	v_fma_f32 v95, v108, v95, v112
	v_or_b32_e32 v104, 0x22290, v94
	v_or_b32_e32 v108, 0x22490, v94
	ds_read_b128 v[104:107], v104
	ds_read_b128 v[108:111], v108
	s_waitcnt lgkmcnt(4)
	v_mov_b32_e32 v112, v116
	s_waitcnt lgkmcnt(3)
	v_mov_b32_e32 v113, v96
	v_pk_mul_f32 v[112:113], v[92:93], v[112:113]
	v_max_f32_e32 v95, 0, v95
	v_add_f32_e32 v96, v112, v113
	s_waitcnt lgkmcnt(2)
	v_add_f32_e32 v96, v100, v96
	s_waitcnt lgkmcnt(0)
	v_fma_f32 v96, v104, v96, v108
	v_max_f32_e32 v100, 0, v96
	v_mov_b32_e32 v96, v117
	v_pk_mul_f32 v[96:97], v[92:93], v[96:97]
	v_max_f32_e32 v115, 0, v115
	v_add_f32_e32 v96, v96, v97
	v_add_f32_e32 v96, v101, v96
	v_fma_f32 v96, v105, v96, v109
	v_max_f32_e32 v101, 0, v96
	v_mov_b32_e32 v96, v118
	v_mov_b32_e32 v97, v98
	v_pk_mul_f32 v[96:97], v[92:93], v[96:97]
	v_mov_b32_e32 v98, v119
	v_add_f32_e32 v96, v96, v97
	v_add_f32_e32 v96, v102, v96
	v_fma_f32 v96, v106, v96, v110
	v_max_f32_e32 v102, 0, v96
	v_pk_mul_f32 v[96:97], v[92:93], v[98:99]
	s_nop 0
	v_add_f32_e32 v104, v96, v97
	ds_read_b128 v[96:99], v166 offset:64
	v_add_f32_e32 v103, v103, v104
	v_fmac_f32_e32 v111, v107, v103
	v_max_f32_e32 v103, 0, v111
	v_cvt_pk_f16_f32 v103, v102, v103
	v_cvt_pk_f16_f32 v102, v100, v101
	v_cvt_pk_f16_f32 v101, v114, v115
	v_cvt_pk_f16_f32 v100, v95, v120
	ds_read_b128 v[104:107], v166 offset:96
	v_or_b32_e32 v95, 0x21cc0, v94
	s_waitcnt lgkmcnt(1)
	v_mfma_f32_32x32x16_f16 v[48:63], v[96:99], v[100:103], v[48:63]
	ds_read_b128 v[96:99], v166 offset:8768
	ds_read_b128 v[108:111], v166 offset:8800
	v_or_b32_e32 v120, 0x21ec0, v94
	s_waitcnt lgkmcnt(1)
	v_mfma_f32_32x32x16_f16 v[32:47], v[96:99], v[100:103], v[32:47]
	ds_read_b128 v[96:99], v166 offset:17472
	ds_read_b128 v[112:115], v166 offset:17504
	s_waitcnt lgkmcnt(1)
	v_mfma_f32_32x32x16_f16 v[16:31], v[96:99], v[100:103], v[16:31]
	ds_read_b128 v[96:99], v166 offset:26176
	ds_read_b128 v[116:119], v95
	ds_read_b128 v[120:123], v120
	ds_read_b128 v[168:171], v166 offset:26208
	v_or_b32_e32 v95, 0x220c0, v94
	s_waitcnt lgkmcnt(3)
	v_mfma_f32_32x32x16_f16 v[0:15], v[96:99], v[100:103], v[0:15]
	s_waitcnt lgkmcnt(2)
	v_mov_b32_e32 v96, v116
	s_waitcnt lgkmcnt(1)
	v_mov_b32_e32 v97, v120
	v_or_b32_e32 v100, 0x222c0, v94
	v_pk_mul_f32 v[124:125], v[92:93], v[96:97]
	ds_read_b128 v[96:99], v95
	ds_read_b128 v[100:103], v100
	v_or_b32_e32 v95, 0x224c0, v94
	ds_read_b128 v[172:175], v95
	v_add_f32_e32 v95, v124, v125
	v_mov_b32_e32 v120, v117
	s_waitcnt lgkmcnt(2)
	v_add_f32_e32 v95, v96, v95
	v_or_b32_e32 v96, 0x21cd0, v94
	v_pk_mul_f32 v[116:117], v[92:93], v[120:121]
	ds_read_b128 v[176:179], v96
	v_add_f32_e32 v96, v116, v117
	v_add_f32_e32 v96, v97, v96
	s_waitcnt lgkmcnt(1)
	v_fma_f32 v96, v101, v96, v173
	v_max_f32_e32 v167, 0, v96
	v_mov_b32_e32 v96, v118
	v_mov_b32_e32 v97, v122
	v_pk_mul_f32 v[96:97], v[92:93], v[96:97]
	v_mov_b32_e32 v122, v119
	v_add_f32_e32 v96, v96, v97
	v_add_f32_e32 v96, v98, v96
	v_fma_f32 v96, v102, v96, v174
	v_fma_f32 v95, v100, v95, v172
	v_max_f32_e32 v172, 0, v96
	v_pk_mul_f32 v[96:97], v[92:93], v[122:123]
	v_or_b32_e32 v100, 0x220d0, v94
	v_add_f32_e32 v96, v96, v97
	v_add_f32_e32 v96, v99, v96
	v_fmac_f32_e32 v175, v103, v96
	v_or_b32_e32 v96, 0x21ed0, v94
	ds_read_b128 v[96:99], v96
	ds_read_b128 v[100:103], v100
	v_or_b32_e32 v116, 0x222d0, v94
	v_or_b32_e32 v120, 0x224d0, v94
	ds_read_b128 v[116:119], v116
	ds_read_b128 v[120:123], v120
	s_waitcnt lgkmcnt(4)
	v_mov_b32_e32 v124, v176
	s_waitcnt lgkmcnt(3)
	v_mov_b32_e32 v125, v96
	v_pk_mul_f32 v[124:125], v[92:93], v[124:125]
	v_max_f32_e32 v95, 0, v95
	v_add_f32_e32 v96, v124, v125
	s_waitcnt lgkmcnt(2)
	v_add_f32_e32 v96, v100, v96
	s_waitcnt lgkmcnt(0)
	v_fma_f32 v96, v116, v96, v120
	v_max_f32_e32 v100, 0, v96
	v_mov_b32_e32 v96, v177
	v_pk_mul_f32 v[96:97], v[92:93], v[96:97]
	v_max_f32_e32 v173, 0, v175
	v_add_f32_e32 v96, v96, v97
	v_add_f32_e32 v96, v101, v96
	v_fma_f32 v96, v117, v96, v121
	v_max_f32_e32 v101, 0, v96
	v_mov_b32_e32 v96, v178
	v_mov_b32_e32 v97, v98
	v_pk_mul_f32 v[96:97], v[92:93], v[96:97]
	v_mov_b32_e32 v98, v179
	v_add_f32_e32 v96, v96, v97
	v_add_f32_e32 v96, v102, v96
	v_fma_f32 v96, v118, v96, v122
	v_max_f32_e32 v102, 0, v96
	v_pk_mul_f32 v[96:97], v[92:93], v[98:99]
	v_cvt_pk_f16_f32 v98, v100, v101
	v_add_f32_e32 v96, v96, v97
	v_add_f32_e32 v96, v103, v96
	v_fmac_f32_e32 v123, v119, v96
	v_max_f32_e32 v96, 0, v123
	v_cvt_pk_f16_f32 v99, v102, v96
	v_cvt_pk_f16_f32 v97, v172, v173
	v_cvt_pk_f16_f32 v96, v95, v167
	v_or_b32_e32 v95, 0x21d00, v94
	s_nop 0
	v_mfma_f32_32x32x16_f16 v[48:63], v[104:107], v[96:99], v[48:63]
	v_or_b32_e32 v104, 0x21f00, v94
	ds_read_b128 v[100:103], v95
	ds_read_b128 v[104:107], v104
	v_or_b32_e32 v95, 0x22100, v94
	v_mfma_f32_32x32x16_f16 v[32:47], v[108:111], v[96:99], v[32:47]
	v_mfma_f32_32x32x16_f16 v[16:31], v[112:115], v[96:99], v[16:31]
	v_mfma_f32_32x32x16_f16 v[0:15], v[168:171], v[96:99], v[0:15]
	s_waitcnt lgkmcnt(1)
	v_mov_b32_e32 v96, v100
	s_waitcnt lgkmcnt(0)
	v_mov_b32_e32 v97, v104
	v_mul_f32_e64 v116, v92, v96
	v_mul_f32_e64 v117, v93, v97
	v_or_b32_e32 v100, 0x22300, v94
	ds_read_b128 v[96:99], v95
	ds_read_b128 v[108:111], v100
	v_or_b32_e32 v95, 0x22500, v94
	ds_read_b128 v[112:115], v95
	v_add_f32_e32 v95, v116, v117
	v_mov_b32_e32 v104, v101
	s_waitcnt lgkmcnt(2)
	v_add_f32_e32 v95, v96, v95
	v_or_b32_e32 v96, 0x21d10, v94
	v_pk_mul_f32 v[100:101], v[92:93], v[104:105]
	ds_read_b128 v[116:119], v96
	v_add_f32_e32 v96, v100, v101
	v_add_f32_e32 v96, v97, v96
	s_waitcnt lgkmcnt(1)
	v_fma_f32 v96, v109, v96, v113
	v_max_f32_e32 v120, 0, v96
	v_mov_b32_e32 v96, v102
	v_mov_b32_e32 v97, v106
	v_pk_mul_f32 v[96:97], v[92:93], v[96:97]
	v_mov_b32_e32 v106, v103
	v_add_f32_e32 v96, v96, v97
	v_add_f32_e32 v96, v98, v96
	v_fma_f32 v96, v110, v96, v114
	v_max_f32_e32 v114, 0, v96
	v_pk_mul_f32 v[96:97], v[92:93], v[106:107]
	v_or_b32_e32 v100, 0x22110, v94
	v_add_f32_e32 v96, v96, v97
	v_add_f32_e32 v96, v99, v96
	v_fmac_f32_e32 v115, v111, v96
	v_or_b32_e32 v96, 0x21f10, v94
	ds_read_b128 v[96:99], v96
	ds_read_b128 v[100:103], v100
	v_fma_f32 v95, v108, v95, v112
	v_or_b32_e32 v104, 0x22310, v94
	v_or_b32_e32 v108, 0x22510, v94
	ds_read_b128 v[104:107], v104
	ds_read_b128 v[108:111], v108
	s_waitcnt lgkmcnt(4)
	v_mov_b32_e32 v112, v116
	s_waitcnt lgkmcnt(3)
	v_mov_b32_e32 v113, v96
	v_pk_mul_f32 v[112:113], v[92:93], v[112:113]
	v_max_f32_e32 v95, 0, v95
	v_add_f32_e32 v96, v112, v113
	s_waitcnt lgkmcnt(2)
	v_add_f32_e32 v96, v100, v96
	s_waitcnt lgkmcnt(0)
	v_fma_f32 v96, v104, v96, v108
	v_max_f32_e32 v100, 0, v96
	v_mov_b32_e32 v96, v117
	v_pk_mul_f32 v[96:97], v[92:93], v[96:97]
	v_max_f32_e32 v115, 0, v115
	v_add_f32_e32 v96, v96, v97
	v_add_f32_e32 v96, v101, v96
	v_fma_f32 v96, v105, v96, v109
	v_max_f32_e32 v101, 0, v96
	v_mov_b32_e32 v96, v118
	v_mov_b32_e32 v97, v98
	v_pk_mul_f32 v[96:97], v[92:93], v[96:97]
	v_mov_b32_e32 v98, v119
	v_add_f32_e32 v96, v96, v97
	v_add_f32_e32 v96, v102, v96
	v_fma_f32 v96, v106, v96, v110
	v_max_f32_e32 v102, 0, v96
	v_pk_mul_f32 v[96:97], v[92:93], v[98:99]
	s_nop 0
	v_add_f32_e32 v104, v96, v97
	ds_read_b128 v[96:99], v166 offset:128
	v_add_f32_e32 v103, v103, v104
	v_fmac_f32_e32 v111, v107, v103
	v_max_f32_e32 v103, 0, v111
	v_cvt_pk_f16_f32 v103, v102, v103
	v_cvt_pk_f16_f32 v102, v100, v101
	v_cvt_pk_f16_f32 v101, v114, v115
	v_cvt_pk_f16_f32 v100, v95, v120
	ds_read_b128 v[104:107], v166 offset:160
	v_or_b32_e32 v95, 0x21d40, v94
	s_waitcnt lgkmcnt(1)
	v_mfma_f32_32x32x16_f16 v[48:63], v[96:99], v[100:103], v[48:63]
	ds_read_b128 v[96:99], v166 offset:8832
	ds_read_b128 v[108:111], v166 offset:8864
	v_or_b32_e32 v120, 0x21f40, v94
	s_waitcnt lgkmcnt(1)
	v_mfma_f32_32x32x16_f16 v[32:47], v[96:99], v[100:103], v[32:47]
	ds_read_b128 v[96:99], v166 offset:17536
	ds_read_b128 v[112:115], v166 offset:17568
	s_waitcnt lgkmcnt(1)
	v_mfma_f32_32x32x16_f16 v[16:31], v[96:99], v[100:103], v[16:31]
	ds_read_b128 v[96:99], v166 offset:26240
	ds_read_b128 v[116:119], v95
	ds_read_b128 v[120:123], v120
	ds_read_b128 v[168:171], v166 offset:26272
	v_or_b32_e32 v95, 0x22140, v94
	s_waitcnt lgkmcnt(3)
	v_mfma_f32_32x32x16_f16 v[0:15], v[96:99], v[100:103], v[0:15]
	s_waitcnt lgkmcnt(2)
	v_mov_b32_e32 v96, v116
	s_waitcnt lgkmcnt(1)
	v_mov_b32_e32 v97, v120
	v_or_b32_e32 v100, 0x22340, v94
	v_pk_mul_f32 v[124:125], v[92:93], v[96:97]
	ds_read_b128 v[96:99], v95
	ds_read_b128 v[100:103], v100
	v_or_b32_e32 v95, 0x22540, v94
	ds_read_b128 v[172:175], v95
	v_add_f32_e32 v95, v124, v125
	v_mov_b32_e32 v120, v117
	s_waitcnt lgkmcnt(2)
	v_add_f32_e32 v95, v96, v95
	v_or_b32_e32 v96, 0x21d50, v94
	v_pk_mul_f32 v[116:117], v[92:93], v[120:121]
	ds_read_b128 v[176:179], v96
	v_add_f32_e32 v96, v116, v117
	v_add_f32_e32 v96, v97, v96
	s_waitcnt lgkmcnt(1)
	v_fma_f32 v96, v101, v96, v173
	v_max_f32_e32 v167, 0, v96
	v_mov_b32_e32 v96, v118
	v_mov_b32_e32 v97, v122
	v_pk_mul_f32 v[96:97], v[92:93], v[96:97]
	v_mov_b32_e32 v122, v119
	v_add_f32_e32 v96, v96, v97
	v_add_f32_e32 v96, v98, v96
	v_fma_f32 v96, v102, v96, v174
	v_fma_f32 v95, v100, v95, v172
	v_max_f32_e32 v172, 0, v96
	v_pk_mul_f32 v[96:97], v[92:93], v[122:123]
	v_or_b32_e32 v100, 0x22150, v94
	v_add_f32_e32 v96, v96, v97
	v_add_f32_e32 v96, v99, v96
	v_fmac_f32_e32 v175, v103, v96
	v_or_b32_e32 v96, 0x21f50, v94
	ds_read_b128 v[96:99], v96
	ds_read_b128 v[100:103], v100
	v_or_b32_e32 v116, 0x22350, v94
	v_or_b32_e32 v120, 0x22550, v94
	ds_read_b128 v[116:119], v116
	ds_read_b128 v[120:123], v120
	s_waitcnt lgkmcnt(4)
	v_mov_b32_e32 v124, v176
	s_waitcnt lgkmcnt(3)
	v_mov_b32_e32 v125, v96
	v_pk_mul_f32 v[124:125], v[92:93], v[124:125]
	v_max_f32_e32 v95, 0, v95
	v_add_f32_e32 v96, v124, v125
	s_waitcnt lgkmcnt(2)
	v_add_f32_e32 v96, v100, v96
	s_waitcnt lgkmcnt(0)
	v_fma_f32 v96, v116, v96, v120
	v_max_f32_e32 v100, 0, v96
	v_mov_b32_e32 v96, v177
	v_pk_mul_f32 v[96:97], v[92:93], v[96:97]
	v_max_f32_e32 v173, 0, v175
	v_add_f32_e32 v96, v96, v97
	v_add_f32_e32 v96, v101, v96
	v_fma_f32 v96, v117, v96, v121
	v_max_f32_e32 v101, 0, v96
	v_mov_b32_e32 v96, v178
	v_mov_b32_e32 v97, v98
	v_pk_mul_f32 v[96:97], v[92:93], v[96:97]
	v_mov_b32_e32 v98, v179
	v_add_f32_e32 v96, v96, v97
	v_add_f32_e32 v96, v102, v96
	v_fma_f32 v96, v118, v96, v122
	v_max_f32_e32 v102, 0, v96
	v_pk_mul_f32 v[96:97], v[92:93], v[98:99]
	v_cvt_pk_f16_f32 v98, v100, v101
	v_add_f32_e32 v96, v96, v97
	v_add_f32_e32 v96, v103, v96
	v_fmac_f32_e32 v123, v119, v96
	v_max_f32_e32 v96, 0, v123
	v_cvt_pk_f16_f32 v99, v102, v96
	v_cvt_pk_f16_f32 v97, v172, v173
	v_cvt_pk_f16_f32 v96, v95, v167
	v_or_b32_e32 v95, 0x21d80, v94
	s_nop 0
	v_mfma_f32_32x32x16_f16 v[48:63], v[104:107], v[96:99], v[48:63]
	v_or_b32_e32 v104, 0x21f80, v94
	ds_read_b128 v[100:103], v95
	ds_read_b128 v[104:107], v104
	v_or_b32_e32 v95, 0x22180, v94
	v_mfma_f32_32x32x16_f16 v[32:47], v[108:111], v[96:99], v[32:47]
	v_mfma_f32_32x32x16_f16 v[16:31], v[112:115], v[96:99], v[16:31]
	v_mfma_f32_32x32x16_f16 v[0:15], v[168:171], v[96:99], v[0:15]
	s_waitcnt lgkmcnt(1)
	v_mov_b32_e32 v96, v100
	s_waitcnt lgkmcnt(0)
	v_mov_b32_e32 v97, v104
	v_mul_f32_e64 v116, v92, v96
	v_mul_f32_e64 v117, v93, v97
	v_or_b32_e32 v100, 0x22380, v94
	ds_read_b128 v[96:99], v95
	ds_read_b128 v[108:111], v100
	v_or_b32_e32 v95, 0x22580, v94
	ds_read_b128 v[112:115], v95
	v_add_f32_e32 v95, v116, v117
	v_mov_b32_e32 v104, v101
	s_waitcnt lgkmcnt(2)
	v_add_f32_e32 v95, v96, v95
	v_or_b32_e32 v96, 0x21d90, v94
	v_pk_mul_f32 v[100:101], v[92:93], v[104:105]
	ds_read_b128 v[116:119], v96
	v_add_f32_e32 v96, v100, v101
	v_add_f32_e32 v96, v97, v96
	s_waitcnt lgkmcnt(1)
	v_fma_f32 v96, v109, v96, v113
	v_max_f32_e32 v120, 0, v96
	v_mov_b32_e32 v96, v102
	v_mov_b32_e32 v97, v106
	v_pk_mul_f32 v[96:97], v[92:93], v[96:97]
	v_mov_b32_e32 v106, v103
	v_add_f32_e32 v96, v96, v97
	v_add_f32_e32 v96, v98, v96
	v_fma_f32 v96, v110, v96, v114
	v_max_f32_e32 v114, 0, v96
	v_pk_mul_f32 v[96:97], v[92:93], v[106:107]
	v_or_b32_e32 v100, 0x22190, v94
	v_add_f32_e32 v96, v96, v97
	v_add_f32_e32 v96, v99, v96
	v_fmac_f32_e32 v115, v111, v96
	v_or_b32_e32 v96, 0x21f90, v94
	ds_read_b128 v[96:99], v96
	ds_read_b128 v[100:103], v100
	v_fma_f32 v95, v108, v95, v112
	v_or_b32_e32 v104, 0x22390, v94
	v_or_b32_e32 v108, 0x22590, v94
	ds_read_b128 v[104:107], v104
	ds_read_b128 v[108:111], v108
	s_waitcnt lgkmcnt(4)
	v_mov_b32_e32 v112, v116
	s_waitcnt lgkmcnt(3)
	v_mov_b32_e32 v113, v96
	v_pk_mul_f32 v[112:113], v[92:93], v[112:113]
	v_max_f32_e32 v95, 0, v95
	v_add_f32_e32 v96, v112, v113
	s_waitcnt lgkmcnt(2)
	v_add_f32_e32 v96, v100, v96
	s_waitcnt lgkmcnt(0)
	v_fma_f32 v96, v104, v96, v108
	v_max_f32_e32 v100, 0, v96
	v_mov_b32_e32 v96, v117
	v_pk_mul_f32 v[96:97], v[92:93], v[96:97]
	v_max_f32_e32 v115, 0, v115
	v_add_f32_e32 v96, v96, v97
	v_add_f32_e32 v96, v101, v96
	v_fma_f32 v96, v105, v96, v109
	v_max_f32_e32 v101, 0, v96
	v_mov_b32_e32 v96, v118
	v_mov_b32_e32 v97, v98
	v_pk_mul_f32 v[96:97], v[92:93], v[96:97]
	v_mov_b32_e32 v98, v119
	v_add_f32_e32 v96, v96, v97
	v_add_f32_e32 v96, v102, v96
	v_fma_f32 v96, v106, v96, v110
	v_max_f32_e32 v102, 0, v96
	v_pk_mul_f32 v[96:97], v[92:93], v[98:99]
	s_nop 0
	v_add_f32_e32 v104, v96, v97
	ds_read_b128 v[96:99], v166 offset:192
	v_add_f32_e32 v103, v103, v104
	v_fmac_f32_e32 v111, v107, v103
	v_max_f32_e32 v103, 0, v111
	v_cvt_pk_f16_f32 v103, v102, v103
	v_cvt_pk_f16_f32 v102, v100, v101
	v_cvt_pk_f16_f32 v101, v114, v115
	v_cvt_pk_f16_f32 v100, v95, v120
	ds_read_b128 v[104:107], v166 offset:224
	v_or_b32_e32 v95, 0x21dc0, v94
	s_waitcnt lgkmcnt(1)
	v_mfma_f32_32x32x16_f16 v[48:63], v[96:99], v[100:103], v[48:63]
	ds_read_b128 v[96:99], v166 offset:8896
	ds_read_b128 v[108:111], v166 offset:8928
	v_or_b32_e32 v120, 0x21fc0, v94
	s_waitcnt lgkmcnt(1)
	v_mfma_f32_32x32x16_f16 v[32:47], v[96:99], v[100:103], v[32:47]
	ds_read_b128 v[96:99], v166 offset:17600
	ds_read_b128 v[112:115], v166 offset:17632
	s_waitcnt lgkmcnt(1)
	v_mfma_f32_32x32x16_f16 v[16:31], v[96:99], v[100:103], v[16:31]
	ds_read_b128 v[96:99], v166 offset:26304
	ds_read_b128 v[116:119], v95
	ds_read_b128 v[120:123], v120
	ds_read_b128 v[168:171], v166 offset:26336
	v_or_b32_e32 v95, 0x221c0, v94
	s_waitcnt lgkmcnt(3)
	v_mfma_f32_32x32x16_f16 v[0:15], v[96:99], v[100:103], v[0:15]
	s_waitcnt lgkmcnt(2)
	v_mov_b32_e32 v96, v116
	s_waitcnt lgkmcnt(1)
	v_mov_b32_e32 v97, v120
	v_or_b32_e32 v100, 0x223c0, v94
	v_pk_mul_f32 v[124:125], v[92:93], v[96:97]
	ds_read_b128 v[96:99], v95
	ds_read_b128 v[100:103], v100
	v_or_b32_e32 v95, 0x225c0, v94
	ds_read_b128 v[172:175], v95
	v_add_f32_e32 v95, v124, v125
	s_waitcnt lgkmcnt(2)
	v_add_f32_e32 v95, v96, v95
	v_mov_b32_e32 v120, v117
	v_pk_mul_f32 v[116:117], v[92:93], v[120:121]
	s_waitcnt lgkmcnt(0)
	v_fma_f32 v95, v100, v95, v172
	v_or_b32_e32 v96, 0x21dd0, v94
	v_max_f32_e32 v167, 0, v95
	v_add_f32_e32 v95, v116, v117
	ds_read_b128 v[176:179], v96
	v_add_f32_e32 v95, v97, v95
	v_mov_b32_e32 v96, v118
	v_mov_b32_e32 v97, v122
	v_fma_f32 v95, v101, v95, v173
	v_pk_mul_f32 v[96:97], v[92:93], v[96:97]
	v_max_f32_e32 v172, 0, v95
	v_add_f32_e32 v95, v96, v97
	v_add_f32_e32 v95, v98, v95
	v_mov_b32_e32 v122, v119
	v_fma_f32 v95, v102, v95, v174
	v_pk_mul_f32 v[96:97], v[92:93], v[122:123]
	v_max_f32_e32 v173, 0, v95
	v_add_f32_e32 v95, v96, v97
	v_add_f32_e32 v95, v99, v95
	v_fmac_f32_e32 v175, v103, v95
	v_or_b32_e32 v95, 0x21fd0, v94
	v_or_b32_e32 v100, 0x221d0, v94
	ds_read_b128 v[96:99], v95
	ds_read_b128 v[100:103], v100
	v_or_b32_e32 v95, 0x223d0, v94
	v_or_b32_e32 v94, 0x225d0, v94
	ds_read_b128 v[116:119], v95
	ds_read_b128 v[120:123], v94
	s_waitcnt lgkmcnt(4)
	v_mov_b32_e32 v124, v176
	s_waitcnt lgkmcnt(3)
	v_mov_b32_e32 v125, v96
	v_pk_mul_f32 v[94:95], v[92:93], v[124:125]
	v_mov_b32_e32 v96, v177
	v_add_f32_e32 v94, v94, v95
	s_waitcnt lgkmcnt(2)
	v_add_f32_e32 v94, v100, v94
	s_waitcnt lgkmcnt(0)
	v_fma_f32 v94, v116, v94, v120
	v_max_f32_e32 v100, 0, v94
	v_pk_mul_f32 v[94:95], v[92:93], v[96:97]
	v_max_f32_e32 v174, 0, v175
	v_add_f32_e32 v94, v94, v95
	v_add_f32_e32 v94, v101, v94
	v_fma_f32 v94, v117, v94, v121
	v_max_f32_e32 v96, 0, v94
	v_mov_b32_e32 v94, v178
	v_mov_b32_e32 v95, v98
	v_mov_b32_e32 v98, v179
	v_pk_mul_f32 v[94:95], v[92:93], v[94:95]
	v_pk_mul_f32 v[92:93], v[92:93], v[98:99]
	v_add_f32_e32 v94, v94, v95
	v_add_f32_e32 v92, v92, v93
	v_add_f32_e32 v94, v102, v94
	v_add_f32_e32 v92, v103, v92
	v_fma_f32 v94, v118, v94, v122
	v_fmac_f32_e32 v123, v119, v92
	v_max_f32_e32 v94, 0, v94
	v_max_f32_e32 v92, 0, v123
	v_cvt_pk_f16_f32 v95, v94, v92
	v_cvt_pk_f16_f32 v94, v100, v96
	v_cvt_pk_f16_f32 v93, v173, v174
	v_cvt_pk_f16_f32 v92, v167, v172
	s_waitcnt vmcnt(0)
	v_cvt_f32_f16_sdwa v183, v163 dst_sel:DWORD dst_unused:UNUSED_PAD src0_sel:WORD_1
	v_cvt_f32_f16_e32 v182, v163
	v_cvt_f32_f16_sdwa v163, v127 dst_sel:DWORD dst_unused:UNUSED_PAD src0_sel:WORD_1
	v_cvt_f32_f16_sdwa v97, v90 dst_sel:DWORD dst_unused:UNUSED_PAD src0_sel:WORD_1
	v_cvt_f32_f16_e32 v96, v90
	v_mfma_f32_32x32x16_f16 v[48:63], v[104:107], v[92:95], v[48:63]
	v_cvt_f32_f16_sdwa v99, v88 dst_sel:DWORD dst_unused:UNUSED_PAD src0_sel:WORD_1
	v_cvt_f32_f16_e32 v98, v88
	v_or_b32_e32 v88, 0x23a00, v165
	v_cvt_f32_f16_sdwa v101, v89 dst_sel:DWORD dst_unused:UNUSED_PAD src0_sel:WORD_1
	v_cvt_f32_f16_e32 v100, v89
	v_pk_fma_f32 v[96:97], v[98:99], s[4:5], v[96:97] op_sel_hi:[1,0,1]
	v_cvt_f32_f16_sdwa v99, v91 dst_sel:DWORD dst_unused:UNUSED_PAD src0_sel:WORD_1
	v_mfma_f32_32x32x16_f16 v[32:47], v[108:111], v[92:95], v[32:47]
	v_cvt_f32_f16_e32 v98, v91
	v_mfma_f32_32x32x16_f16 v[16:31], v[112:115], v[92:95], v[16:31]
	v_mfma_f32_32x32x16_f16 v[0:15], v[168:171], v[92:95], v[0:15]
	ds_read_b128 v[92:95], v88
	v_or_b32_e32 v88, 0x23a20, v165
	ds_read_b128 v[88:91], v88
	s_waitcnt lgkmcnt(1)
	v_add_f32_e64 v48, v48, v92
	v_add_f32_e64 v49, v49, v93
	v_pk_add_f32 v[48:49], v[96:97], v[48:49]
	v_cvt_f32_f16_sdwa v93, v86 dst_sel:DWORD dst_unused:UNUSED_PAD src0_sel:WORD_1
	v_cvt_f32_f16_e32 v92, v86
	v_cvt_f32_f16_sdwa v97, v84 dst_sel:DWORD dst_unused:UNUSED_PAD src0_sel:WORD_1
	v_cvt_f32_f16_e32 v96, v84
	v_cvt_pk_f16_f32 v112, v48, v49
	v_pk_fma_f32 v[48:49], v[100:101], s[4:5], v[98:99] op_sel_hi:[1,0,1]
	v_pk_add_f32 v[50:51], v[50:51], v[94:95]
	v_cvt_f32_f16_e32 v86, v85
	v_pk_add_f32 v[48:49], v[48:49], v[50:51]
	v_cvt_f32_f16_sdwa v51, v87 dst_sel:DWORD dst_unused:UNUSED_PAD src0_sel:WORD_1
	v_cvt_f32_f16_e32 v50, v87
	v_cvt_f32_f16_sdwa v87, v85 dst_sel:DWORD dst_unused:UNUSED_PAD src0_sel:WORD_1
	v_cvt_pk_f16_f32 v113, v48, v49
	v_pk_fma_f32 v[48:49], v[96:97], s[4:5], v[92:93] op_sel_hi:[1,0,1]
	s_waitcnt lgkmcnt(0)
	v_pk_add_f32 v[52:53], v[52:53], v[88:89]
	s_nop 0
	v_pk_add_f32 v[48:49], v[48:49], v[52:53]
	v_cvt_f32_f16_sdwa v53, v82 dst_sel:DWORD dst_unused:UNUSED_PAD src0_sel:WORD_1
	v_cvt_pk_f16_f32 v114, v48, v49
	v_pk_fma_f32 v[48:49], v[86:87], s[4:5], v[50:51] op_sel_hi:[1,0,1]
	v_pk_add_f32 v[50:51], v[54:55], v[90:91]
	v_cvt_f32_f16_e32 v52, v82
	v_pk_add_f32 v[48:49], v[48:49], v[50:51]
	v_cvt_f32_f16_sdwa v55, v80 dst_sel:DWORD dst_unused:UNUSED_PAD src0_sel:WORD_1
	v_cvt_pk_f16_f32 v115, v48, v49
	v_or_b32_e32 v48, 0x23a40, v165
	v_cvt_f32_f16_e32 v54, v80
	ds_read_b128 v[48:51], v48
	v_cvt_f32_f16_sdwa v87, v83 dst_sel:DWORD dst_unused:UNUSED_PAD src0_sel:WORD_1
	v_cvt_f32_f16_e32 v86, v83
	v_cvt_f32_f16_sdwa v83, v81 dst_sel:DWORD dst_unused:UNUSED_PAD src0_sel:WORD_1
	v_cvt_f32_f16_e32 v82, v81
	v_pk_fma_f32 v[84:85], v[54:55], s[4:5], v[52:53] op_sel_hi:[1,0,1]
	v_or_b32_e32 v52, 0x23a60, v165
	ds_read_b128 v[52:55], v52
	s_waitcnt lgkmcnt(1)
	v_pk_add_f32 v[48:49], v[56:57], v[48:49]
	v_cvt_f32_f16_sdwa v57, v78 dst_sel:DWORD dst_unused:UNUSED_PAD src0_sel:WORD_1
	v_cvt_f32_f16_e32 v56, v78
	v_cvt_f32_f16_sdwa v81, v76 dst_sel:DWORD dst_unused:UNUSED_PAD src0_sel:WORD_1
	v_cvt_f32_f16_e32 v80, v76
	v_pk_add_f32 v[48:49], v[84:85], v[48:49]
	v_pk_add_f32 v[50:51], v[58:59], v[50:51]
	v_cvt_pk_f16_f32 v116, v48, v49
	v_pk_fma_f32 v[48:49], v[82:83], s[4:5], v[86:87] op_sel_hi:[1,0,1]
	s_waitcnt lgkmcnt(0)
	v_pk_add_f32 v[52:53], v[60:61], v[52:53]
	v_pk_add_f32 v[48:49], v[48:49], v[50:51]
	v_cvt_f32_f16_sdwa v51, v79 dst_sel:DWORD dst_unused:UNUSED_PAD src0_sel:WORD_1
	v_cvt_pk_f16_f32 v117, v48, v49
	v_pk_fma_f32 v[48:49], v[80:81], s[4:5], v[56:57] op_sel_hi:[1,0,1]
	v_cvt_f32_f16_e32 v50, v79
	v_cvt_f32_f16_sdwa v57, v77 dst_sel:DWORD dst_unused:UNUSED_PAD src0_sel:WORD_1
	v_cvt_f32_f16_e32 v56, v77
	v_pk_add_f32 v[48:49], v[48:49], v[52:53]
	v_cvt_f32_f16_sdwa v53, v74 dst_sel:DWORD dst_unused:UNUSED_PAD src0_sel:WORD_1
	v_cvt_pk_f16_f32 v118, v48, v49
	v_pk_fma_f32 v[48:49], v[56:57], s[4:5], v[50:51] op_sel_hi:[1,0,1]
	v_pk_add_f32 v[50:51], v[62:63], v[54:55]
	v_cvt_f32_f16_e32 v52, v74
	v_pk_add_f32 v[48:49], v[48:49], v[50:51]
	v_cvt_f32_f16_sdwa v55, v72 dst_sel:DWORD dst_unused:UNUSED_PAD src0_sel:WORD_1
	v_cvt_pk_f16_f32 v119, v48, v49
	v_or_b32_e32 v48, 0x23a80, v165
	v_cvt_f32_f16_e32 v54, v72
	ds_read_b128 v[48:51], v48
	v_cvt_f32_f16_sdwa v59, v75 dst_sel:DWORD dst_unused:UNUSED_PAD src0_sel:WORD_1
	v_cvt_f32_f16_e32 v58, v75
	v_pk_fma_f32 v[56:57], v[54:55], s[4:5], v[52:53] op_sel_hi:[1,0,1]
	v_cvt_f32_f16_sdwa v61, v73 dst_sel:DWORD dst_unused:UNUSED_PAD src0_sel:WORD_1
	v_cvt_f32_f16_e32 v60, v73
	v_or_b32_e32 v52, 0x23aa0, v165
	ds_read_b128 v[52:55], v52
	s_waitcnt lgkmcnt(1)
	v_pk_add_f32 v[32:33], v[32:33], v[48:49]
	v_cvt_f32_f16_sdwa v49, v70 dst_sel:DWORD dst_unused:UNUSED_PAD src0_sel:WORD_1
	v_pk_add_f32 v[32:33], v[56:57], v[32:33]
	v_cvt_f32_f16_e32 v48, v70
	v_cvt_f32_f16_sdwa v57, v68 dst_sel:DWORD dst_unused:UNUSED_PAD src0_sel:WORD_1
	v_cvt_f32_f16_e32 v56, v68
	v_cvt_pk_f16_f32 v120, v32, v33
	v_pk_fma_f32 v[32:33], v[60:61], s[4:5], v[58:59] op_sel_hi:[1,0,1]
	v_pk_add_f32 v[34:35], v[34:35], v[50:51]
	s_waitcnt lgkmcnt(0)
	v_pk_add_f32 v[36:37], v[36:37], v[52:53]
	v_pk_add_f32 v[32:33], v[32:33], v[34:35]
	v_cvt_f32_f16_sdwa v35, v71 dst_sel:DWORD dst_unused:UNUSED_PAD src0_sel:WORD_1
	v_cvt_pk_f16_f32 v121, v32, v33
	v_pk_fma_f32 v[32:33], v[56:57], s[4:5], v[48:49] op_sel_hi:[1,0,1]
	v_cvt_f32_f16_e32 v34, v71
	v_cvt_f32_f16_sdwa v49, v69 dst_sel:DWORD dst_unused:UNUSED_PAD src0_sel:WORD_1
	v_cvt_f32_f16_e32 v48, v69
	v_pk_add_f32 v[32:33], v[32:33], v[36:37]
	v_cvt_f32_f16_sdwa v37, v66 dst_sel:DWORD dst_unused:UNUSED_PAD src0_sel:WORD_1
	v_cvt_pk_f16_f32 v122, v32, v33
	v_pk_fma_f32 v[32:33], v[48:49], s[4:5], v[34:35] op_sel_hi:[1,0,1]
	v_pk_add_f32 v[34:35], v[38:39], v[54:55]
	v_cvt_f32_f16_e32 v36, v66
	v_cvt_f32_f16_sdwa v39, v64 dst_sel:DWORD dst_unused:UNUSED_PAD src0_sel:WORD_1
	v_cvt_f32_f16_e32 v38, v64
	v_pk_add_f32 v[32:33], v[32:33], v[34:35]
	v_or_b32_e32 v48, 0x23ac0, v165
	v_cvt_pk_f16_f32 v123, v32, v33
	v_pk_fma_f32 v[32:33], v[38:39], s[4:5], v[36:37] op_sel_hi:[1,0,1]
	ds_read_b128 v[36:39], v166 offset:34816
	v_cvt_f32_f16_sdwa v35, v67 dst_sel:DWORD dst_unused:UNUSED_PAD src0_sel:WORD_1
	v_cvt_f32_f16_e32 v34, v67
	v_cvt_f32_f16_sdwa v57, v65 dst_sel:DWORD dst_unused:UNUSED_PAD src0_sel:WORD_1
	v_cvt_f32_f16_e32 v56, v65
	v_or_b32_e32 v52, 0x23ae0, v165
	ds_read_b128 v[48:51], v48
	ds_read_b128 v[168:171], v52
	ds_read_b128 v[52:55], v166 offset:43520
	ds_read_b128 v[172:175], v166 offset:34848
	s_waitcnt lgkmcnt(4)
	v_mfma_f32_32x32x16_f16 v[96:111], v[36:39], v[112:115], 0
	s_waitcnt lgkmcnt(3)
	v_add_f32_e64 v36, v40, v48
	v_add_f32_e64 v37, v41, v49
	v_fma_f32 v40, v56, s4, v34
	v_fma_f32 v41, v57, s4, v35
	v_pk_add_f32 v[32:33], v[32:33], v[36:37]
	v_pk_add_f32 v[42:43], v[42:43], v[50:51]
	v_cvt_pk_f16_f32 v124, v32, v33
	ds_read_b128 v[32:35], v166 offset:52224
	ds_read_b128 v[36:39], v166 offset:43552
	v_pk_add_f32 v[48:49], v[40:41], v[42:43]
	s_waitcnt lgkmcnt(3)
	v_mfma_f32_32x32x16_f16 v[80:95], v[52:55], v[112:115], 0
	v_cvt_f32_f16_sdwa v51, v162 dst_sel:DWORD dst_unused:UNUSED_PAD src0_sel:WORD_1
	v_cvt_f32_f16_e32 v50, v162
	v_cvt_f32_f16_sdwa v53, v126 dst_sel:DWORD dst_unused:UNUSED_PAD src0_sel:WORD_1
	v_cvt_f32_f16_e32 v52, v126
	ds_read_b128 v[40:43], v166 offset:60928
	ds_read_b128 v[176:179], v166 offset:52256
	v_cvt_f32_f16_e32 v162, v127
	v_cvt_pk_f16_f32 v125, v48, v49
	v_pk_fma_f32 v[180:181], v[52:53], s[4:5], v[50:51] op_sel_hi:[1,0,1]
	s_waitcnt lgkmcnt(1)
	v_mfma_f32_32x32x16_f16 v[48:63], v[40:43], v[112:115], 0
	v_add_f32_e64 v40, v44, v168
	v_add_f32_e64 v41, v45, v169
	v_add_f32_e64 v42, v46, v170
	v_add_f32_e64 v43, v47, v171
	v_add_f32_e64 v40, v180, v40
	v_add_f32_e64 v41, v181, v41
	v_cvt_f32_f16_sdwa v45, v160 dst_sel:DWORD dst_unused:UNUSED_PAD src0_sel:WORD_1
	v_cvt_pk_f16_f32 v126, v40, v41
	v_pk_fma_f32 v[40:41], v[162:163], s[4:5], v[182:183] op_sel_hi:[1,0,1]
	v_cvt_f32_f16_e32 v44, v160
	v_pk_add_f32 v[40:41], v[40:41], v[42:43]
	v_cvt_f32_f16_sdwa v47, v128 dst_sel:DWORD dst_unused:UNUSED_PAD src0_sel:WORD_1
	v_cvt_pk_f16_f32 v127, v40, v41
	v_or_b32_e32 v40, 0x23b00, v165
	ds_read_b128 v[40:43], v40
	v_cvt_f32_f16_e32 v46, v128
	v_mfma_f32_32x32x16_f16 v[64:79], v[32:35], v[112:115], 0
	ds_read_b128 v[32:35], v166 offset:60960
	v_cvt_f32_f16_e32 v160, v130
	v_fma_f32 v44, v46, s4, v44
	v_fma_f32 v45, v47, s4, v45
	v_cvt_f32_f16_sdwa v47, v129 dst_sel:DWORD dst_unused:UNUSED_PAD src0_sel:WORD_1
	v_cvt_f32_f16_e32 v46, v129
	v_mfma_f32_32x32x16_f16 v[80:95], v[36:39], v[116:119], v[80:95]
	v_or_b32_e32 v36, 0x23b20, v165
	ds_read_b128 v[36:39], v36
	s_waitcnt lgkmcnt(2)
	v_add_f32_e64 v16, v16, v40
	v_add_f32_e64 v17, v17, v41
	v_cvt_f32_f16_sdwa v41, v161 dst_sel:DWORD dst_unused:UNUSED_PAD src0_sel:WORD_1
	v_cvt_f32_f16_e32 v40, v161
	v_pk_add_f32 v[16:17], v[44:45], v[16:17]
	v_pk_add_f32 v[18:19], v[18:19], v[42:43]
	v_cvt_pk_f16_f32 v128, v16, v17
	v_pk_fma_f32 v[16:17], v[46:47], s[4:5], v[40:41] op_sel_hi:[1,0,1]
	ds_read_b128 v[44:47], v166 offset:34880
	v_mfma_f32_32x32x16_f16 v[96:111], v[172:175], v[116:119], v[96:111]
	v_cvt_f32_f16_sdwa v41, v158 dst_sel:DWORD dst_unused:UNUSED_PAD src0_sel:WORD_1
	v_cvt_f32_f16_e32 v40, v158
	v_cvt_f32_f16_sdwa v161, v130 dst_sel:DWORD dst_unused:UNUSED_PAD src0_sel:WORD_1
	v_add_f32_e64 v16, v16, v18
	v_add_f32_e64 v17, v17, v19
	s_waitcnt lgkmcnt(1)
	v_pk_add_f32 v[20:21], v[20:21], v[36:37]
	v_cvt_pk_f16_f32 v129, v16, v17
	v_cvt_f32_f16_sdwa v37, v159 dst_sel:DWORD dst_unused:UNUSED_PAD src0_sel:WORD_1
	v_mfma_f32_32x32x16_f16 v[48:63], v[32:35], v[116:119], v[48:63]
	ds_read_b128 v[16:19], v166 offset:43584
	ds_read_b128 v[32:35], v166 offset:34912
	v_cvt_f32_f16_e32 v36, v159
	v_cvt_f32_f16_sdwa v159, v131 dst_sel:DWORD dst_unused:UNUSED_PAD src0_sel:WORD_1
	v_cvt_f32_f16_e32 v158, v131
	v_pk_fma_f32 v[160:161], v[160:161], s[4:5], v[40:41] op_sel_hi:[1,0,1]
	v_mfma_f32_32x32x16_f16 v[64:79], v[176:179], v[116:119], v[64:79]
	s_waitcnt lgkmcnt(1)
	v_mfma_f32_32x32x16_f16 v[80:95], v[16:19], v[120:123], v[80:95]
	v_add_f32_e64 v16, v160, v20
	v_add_f32_e64 v17, v161, v21
	v_add_f32_e64 v18, v22, v38
	v_add_f32_e64 v19, v23, v39
	v_cvt_pk_f16_f32 v130, v16, v17
	v_pk_fma_f32 v[16:17], v[158:159], s[4:5], v[36:37] op_sel_hi:[1,0,1]
	s_nop 0
	v_pk_add_f32 v[36:37], v[16:17], v[18:19]
	v_mfma_f32_32x32x16_f16 v[96:111], v[44:47], v[120:123], v[96:111]
	ds_read_b128 v[40:43], v166 offset:52288
	ds_read_b128 v[44:47], v166 offset:43616
	ds_read_b128 v[16:19], v166 offset:60992
	ds_read_b128 v[20:23], v166 offset:52320
	v_cvt_pk_f16_f32 v131, v36, v37
	ds_read_b128 v[36:39], v166 offset:61024
	s_waitcnt lgkmcnt(4)
	v_mfma_f32_32x32x16_f16 v[64:79], v[40:43], v[120:123], v[64:79]
	v_cvt_f32_f16_sdwa v43, v132 dst_sel:DWORD dst_unused:UNUSED_PAD src0_sel:WORD_1
	v_cvt_f32_f16_e32 v42, v132
	v_or_b32_e32 v132, 0x23b40, v165
	v_cvt_f32_f16_sdwa v41, v156 dst_sel:DWORD dst_unused:UNUSED_PAD src0_sel:WORD_1
	v_cvt_f32_f16_e32 v40, v156
	v_cvt_f32_f16_e32 v156, v133
	v_pk_fma_f32 v[40:41], v[42:43], s[4:5], v[40:41] op_sel_hi:[1,0,1]
	s_waitcnt lgkmcnt(2)
	v_mfma_f32_32x32x16_f16 v[48:63], v[16:19], v[120:123], v[48:63]
	ds_read_b128 v[16:19], v132
	v_cvt_f32_f16_sdwa v43, v157 dst_sel:DWORD dst_unused:UNUSED_PAD src0_sel:WORD_1
	v_cvt_f32_f16_e32 v42, v157
	v_cvt_f32_f16_sdwa v157, v133 dst_sel:DWORD dst_unused:UNUSED_PAD src0_sel:WORD_1
	v_or_b32_e32 v132, 0x23b60, v165
	s_waitcnt lgkmcnt(0)
	v_pk_add_f32 v[16:17], v[24:25], v[16:17]
	v_cvt_f32_f16_sdwa v25, v154 dst_sel:DWORD dst_unused:UNUSED_PAD src0_sel:WORD_1
	v_mfma_f32_32x32x16_f16 v[96:111], v[32:35], v[124:127], v[96:111]
	ds_read_b128 v[32:35], v132
	v_add_f32_e64 v16, v40, v16
	v_add_f32_e64 v17, v41, v17
	v_cvt_f32_f16_e32 v24, v154
	v_cvt_f32_f16_sdwa v41, v134 dst_sel:DWORD dst_unused:UNUSED_PAD src0_sel:WORD_1
	v_cvt_f32_f16_e32 v40, v134
	v_cvt_pk_f16_f32 v132, v16, v17
	v_pk_fma_f32 v[16:17], v[156:157], s[4:5], v[42:43] op_sel_hi:[1,0,1]
	v_pk_add_f32 v[18:19], v[26:27], v[18:19]
	v_mfma_f32_32x32x16_f16 v[80:95], v[44:47], v[124:127], v[80:95]
	v_add_f32_e64 v16, v16, v18
	v_add_f32_e64 v17, v17, v19
	s_waitcnt lgkmcnt(0)
	v_add_f32_e64 v18, v28, v32
	v_add_f32_e64 v19, v29, v33
	v_cvt_pk_f16_f32 v133, v16, v17
	v_pk_fma_f32 v[16:17], v[40:41], s[4:5], v[24:25] op_sel_hi:[1,0,1]
	v_pk_add_f32 v[30:31], v[30:31], v[34:35]
	v_pk_add_f32 v[16:17], v[16:17], v[18:19]
	v_cvt_f32_f16_sdwa v33, v152 dst_sel:DWORD dst_unused:UNUSED_PAD src0_sel:WORD_1
	v_cvt_pk_f16_f32 v134, v16, v17
	ds_read_b128 v[16:19], v166 offset:34944
	v_mfma_f32_32x32x16_f16 v[64:79], v[20:23], v[124:127], v[64:79]
	v_cvt_f32_f16_sdwa v21, v155 dst_sel:DWORD dst_unused:UNUSED_PAD src0_sel:WORD_1
	v_cvt_f32_f16_e32 v20, v155
	v_cvt_f32_f16_sdwa v23, v135 dst_sel:DWORD dst_unused:UNUSED_PAD src0_sel:WORD_1
	v_cvt_f32_f16_e32 v22, v135
	v_cvt_f32_f16_e32 v32, v152
	v_cvt_f32_f16_sdwa v35, v136 dst_sel:DWORD dst_unused:UNUSED_PAD src0_sel:WORD_1
	v_cvt_f32_f16_e32 v34, v136
	v_pk_fma_f32 v[28:29], v[22:23], s[4:5], v[20:21] op_sel_hi:[1,0,1]
	ds_read_b128 v[20:23], v166 offset:43648
	ds_read_b128 v[24:27], v166 offset:34976
	s_waitcnt lgkmcnt(2)
	v_mfma_f32_32x32x16_f16 v[96:111], v[16:19], v[128:131], v[96:111]
	v_add_f32_e64 v16, v28, v30
	v_add_f32_e64 v17, v29, v31
	v_fma_f32 v40, v34, s4, v32
	v_fma_f32 v41, v35, s4, v33
	v_cvt_pk_f16_f32 v135, v16, v17
	ds_read_b128 v[16:19], v166 offset:52352
	ds_read_b128 v[28:31], v166 offset:43680
	v_cvt_f32_f16_sdwa v43, v153 dst_sel:DWORD dst_unused:UNUSED_PAD src0_sel:WORD_1
	v_cvt_f32_f16_e32 v42, v153
	v_cvt_f32_f16_sdwa v45, v137 dst_sel:DWORD dst_unused:UNUSED_PAD src0_sel:WORD_1
	v_mfma_f32_32x32x16_f16 v[48:63], v[36:39], v[124:127], v[48:63]
	v_or_b32_e32 v36, 0x23b80, v165
	v_cvt_f32_f16_e32 v44, v137
	s_waitcnt lgkmcnt(3)
	v_mfma_f32_32x32x16_f16 v[80:95], v[20:23], v[128:131], v[80:95]
	ds_read_b128 v[20:23], v36
	ds_read_b128 v[32:35], v166 offset:61056
	ds_read_b128 v[36:39], v166 offset:52384
	s_waitcnt lgkmcnt(2)
	v_add_f32_e64 v0, v0, v20
	v_add_f32_e64 v1, v1, v21
	v_pk_add_f32 v[0:1], v[40:41], v[0:1]
	v_mfma_f32_32x32x16_f16 v[64:79], v[16:19], v[128:131], v[64:79]
	v_or_b32_e32 v16, 0x23ba0, v165
	ds_read_b128 v[16:19], v16
	v_add_f32_e64 v2, v2, v22
	v_add_f32_e64 v3, v3, v23
	v_cvt_f32_f16_sdwa v21, v150 dst_sel:DWORD dst_unused:UNUSED_PAD src0_sel:WORD_1
	v_cvt_f32_f16_e32 v20, v150
	v_cvt_f32_f16_sdwa v23, v138 dst_sel:DWORD dst_unused:UNUSED_PAD src0_sel:WORD_1
	v_cvt_f32_f16_e32 v22, v138
	v_cvt_pk_f16_f32 v136, v0, v1
	v_pk_fma_f32 v[0:1], v[44:45], s[4:5], v[42:43] op_sel_hi:[1,0,1]
	ds_read_b128 v[40:43], v166 offset:61088
	v_pk_add_f32 v[0:1], v[0:1], v[2:3]
	s_waitcnt lgkmcnt(1)
	v_pk_add_f32 v[2:3], v[4:5], v[16:17]
	v_cvt_f32_f16_sdwa v5, v151 dst_sel:DWORD dst_unused:UNUSED_PAD src0_sel:WORD_1
	v_cvt_f32_f16_e32 v4, v151
	v_cvt_f32_f16_sdwa v17, v139 dst_sel:DWORD dst_unused:UNUSED_PAD src0_sel:WORD_1
	v_cvt_f32_f16_e32 v16, v139
	v_cvt_pk_f16_f32 v137, v0, v1
	v_pk_fma_f32 v[0:1], v[22:23], s[4:5], v[20:21] op_sel_hi:[1,0,1]
	v_mfma_f32_32x32x16_f16 v[48:63], v[32:35], v[128:131], v[48:63]
	v_add_f32_e64 v0, v0, v2
	v_add_f32_e64 v1, v1, v3
	v_add_f32_e64 v2, v6, v18
	v_add_f32_e64 v3, v7, v19
	v_cvt_pk_f16_f32 v138, v0, v1
	v_pk_fma_f32 v[0:1], v[16:17], s[4:5], v[4:5] op_sel_hi:[1,0,1]
	v_cvt_f32_f16_sdwa v5, v148 dst_sel:DWORD dst_unused:UNUSED_PAD src0_sel:WORD_1
	v_pk_add_f32 v[0:1], v[0:1], v[2:3]
	v_cvt_f32_f16_e32 v4, v148
	v_cvt_pk_f16_f32 v139, v0, v1
	ds_read_b128 v[0:3], v166 offset:35008
	v_mfma_f32_32x32x16_f16 v[96:111], v[24:27], v[132:135], v[96:111]
	v_cvt_f32_f16_sdwa v7, v140 dst_sel:DWORD dst_unused:UNUSED_PAD src0_sel:WORD_1
	v_cvt_f32_f16_e32 v6, v140
	v_or_b32_e32 v16, 0x23bc0, v165
	v_or_b32_e32 v17, 0x23be0, v165
	v_cvt_f32_f16_sdwa v33, v141 dst_sel:DWORD dst_unused:UNUSED_PAD src0_sel:WORD_1
	v_cvt_f32_f16_e32 v32, v141
	v_mfma_f32_32x32x16_f16 v[80:95], v[28:31], v[132:135], v[80:95]
	v_fma_f32 v28, v6, s4, v4
	v_fma_f32 v29, v7, s4, v5
	v_cvt_f32_f16_sdwa v31, v149 dst_sel:DWORD dst_unused:UNUSED_PAD src0_sel:WORD_1
	v_cvt_f32_f16_e32 v30, v149
	ds_read_b128 v[4:7], v16
	ds_read_b128 v[16:19], v17
	ds_read_b128 v[20:23], v166 offset:43712
	ds_read_b128 v[24:27], v166 offset:35040
	s_waitcnt lgkmcnt(3)
	v_pk_add_f32 v[10:11], v[10:11], v[6:7]
	v_mfma_f32_32x32x16_f16 v[64:79], v[36:39], v[132:135], v[64:79]
	v_mfma_f32_32x32x16_f16 v[48:63], v[40:43], v[132:135], v[48:63]
	v_mfma_f32_32x32x16_f16 v[96:111], v[0:3], v[136:139], v[96:111]
	v_add_f32_e64 v0, v8, v4
	v_add_f32_e64 v1, v9, v5
	v_fma_f32 v8, v32, s4, v30
	v_fma_f32 v9, v33, s4, v31
	v_add_f32_e64 v0, v28, v0
	v_add_f32_e64 v1, v29, v1
	v_pk_add_f32 v[28:29], v[8:9], v[10:11]
	v_cvt_pk_f16_f32 v140, v0, v1
	ds_read_b128 v[0:3], v166 offset:52416
	ds_read_b128 v[4:7], v166 offset:43744
	v_cvt_f32_f16_sdwa v31, v146 dst_sel:DWORD dst_unused:UNUSED_PAD src0_sel:WORD_1
	s_waitcnt lgkmcnt(3)
	v_mfma_f32_32x32x16_f16 v[80:95], v[20:23], v[136:139], v[80:95]
	ds_read_b128 v[8:11], v166 offset:61120
	ds_read_b128 v[20:23], v166 offset:52448
	v_cvt_f32_f16_e32 v30, v146
	v_cvt_f32_f16_sdwa v33, v142 dst_sel:DWORD dst_unused:UNUSED_PAD src0_sel:WORD_1
	v_cvt_f32_f16_e32 v32, v142
	v_cvt_pk_f16_f32 v141, v28, v29
	v_lshlrev_b32_e32 v146, 2, v164
	v_pk_fma_f32 v[28:29], v[32:33], s[4:5], v[30:31] op_sel_hi:[1,0,1]
	s_waitcnt lgkmcnt(3)
	v_mfma_f32_32x32x16_f16 v[64:79], v[0:3], v[136:139], v[64:79]
	ds_read_b128 v[0:3], v166 offset:61152
	v_cvt_f32_f16_sdwa v31, v147 dst_sel:DWORD dst_unused:UNUSED_PAD src0_sel:WORD_1
	v_cvt_f32_f16_e32 v30, v147
	v_cvt_f32_f16_sdwa v33, v143 dst_sel:DWORD dst_unused:UNUSED_PAD src0_sel:WORD_1
	v_cvt_f32_f16_e32 v32, v143
	v_lshlrev_b32_e32 v147, 2, v146
	s_waitcnt lgkmcnt(2)
	v_mfma_f32_32x32x16_f16 v[48:63], v[8:11], v[136:139], v[48:63]
	v_add_f32_e64 v8, v12, v16
	v_add_f32_e64 v9, v13, v17
	v_add_f32_e64 v10, v14, v18
	v_add_f32_e64 v11, v15, v19
	v_add_f32_e64 v8, v28, v8
	v_add_f32_e64 v9, v29, v9
	v_cvt_pk_f16_f32 v142, v8, v9
	v_pk_fma_f32 v[8:9], v[32:33], s[4:5], v[30:31] op_sel_hi:[1,0,1]
	s_load_dwordx4 s[4:7], s[0:1], 0x1f0
	v_pk_add_f32 v[8:9], v[8:9], v[10:11]
	s_nop 0
	v_cvt_pk_f16_f32 v143, v8, v9
	s_nop 1
	v_mfma_f32_32x32x16_f16 v[96:111], v[24:27], v[140:143], v[96:111]
	v_mfma_f32_32x32x16_f16 v[80:95], v[4:7], v[140:143], v[80:95]
	v_mul_u32_u24_e32 v4, 0x110, v145
	v_ashrrev_i32_e32 v145, 31, v144
	s_waitcnt lgkmcnt(0)
	v_mfma_f32_32x32x16_f16 v[64:79], v[20:23], v[140:143], v[64:79]
	v_mfma_f32_32x32x16_f16 v[48:63], v[0:3], v[140:143], v[48:63]
	s_and_saveexec_b64 s[0:1], s[8:9]
	s_cbranch_execz .LBB12_28
	v_or_b32_e32 v0, 0x23600, v147
	ds_read_b128 v[6:9], v0
	v_or_b32_e32 v2, 0x23620, v147
	ds_read_b128 v[10:13], v2
	v_lshlrev_b64 v[0:1], 5, v[144:145]
	v_lshl_add_u64 v[0:1], s[4:5], 0, v[0:1]
	s_waitcnt lgkmcnt(1)
	v_pk_add_f32 v[2:3], v[96:97], v[6:7]
	s_lshl_b64 s[4:5], s[36:37], 20
	v_cvt_pk_f16_f32 v6, v2, v3
	v_pk_add_f32 v[2:3], v[98:99], v[8:9]
	v_lshl_add_u64 v[8:9], v[0:1], 0, s[4:5]
	v_cvt_pk_f16_f32 v7, v2, v3
	v_lshlrev_b32_e32 v2, 1, v146
	v_mov_b32_e32 v3, 0
	v_lshl_add_u64 v[14:15], v[8:9], 0, v[2:3]
	global_store_dwordx2 v[14:15], v[6:7], off
	s_waitcnt lgkmcnt(0)
	v_pk_add_f32 v[6:7], v[100:101], v[10:11]
	v_or_b32_e32 v5, 0x23640, v147
	v_cvt_pk_f16_f32 v10, v6, v7
	ds_read_b128 v[6:9], v5
	v_pk_add_f32 v[12:13], v[102:103], v[12:13]
	v_or_b32_e32 v5, 0x23660, v147
	v_cvt_pk_f16_f32 v11, v12, v13
	global_store_dwordx2 v[14:15], v[10:11], off offset:16
	ds_read_b128 v[10:13], v5
	s_waitcnt lgkmcnt(1)
	v_pk_add_f32 v[6:7], v[104:105], v[6:7]
	v_pk_add_f32 v[8:9], v[106:107], v[8:9]
	s_lshl_b64 s[4:5], s[34:35], 20
	v_cvt_pk_f16_f32 v6, v6, v7
	v_cvt_pk_f16_f32 v7, v8, v9
	v_lshl_add_u64 v[8:9], v[0:1], 0, s[4:5]
	v_lshl_add_u64 v[14:15], v[8:9], 0, v[2:3]
	global_store_dwordx2 v[14:15], v[6:7], off
	s_waitcnt lgkmcnt(0)
	v_pk_add_f32 v[6:7], v[108:109], v[10:11]
	v_or_b32_e32 v5, 0x23680, v147
	v_cvt_pk_f16_f32 v10, v6, v7
	ds_read_b128 v[6:9], v5
	v_pk_add_f32 v[12:13], v[110:111], v[12:13]
	v_or_b32_e32 v5, 0x236a0, v147
	v_cvt_pk_f16_f32 v11, v12, v13
	global_store_dwordx2 v[14:15], v[10:11], off offset:16
	ds_read_b128 v[10:13], v5
	s_waitcnt lgkmcnt(1)
	v_pk_add_f32 v[6:7], v[80:81], v[6:7]
	v_pk_add_f32 v[8:9], v[82:83], v[8:9]
	s_lshl_b64 s[4:5], s[30:31], 20
	v_cvt_pk_f16_f32 v6, v6, v7
	v_cvt_pk_f16_f32 v7, v8, v9
	v_lshl_add_u64 v[8:9], v[0:1], 0, s[4:5]
	v_lshl_add_u64 v[14:15], v[8:9], 0, v[2:3]
	global_store_dwordx2 v[14:15], v[6:7], off
	s_waitcnt lgkmcnt(0)
	v_pk_add_f32 v[6:7], v[84:85], v[10:11]
	v_or_b32_e32 v5, 0x236c0, v147
	v_cvt_pk_f16_f32 v10, v6, v7
	ds_read_b128 v[6:9], v5
	v_pk_add_f32 v[12:13], v[86:87], v[12:13]
	v_or_b32_e32 v5, 0x236e0, v147
	v_cvt_pk_f16_f32 v11, v12, v13
	global_store_dwordx2 v[14:15], v[10:11], off offset:16
	ds_read_b128 v[10:13], v5
	s_waitcnt lgkmcnt(1)
	v_pk_add_f32 v[6:7], v[88:89], v[6:7]
	v_pk_add_f32 v[8:9], v[90:91], v[8:9]
	s_lshl_b64 s[4:5], s[28:29], 20
	v_cvt_pk_f16_f32 v6, v6, v7
	v_cvt_pk_f16_f32 v7, v8, v9
	v_lshl_add_u64 v[8:9], v[0:1], 0, s[4:5]
	v_lshl_add_u64 v[14:15], v[8:9], 0, v[2:3]
	global_store_dwordx2 v[14:15], v[6:7], off
	s_waitcnt lgkmcnt(0)
	v_pk_add_f32 v[6:7], v[92:93], v[10:11]
	v_or_b32_e32 v5, 0x23700, v147
	v_cvt_pk_f16_f32 v10, v6, v7
	ds_read_b128 v[6:9], v5
	v_pk_add_f32 v[12:13], v[94:95], v[12:13]
	v_or_b32_e32 v5, 0x23720, v147
	v_cvt_pk_f16_f32 v11, v12, v13
	global_store_dwordx2 v[14:15], v[10:11], off offset:16
	ds_read_b128 v[10:13], v5
	s_waitcnt lgkmcnt(1)
	v_pk_add_f32 v[6:7], v[64:65], v[6:7]
	v_pk_add_f32 v[8:9], v[66:67], v[8:9]
	s_lshl_b64 s[4:5], s[26:27], 20
	v_cvt_pk_f16_f32 v6, v6, v7
	v_cvt_pk_f16_f32 v7, v8, v9
	v_lshl_add_u64 v[8:9], v[0:1], 0, s[4:5]
	v_lshl_add_u64 v[14:15], v[8:9], 0, v[2:3]
	global_store_dwordx2 v[14:15], v[6:7], off
	s_waitcnt lgkmcnt(0)
	v_pk_add_f32 v[6:7], v[68:69], v[10:11]
	v_or_b32_e32 v5, 0x23740, v147
	v_cvt_pk_f16_f32 v10, v6, v7
	ds_read_b128 v[6:9], v5
	v_pk_add_f32 v[12:13], v[70:71], v[12:13]
	v_or_b32_e32 v5, 0x23760, v147
	v_cvt_pk_f16_f32 v11, v12, v13
	global_store_dwordx2 v[14:15], v[10:11], off offset:16
	ds_read_b128 v[10:13], v5
	s_waitcnt lgkmcnt(1)
	v_pk_add_f32 v[6:7], v[72:73], v[6:7]
	v_pk_add_f32 v[8:9], v[74:75], v[8:9]
	s_lshl_b64 s[4:5], s[24:25], 20
	v_cvt_pk_f16_f32 v6, v6, v7
	v_cvt_pk_f16_f32 v7, v8, v9
	v_lshl_add_u64 v[8:9], v[0:1], 0, s[4:5]
	v_lshl_add_u64 v[14:15], v[8:9], 0, v[2:3]
	global_store_dwordx2 v[14:15], v[6:7], off
	s_waitcnt lgkmcnt(0)
	v_pk_add_f32 v[6:7], v[76:77], v[10:11]
	v_or_b32_e32 v5, 0x23780, v147
	v_cvt_pk_f16_f32 v10, v6, v7
	ds_read_b128 v[6:9], v5
	v_pk_add_f32 v[12:13], v[78:79], v[12:13]
	v_or_b32_e32 v5, 0x237a0, v147
	v_cvt_pk_f16_f32 v11, v12, v13
	global_store_dwordx2 v[14:15], v[10:11], off offset:16
	ds_read_b128 v[10:13], v5
	s_waitcnt lgkmcnt(1)
	v_pk_add_f32 v[6:7], v[48:49], v[6:7]
	v_pk_add_f32 v[8:9], v[50:51], v[8:9]
	s_lshl_b64 s[4:5], s[10:11], 20
	v_cvt_pk_f16_f32 v6, v6, v7
	v_cvt_pk_f16_f32 v7, v8, v9
	v_lshl_add_u64 v[8:9], v[0:1], 0, s[4:5]
	v_lshl_add_u64 v[14:15], v[8:9], 0, v[2:3]
	global_store_dwordx2 v[14:15], v[6:7], off
	s_waitcnt lgkmcnt(0)
	v_pk_add_f32 v[6:7], v[52:53], v[10:11]
	v_or_b32_e32 v5, 0x237c0, v147
	v_cvt_pk_f16_f32 v10, v6, v7
	v_pk_add_f32 v[12:13], v[54:55], v[12:13]
	ds_read_b128 v[6:9], v5
	v_cvt_pk_f16_f32 v11, v12, v13
	v_or_b32_e32 v5, 0x237e0, v147
	global_store_dwordx2 v[14:15], v[10:11], off offset:16
	ds_read_b128 v[10:13], v5
	s_lshl_b64 s[4:5], s[2:3], 20
	s_waitcnt lgkmcnt(1)
	v_pk_add_f32 v[6:7], v[56:57], v[6:7]
	v_pk_add_f32 v[8:9], v[58:59], v[8:9]
	v_lshl_add_u64 v[0:1], v[0:1], 0, s[4:5]
	v_cvt_pk_f16_f32 v6, v6, v7
	v_cvt_pk_f16_f32 v7, v8, v9
	v_lshl_add_u64 v[0:1], v[0:1], 0, v[2:3]
	global_store_dwordx2 v[0:1], v[6:7], off
	s_waitcnt lgkmcnt(0)
	v_pk_add_f32 v[2:3], v[60:61], v[10:11]
	v_pk_add_f32 v[6:7], v[62:63], v[12:13]
	v_cvt_pk_f16_f32 v2, v2, v3
	v_cvt_pk_f16_f32 v3, v6, v7
	global_store_dwordx2 v[0:1], v[2:3], off offset:16

amdhsa.kernels:
  - .agpr_count:     0
    .args:
      - .actual_access:  read_only
        .address_space:  global
        .offset:         0
        .size:           8
        .value_kind:     global_buffer
      - .actual_access:  write_only
        .address_space:  global
        .offset:         8
        .size:           8
        .value_kind:     global_buffer
    .group_segment_fixed_size: 0
    .kernarg_segment_align: 8
    .kernarg_segment_size: 16
    .language:       OpenCL C
    .language_version:
      - 2
      - 0
    .max_flat_workgroup_size: 256
    .name:           _Z13prep_x_kernelPKfP15HIP_vector_typeIjLj4EE
    .private_segment_fixed_size: 0
    .sgpr_count:     23
    .sgpr_spill_count: 0
    .symbol:         _Z13prep_x_kernelPKfP15HIP_vector_typeIjLj4EE.kd
    .uniform_work_group_size: 1
    .uses_dynamic_stack: false
    .vgpr_count:     36
    .vgpr_spill_count: 0
    .wavefront_size: 64
  - .agpr_count:     0
    .args:
      - .actual_access:  read_only
        .address_space:  global
        .offset:         0
        .size:           8
        .value_kind:     global_buffer
      - .actual_access:  write_only
        .address_space:  global
        .offset:         8
        .size:           8
        .value_kind:     global_buffer
      - .offset:         16
        .size:           4
        .value_kind:     by_value
      - .offset:         20
        .size:           4
        .value_kind:     by_value
      - .offset:         24
        .size:           4
        .value_kind:     by_value
      - .offset:         28
        .size:           4
        .value_kind:     by_value
    .group_segment_fixed_size: 0
    .kernarg_segment_align: 8
    .kernarg_segment_size: 32
    .language:       OpenCL C
    .language_version:
      - 2
      - 0
    .max_flat_workgroup_size: 256
    .name:           _Z13prep_w_kernelPKfP15HIP_vector_typeIjLj4EEiiii
    .private_segment_fixed_size: 0
    .sgpr_count:     15
    .sgpr_spill_count: 0
    .symbol:         _Z13prep_w_kernelPKfP15HIP_vector_typeIjLj4EEiiii.kd
    .uniform_work_group_size: 1
    .uses_dynamic_stack: false
    .vgpr_count:     34
    .vgpr_spill_count: 0
    .wavefront_size: 64
  - .agpr_count:     0
    .args:
      - .actual_access:  write_only
        .address_space:  global
        .offset:         0
        .size:           8
        .value_kind:     global_buffer
    .group_segment_fixed_size: 0
    .kernarg_segment_align: 8
    .kernarg_segment_size: 8
    .language:       OpenCL C
    .language_version:
      - 2
      - 0
    .max_flat_workgroup_size: 256
    .name:           _Z18zero_border_kernelP15HIP_vector_typeIjLj4EE
    .private_segment_fixed_size: 0
    .sgpr_count:     12
    .sgpr_spill_count: 0
    .symbol:         _Z18zero_border_kernelP15HIP_vector_typeIjLj4EE.kd
    .uniform_work_group_size: 1
    .uses_dynamic_stack: false
    .vgpr_count:     6
    .vgpr_spill_count: 0
    .wavefront_size: 64
  - .agpr_count:     0
    .args:
      - .actual_access:  read_only
        .address_space:  global
        .offset:         0
        .size:           8
        .value_kind:     global_buffer
      - .address_space:  global
        .offset:         8
        .size:           8
        .value_kind:     global_buffer
      - .actual_access:  read_only
        .address_space:  global
        .offset:         16
        .size:           8
        .value_kind:     global_buffer
      - .actual_access:  read_only
        .address_space:  global
        .offset:         24
        .size:           8
        .value_kind:     global_buffer
      - .actual_access:  read_only
        .address_space:  global
        .offset:         32
        .size:           8
        .value_kind:     global_buffer
      - .actual_access:  write_only
        .address_space:  global
        .offset:         40
        .size:           8
        .value_kind:     global_buffer
    .group_segment_fixed_size: 154880
    .kernarg_segment_align: 8
    .kernarg_segment_size: 48
    .language:       OpenCL C
    .language_version:
      - 2
      - 0
    .max_flat_workgroup_size: 512
    .name:           _Z12conv1_kernelPKfPK15HIP_vector_typeIjLj4EES0_S0_S0_PDF16_
    .private_segment_fixed_size: 0
    .sgpr_count:     46
    .sgpr_spill_count: 0
    .symbol:         _Z12conv1_kernelPKfPK15HIP_vector_typeIjLj4EES0_S0_S0_PDF16_.kd
    .uniform_work_group_size: 1
    .uses_dynamic_stack: false
    .vgpr_count:     256
    .vgpr_spill_count: 0
    .wavefront_size: 64
  - .agpr_count:     0
    .args:
      - .actual_access:  read_only
        .address_space:  global
        .offset:         0
        .size:           8
        .value_kind:     global_buffer
      - .actual_access:  read_only
        .address_space:  global
        .offset:         8
        .size:           8
        .value_kind:     global_buffer
      - .actual_access:  read_only
        .address_space:  global
        .offset:         16
        .size:           8
        .value_kind:     global_buffer
      - .actual_access:  write_only
        .address_space:  global
        .offset:         24
        .size:           8
        .value_kind:     global_buffer
      - .actual_access:  write_only
        .address_space:  global
        .offset:         32
        .size:           8
        .value_kind:     global_buffer
    .group_segment_fixed_size: 116480
    .kernarg_segment_align: 8
    .kernarg_segment_size: 40
    .language:       OpenCL C
    .language_version:
      - 2
      - 0
    .max_flat_workgroup_size: 512
    .name:           _Z12conv3_kernelPK15HIP_vector_typeIjLj4EES2_PKfPfS5_
    .private_segment_fixed_size: 0
    .sgpr_count:     22
    .sgpr_spill_count: 0
    .symbol:         _Z12conv3_kernelPK15HIP_vector_typeIjLj4EES2_PKfPfS5_.kd
    .uniform_work_group_size: 1
    .uses_dynamic_stack: false
    .vgpr_count:     122
    .vgpr_spill_count: 0
    .wavefront_size: 64
  - .agpr_count:     0
    .args:
      - .actual_access:  read_only
        .address_space:  global
        .offset:         0
        .size:           8
        .value_kind:     global_buffer
      - .actual_access:  read_only
        .address_space:  global
        .offset:         8
        .size:           8
        .value_kind:     global_buffer
      - .actual_access:  write_only
        .address_space:  global
        .offset:         16
        .size:           8
        .value_kind:     global_buffer
      - .address_space:  global
        .offset:         24
        .size:           8
        .value_kind:     global_buffer
    .group_segment_fixed_size: 32768
    .kernarg_segment_align: 8
    .kernarg_segment_size: 32
    .language:       OpenCL C
    .language_version:
      - 2
      - 0
    .max_flat_workgroup_size: 256
    .name:           _Z15nms_hist_kernelPKfS0_PjS1_
    .private_segment_fixed_size: 0
    .sgpr_count:     102
    .sgpr_spill_count: 0
    .symbol:         _Z15nms_hist_kernelPKfS0_PjS1_.kd
    .uniform_work_group_size: 1
    .uses_dynamic_stack: false
    .vgpr_count:     128
    .vgpr_spill_count: 0
    .wavefront_size: 64
  - .agpr_count:     0
    .args:
      - .actual_access:  read_only
        .address_space:  global
        .offset:         0
        .size:           8
        .value_kind:     global_buffer
      - .actual_access:  write_only
        .address_space:  global
        .offset:         8
        .size:           8
        .value_kind:     global_buffer
    .group_segment_fixed_size: 4096
    .kernarg_segment_align: 8
    .kernarg_segment_size: 16
    .language:       OpenCL C
    .language_version:
      - 2
      - 0
    .max_flat_workgroup_size: 1024
    .name:           _Z17select_bin_kernelPKjPi
    .private_segment_fixed_size: 0
    .sgpr_count:     23
    .sgpr_spill_count: 0
    .symbol:         _Z17select_bin_kernelPKjPi.kd
    .uniform_work_group_size: 1
    .uses_dynamic_stack: false
    .vgpr_count:     13
    .vgpr_spill_count: 0
    .wavefront_size: 64
  - .agpr_count:     0
    .args:
      - .actual_access:  read_only
        .address_space:  global
        .offset:         0
        .size:           8
        .value_kind:     global_buffer
      - .actual_access:  read_only
        .address_space:  global
        .offset:         8
        .size:           8
        .value_kind:     global_buffer
      - .address_space:  global
        .offset:         16
        .size:           8
        .value_kind:     global_buffer
      - .actual_access:  write_only
        .address_space:  global
        .offset:         24
        .size:           8
        .value_kind:     global_buffer
    .group_segment_fixed_size: 2052
    .kernarg_segment_align: 8
    .kernarg_segment_size: 32
    .language:       OpenCL C
    .language_version:
      - 2
      - 0
    .max_flat_workgroup_size: 512
    .name:           _Z14collect_kernelPKjS0_PiS1_
    .private_segment_fixed_size: 0
    .sgpr_count:     54
    .sgpr_spill_count: 0
    .symbol:         _Z14collect_kernelPKjS0_PiS1_.kd
    .uniform_work_group_size: 1
    .uses_dynamic_stack: false
    .vgpr_count:     34
    .vgpr_spill_count: 0
    .wavefront_size: 64
  - .agpr_count:     0
    .args:
      - .actual_access:  read_only
        .address_space:  global
        .offset:         0
        .size:           8
        .value_kind:     global_buffer
      - .actual_access:  read_only
        .address_space:  global
        .offset:         8
        .size:           8
        .value_kind:     global_buffer
      - .actual_access:  read_only
        .address_space:  global
        .offset:         16
        .size:           8
        .value_kind:     global_buffer
      - .actual_access:  read_only
        .address_space:  global
        .offset:         24
        .size:           8
        .value_kind:     global_buffer
      - .actual_access:  write_only
        .address_space:  global
        .offset:         32
        .size:           8
        .value_kind:     global_buffer
    .group_segment_fixed_size: 49664
    .kernarg_segment_align: 8
    .kernarg_segment_size: 40
    .language:       OpenCL C
    .language_version:
      - 2
      - 0
    .max_flat_workgroup_size: 1024
    .name:           _Z11rank_kernelPKfS0_PKiS2_Pi
    .private_segment_fixed_size: 0
    .sgpr_count:     23
    .sgpr_spill_count: 0
    .symbol:         _Z11rank_kernelPKfS0_PKiS2_Pi.kd
    .uniform_work_group_size: 1
    .uses_dynamic_stack: false
    .vgpr_count:     12
    .vgpr_spill_count: 0
    .wavefront_size: 64
  - .agpr_count:     0
    .args:
      - .actual_access:  read_only
        .address_space:  global
        .offset:         0
        .size:           8
        .value_kind:     global_buffer
      - .actual_access:  read_only
        .address_space:  global
        .offset:         8
        .size:           8
        .value_kind:     global_buffer
      - .actual_access:  write_only
        .address_space:  global
        .offset:         16
        .size:           8
        .value_kind:     global_buffer
      - .actual_access:  write_only
        .address_space:  global
        .offset:         24
        .size:           8
        .value_kind:     global_buffer
    .group_segment_fixed_size: 0
    .kernarg_segment_align: 8
    .kernarg_segment_size: 32
    .language:       OpenCL C
    .language_version:
      - 2
      - 0
    .max_flat_workgroup_size: 256
    .name:           _Z15prep_kvw_kernelPKfS0_PDF16_S1_
    .private_segment_fixed_size: 0
    .sgpr_count:     14
    .sgpr_spill_count: 0
    .symbol:         _Z15prep_kvw_kernelPKfS0_PDF16_S1_.kd
    .uniform_work_group_size: 1
    .uses_dynamic_stack: false
    .vgpr_count:     7
    .vgpr_spill_count: 0
    .wavefront_size: 64
  - .agpr_count:     0
    .args:
      - .actual_access:  read_only
        .address_space:  global
        .offset:         0
        .size:           8
        .value_kind:     global_buffer
      - .actual_access:  read_only
        .address_space:  global
        .offset:         8
        .size:           8
        .value_kind:     global_buffer
      - .actual_access:  read_only
        .address_space:  global
        .offset:         16
        .size:           8
        .value_kind:     global_buffer
      - .actual_access:  read_only
        .address_space:  global
        .offset:         24
        .size:           8
        .value_kind:     global_buffer
      - .actual_access:  write_only
        .address_space:  global
        .offset:         32
        .size:           8
        .value_kind:     global_buffer
    .group_segment_fixed_size: 67856
    .kernarg_segment_align: 8
    .kernarg_segment_size: 40
    .language:       OpenCL C
    .language_version:
      - 2
      - 0
    .max_flat_workgroup_size: 448
    .name:           _Z17cross_attn_kernelPKDF16_S0_S0_S0_Pf
    .private_segment_fixed_size: 0
    .sgpr_count:     26
    .sgpr_spill_count: 0
    .symbol:         _Z17cross_attn_kernelPKDF16_S0_S0_S0_Pf.kd
    .uniform_work_group_size: 1
    .uses_dynamic_stack: false
    .vgpr_count:     74
    .vgpr_spill_count: 0
    .wavefront_size: 64
  - .agpr_count:     0
    .args:
      - .offset:         0
        .size:           424
        .value_kind:     by_value
      - .offset:         424
        .size:           88
        .value_kind:     by_value
    .group_segment_fixed_size: 137216
    .kernarg_segment_align: 8
    .kernarg_segment_size: 512
    .language:       OpenCL C
    .language_version:
      - 2
      - 0
    .max_flat_workgroup_size: 512
    .name:           _Z12tailA_kernel5TailP3KvP
    .private_segment_fixed_size: 0
    .sgpr_count:     44
    .sgpr_spill_count: 0
    .symbol:         _Z12tailA_kernel5TailP3KvP.kd
    .uniform_work_group_size: 1
    .uses_dynamic_stack: false
    .vgpr_count:     200
    .vgpr_spill_count: 0
    .wavefront_size: 64
  - .agpr_count:     0
    .args:
      - .offset:         0
        .size:           424
        .value_kind:     by_value
      - .offset:         424
        .size:           88
        .value_kind:     by_value
    .group_segment_fixed_size: 146592
    .kernarg_segment_align: 8
    .kernarg_segment_size: 512
    .language:       OpenCL C
    .language_version:
      - 2
      - 0
    .max_flat_workgroup_size: 512
    .name:           _Z12tailB_kernel5TailP3KvP
    .private_segment_fixed_size: 0
    .sgpr_count:     44
    .sgpr_spill_count: 0
    .symbol:         _Z12tailB_kernel5TailP3KvP.kd
    .uniform_work_group_size: 1
    .uses_dynamic_stack: false
    .vgpr_count:     216
    .vgpr_spill_count: 0
    .wavefront_size: 64
  - .agpr_count:     0
    .args:
      - .offset:         0
        .size:           424
        .value_kind:     by_value
    .group_segment_fixed_size: 36896
    .kernarg_segment_align: 8
    .kernarg_segment_size: 424
    .language:       OpenCL C
    .language_version:
      - 2
      - 0
    .max_flat_workgroup_size: 512
    .name:           _Z12tailC_kernel5TailP
    .private_segment_fixed_size: 0
    .sgpr_count:     58
    .sgpr_spill_count: 0
    .symbol:         _Z12tailC_kernel5TailP.kd
    .uniform_work_group_size: 1
    .uses_dynamic_stack: false
    .vgpr_count:     113
    .vgpr_spill_count: 0
    .wavefront_size: 64
  - .agpr_count:     0
    .args:
      - .offset:         0
        .size:           344
        .value_kind:     by_value
    .group_segment_fixed_size: 0
    .kernarg_segment_align: 8
    .kernarg_segment_size: 344
    .language:       OpenCL C
    .language_version:
      - 2
      - 0
    .max_flat_workgroup_size: 256
    .name:           _Z15prep_all_kernel5PrepP
    .private_segment_fixed_size: 0
    .sgpr_count:     31
    .sgpr_spill_count: 0
    .symbol:         _Z15prep_all_kernel5PrepP.kd
    .uniform_work_group_size: 1
    .uses_dynamic_stack: false
    .vgpr_count:     39
    .vgpr_spill_count: 0
    .wavefront_size: 64
  - .agpr_count:     0
    .args:
      - .actual_access:  read_only
        .address_space:  global
        .offset:         0
        .size:           8
        .value_kind:     global_buffer
      - .actual_access:  read_only
        .address_space:  global
        .offset:         8
        .size:           8
        .value_kind:     global_buffer
      - .actual_access:  read_only
        .address_space:  global
        .offset:         16
        .size:           8
        .value_kind:     global_buffer
      - .actual_access:  read_only
        .address_space:  global
        .offset:         24
        .size:           8
        .value_kind:     global_buffer
      - .actual_access:  read_only
        .address_space:  global
        .offset:         32
        .size:           8
        .value_kind:     global_buffer
      - .actual_access:  write_only
        .address_space:  global
        .offset:         40
        .size:           8
        .value_kind:     global_buffer
      - .actual_access:  read_only
        .address_space:  global
        .offset:         48
        .size:           8
        .value_kind:     global_buffer
      - .actual_access:  read_only
        .address_space:  global
        .offset:         56
        .size:           8
        .value_kind:     global_buffer
    .group_segment_fixed_size: 130304
    .kernarg_segment_align: 8
    .kernarg_segment_size: 64
    .language:       OpenCL C
    .language_version:
      - 2
      - 0
    .max_flat_workgroup_size: 512
    .name:           _Z11conv_kernelILi8ELi128ELi0EEvPK15HIP_vector_typeIjLj4EES3_PKfS5_S5_PDF16_PfS7_
    .private_segment_fixed_size: 0
    .sgpr_count:     30
    .sgpr_spill_count: 0
    .symbol:         _Z11conv_kernelILi8ELi128ELi0EEvPK15HIP_vector_typeIjLj4EES3_PKfS5_S5_PDF16_PfS7_.kd
    .uniform_work_group_size: 1
    .uses_dynamic_stack: false
    .vgpr_count:     254
    .vgpr_spill_count: 0
    .wavefront_size: 64
